# MoE-up loop hand-rescheduled: 3 A LDS buffers, 4 B reg sets, counted vmcnt(21), gain via s_load
# speedup vs baseline: 1.0109x; 1.0109x over previous
; #define REP(k) for (int rep_ = 0; rep_ < ((PROBE_DUP) == (k) ? 2 : 1); ++rep_)
; #define LAS __attribute__((address_space(3)))
; #define MOE_OFFSETS() do { __syncthreads(); if (F.tid < 64) { const int c_ = (int)ctl[CW_CNT + F.tid]; int s_ = c_; _Pragma("unroll") for (int d_ = 1; d_ < 64; d_ <<= 1) { const int t_ = __shfl_up(s_, d_); if (F.lane >= d_) s_ += t_; } \
;         eo[F.tid + 1] = s_; ecnt[F.tid] = c_; if (F.tid == 0) eo[0] = 0; } __syncthreads(); } while (0)
; #define MOE_UNIT(idx_, x_, RMAX, CBN, e_, rb_, cb_, ok_) do { int b_ = 0; ok_ = false; for (int k_ = 0; k_ < 8; ++k_) { const int ee_ = (x_) + 8 * k_, n_ = ((ecnt[ee_] + (RMAX) - 1) / (RMAX)) * (CBN); \
;         if ((idx_) < b_ + n_) { e_ = ee_; rb_ = ((idx_) - b_) / (CBN); cb_ = ((idx_) - b_) % (CBN); ok_ = true; break; } b_ += n_; } } while (0)
; __global__ void __launch_bounds__(NTHREADS, 2) hymba_fwd(Args args) {
;     ...
;     if (IN(8)) REP(8) {
;         __syncthreads(); for (int i = F.tid; i < D / 4; i += NTHREADS) ((LAS f32x4*)(F.lds + mu::GAIN_OFF))[i] = ((const f32x4*)F.g_ffn)[i];
;         MOE_OFFSETS();
;         const int x = F.bid & 7;
;         for (int j = F.bid >> 3; ; j += F.G >> 3) { int e = 0, rb = 0, cb = 0; bool ok; MOE_UNIT(j, x, mu::MR, 8, e, rb, cb, ok); if (!ok) break;
.LBB0_676:
	global_load_dwordx4 v[6:9], v[2:3], off
	v_add_co_u32_e32 v4, vcc, 0x200, v4
	s_xor_b64 s[8:9], vcc, -1
	s_and_b64 s[8:9], exec, s[8:9]
	v_lshl_add_u64 v[2:3], v[2:3], 0, s[6:7]
	s_or_b64 s[4:5], s[8:9], s[4:5]
	s_waitcnt vmcnt(0)
	ds_write_b128 v5, v[6:9]
	v_add_u32_e32 v5, 0x2000, v5
	s_andn2_b64 exec, exec, s[4:5]
	s_cbranch_execnz .LBB0_676
	s_or_b64 exec, exec, s[4:5]
	v_cmp_gt_u32_e32 vcc, 64, v0
	v_cmp_gt_u32_e64 s[4:5], 32, v131
	s_waitcnt lgkmcnt(0)
	s_barrier
	s_and_saveexec_b64 s[6:7], vcc
	s_cbranch_execz .LBB0_680
	v_lshlrev_b32_e32 v2, 2, v0
	v_mov_b32_e32 v3, 0
	v_lshl_add_u64 v[4:5], s[26:27], 0, v[2:3]
	v_add_co_u32_e32 v4, vcc, 0x1000, v4
	s_add_i32 s3, 0, 0x26c00
	s_nop 0
	v_addc_co_u32_e32 v5, vcc, 0, v5, vcc
	global_load_dword v2, v[4:5], off
	v_mbcnt_lo_u32_b32 v4, -1, 0
	v_mbcnt_hi_u32_b32 v4, -1, v4
	v_and_b32_e32 v5, 64, v4
	v_add_u32_e32 v6, -1, v4
	v_cmp_lt_i32_e32 vcc, v6, v5
	v_add_u32_e32 v7, -2, v4
	v_add_u32_e32 v8, -4, v4
	v_cndmask_b32_e32 v6, v6, v4, vcc
	v_lshlrev_b32_e32 v6, 2, v6
	v_cmp_lt_i32_e32 vcc, v7, v5
	v_add_u32_e32 v9, -8, v4
	v_add_u32_e32 v10, -16, v4
	v_cndmask_b32_e32 v7, v7, v4, vcc
	v_cmp_ne_u32_e32 vcc, 0, v131
	v_lshlrev_b32_e32 v7, 2, v7
	v_subrev_u32_e32 v11, 32, v4
	v_readlane_b32 s8, v254, 5
	v_readlane_b32 s9, v254, 6
	s_waitcnt vmcnt(0)
	ds_bpermute_b32 v6, v6, v2
	s_waitcnt lgkmcnt(0)
	v_cndmask_b32_e32 v6, 0, v6, vcc
	v_add_u32_e32 v6, v6, v2
	ds_bpermute_b32 v7, v7, v6
	v_cmp_lt_i32_e32 vcc, v8, v5
	s_nop 1
	v_cndmask_b32_e32 v8, v8, v4, vcc
	v_cmp_lt_u32_e32 vcc, 1, v131
	v_lshlrev_b32_e32 v8, 2, v8
	s_waitcnt lgkmcnt(0)
	v_cndmask_b32_e32 v7, 0, v7, vcc
	v_add_u32_e32 v6, v7, v6
	ds_bpermute_b32 v7, v8, v6
	v_cmp_lt_i32_e32 vcc, v9, v5
	s_nop 1
	v_cndmask_b32_e32 v8, v9, v4, vcc
	v_cmp_lt_u32_e32 vcc, 3, v131
	v_lshlrev_b32_e32 v8, 2, v8
	s_waitcnt lgkmcnt(0)
	v_cndmask_b32_e32 v7, 0, v7, vcc
	v_add_u32_e32 v6, v7, v6
	ds_bpermute_b32 v7, v8, v6
	v_cmp_lt_i32_e32 vcc, v10, v5
	s_nop 1
	v_cndmask_b32_e32 v8, v10, v4, vcc
	v_cmp_lt_u32_e32 vcc, 7, v131
	v_lshlrev_b32_e32 v8, 2, v8
	s_waitcnt lgkmcnt(0)
	v_cndmask_b32_e32 v7, 0, v7, vcc
	v_add_u32_e32 v6, v7, v6
	ds_bpermute_b32 v7, v8, v6
	v_cmp_lt_i32_e32 vcc, v11, v5
	s_nop 1
	v_cndmask_b32_e32 v4, v11, v4, vcc
	v_cmp_lt_u32_e32 vcc, 15, v131
	v_lshlrev_b32_e32 v4, 2, v4
	s_waitcnt lgkmcnt(0)
	v_cndmask_b32_e32 v5, 0, v7, vcc
	v_add_u32_e32 v5, v5, v6
	ds_bpermute_b32 v4, v4, v5
	v_add_u32_e32 v6, 0, v84
	v_add_u32_e32 v7, s3, v84
	v_add_u32_e32 v6, 0x26d40, v6
	s_waitcnt lgkmcnt(0)
	v_cndmask_b32_e64 v4, v4, 0, s[4:5]
	v_add_u32_e32 v4, v4, v5
	ds_write_b32 v7, v4 offset:4
	ds_write_b32 v6, v2
	s_and_b64 exec, exec, s[8:9]
	v_mov_b32_e32 v2, s3
	ds_write_b32 v2, v3
.LBB0_680:
	s_or_b64 exec, exec, s[6:7]
	s_add_i32 s6, 0, 0x14000
	s_ashr_i32 s3, s2, 3
	s_add_u32 s8, s26, 0x49e00000
	s_addc_u32 s9, s27, 0
	s_add_u32 s10, s26, 0x4aa00000
	s_addc_u32 s11, s27, 0
	s_mov_b64 s[30:31], s[26:27]
	v_and_b32_e32 v4, 44, v0
	s_mov_b64 s[28:29], s[24:25]
	s_mov_b64 s[26:27], s[22:23]
	s_mov_b64 s[24:25], s[20:21]
	v_and_b32_e32 v2, 16, v154
	v_and_b32_e32 v3, 2, v169
	v_and_or_b32 v4, v84, 64, v4
	v_readlane_b32 s12, v254, 7
	v_or3_b32 v3, v4, v2, v3
	v_lshrrev_b32_e32 v2, 1, v0
	v_readlane_b32 s13, v254, 8
	v_readlane_b32 s14, v254, 9
	v_readlane_b32 s15, v254, 10
	v_readlane_b32 s24, v254, 19
	v_readlane_b32 s25, v254, 20
	v_bfe_u32 v4, v0, 1, 3
	v_bitop3_b32 v2, v171, v2, 7 bitop3:0x78
	v_readlane_b32 s26, v254, 21
	v_readlane_b32 s27, v254, 22
	s_mov_b64 s[12:13], s[24:25]
	v_lshlrev_b32_e32 v5, 4, v2
	v_bitop3_b32 v2, v171, v4, 4 bitop3:0x36
	s_mov_b64 s[14:15], s[26:27]
	v_lshlrev_b32_e32 v4, 4, v2
	v_mov_b32_e32 v2, s15
	v_mov_b32_e32 v6, s13
	v_cndmask_b32_e64 v83, v2, v6, s[4:5]
	v_mov_b32_e32 v2, s14
	v_mov_b32_e32 v6, s12
	s_add_i32 s12, 0, 0x18000
	s_ashr_i32 s64, s90, 3
	s_and_b32 s65, s2, 7
	v_cndmask_b32_e64 v82, v2, v6, s[4:5]
	s_add_u32 s4, s30, 0x29e00000
	s_addc_u32 s5, s31, 0
	v_lshlrev_b32_e32 v85, 7, v170
	s_add_u32 s66, s30, 0x59e00000
	v_add_u32_e32 v173, s6, v4
	v_add3_u32 v175, s6, v5, v85
	s_addc_u32 s67, s31, 0
	s_lshl_b32 s6, s65, 2
	v_readlane_b32 s16, v254, 11
	v_readlane_b32 s17, v254, 12
	v_readlane_b32 s18, v254, 13
	v_readlane_b32 s19, v254, 14
	v_readlane_b32 s20, v254, 15
	v_readlane_b32 s21, v254, 16
	v_readlane_b32 s22, v254, 17
	v_readlane_b32 s23, v254, 18
	v_add_u32_e32 v174, s12, v4
	v_and_b32_e32 v2, 62, v169
	v_mov_b32_e32 v87, 0
	v_add_u32_e32 v179, 0, v4
	v_lshlrev_b32_e32 v4, 3, v171
	s_add_i32 s68, s6, 0
	v_lshlrev_b32_e32 v86, 3, v1
	s_mov_b32 s7, 0
	v_lshlrev_b32_e32 v172, 7, v3
	v_lshlrev_b32_e32 v176, 2, v170
	v_bfe_u32 v177, v3, 1, 3
	v_add_u32_e32 v178, 0, v5
	v_add3_u32 v180, s12, v5, v85
	s_add_i32 s68, s68, 0x26d40
	v_lshl_add_u64 v[88:89], v[82:83], 0, v[86:87]
	v_lshlrev_b32_e32 v90, 2, v2
	s_mov_b64 s[12:13], 0x40000
	s_mov_b64 s[14:15], 0x43800
	s_mov_b64 s[16:17], 0x29e00080
	s_mov_b64 s[18:19], 0x60000
	s_mov_b64 s[20:21], 0x60800
	s_mov_b64 s[22:23], 0x61000
	s_mov_b64 s[24:25], 0x61800
	s_mov_b64 s[26:27], 0x62000
	s_mov_b64 s[28:29], 0x62800
	s_mov_b64 s[30:31], 0x63000
	s_mov_b64 s[34:35], 0x63800
	s_mov_b64 s[36:37], 0x29e00100
	s_mov_b64 s[38:39], 0x80000
	v_lshlrev_b32_e32 v92, 1, v4
	s_mov_b64 s[40:41], 0x80800
	s_mov_b64 s[42:43], 0x81000
	s_mov_b64 s[44:45], 0x81800
	s_mov_b64 s[46:47], 0x82000
	s_mov_b64 s[48:49], 0x82800
	s_mov_b64 s[50:51], 0x83000
	s_mov_b64 s[52:53], 0x83800
	s_waitcnt lgkmcnt(0)
	s_barrier
	s_branch .LBB0_683

; #define MOE_UNIT(idx_, x_, RMAX, CBN, e_, rb_, cb_, ok_) do { int b_ = 0; ok_ = false; for (int k_ = 0; k_ < 8; ++k_) { const int ee_ = (x_) + 8 * k_, n_ = ((ecnt[ee_] + (RMAX) - 1) / (RMAX)) * (CBN); \
;         if ((idx_) < b_ + n_) { e_ = ee_; rb_ = ((idx_) - b_) / (CBN); cb_ = ((idx_) - b_) % (CBN); ok_ = true; break; } b_ += n_; } } while (0)
; __global__ void __launch_bounds__(NTHREADS, 2) hymba_fwd(Args args) {
;     ...
;         for (int j = F.bid >> 3; ; j += F.G >> 3) { int e = 0, rb = 0, cb = 0; bool ok; MOE_UNIT(j, x, mu::MR, 8, e, rb, cb, ok); if (!ok) break;
;             const int n = ecnt[e], nrb = (n + mu::MR - 1) / mu::MR, base = n / nrb, rem = n % nrb, r0 = rb * base + (rb < rem ? rb : rem), nv = base + (rb < rem ? 1 : 0);
;             const long adj = (long)e * CAPS - eo[e];
;             mu::moe_unit<0>(F.lds, e, cb, eo[e] + r0, nv, (const bf16_t*)(F.ws + WS_HB), (const int*)(F.ws + WS_T2 + T2_TOK) + adj, F.wg, F.wu, (bf16_t*)(F.ws + WS_HID), (const float*)(F.ws + WS_T2 + T2_RS) + adj, nullptr); }
.LBB0_688:
	s_andn2_b64 vcc, exec, s[56:57]
	s_mov_b64 s[56:57], -1
	s_cbranch_vccnz .LBB0_682
	s_lshl_b32 s33, s54, 2
	s_add_i32 s33, s33, 0
	s_add_i32 s55, s33, 0x26d40
	v_mov_b32_e32 v1, s55
	ds_read_b32 v1, v1
	v_mov_b32_e32 v5, 0
	s_waitcnt lgkmcnt(0)
	v_readfirstlane_b32 s56, v1
	s_add_i32 s55, s56, 0x13f
	s_mul_hi_i32 s55, s55, 0x66666667
	s_lshr_b32 s57, s55, 31
	s_ashr_i32 s55, s55, 7
	s_add_i32 s57, s55, s57
	s_abs_i32 s58, s57
	v_cvt_f32_u32_e32 v1, s58
	s_sub_i32 s62, 0, s58
	s_abs_i32 s59, s56
	s_xor_b32 s61, s56, s57
	v_rcp_iflag_f32_e32 v1, v1
	s_ashr_i32 s55, s54, 31
	s_ashr_i32 s61, s61, 31
	v_mul_f32_e32 v1, 0x4f7ffffe, v1
	v_cvt_u32_f32_e32 v1, v1
	s_nop 0
	v_readfirstlane_b32 s63, v1
	s_mul_i32 s62, s62, s63
	s_mul_hi_u32 s62, s63, s62
	s_add_i32 s63, s63, s62
	s_mul_hi_u32 s62, s59, s63
	s_mul_i32 s63, s62, s58
	s_sub_i32 s59, s59, s63
	s_add_i32 s69, s62, 1
	s_sub_i32 s63, s59, s58
	s_cmp_ge_u32 s59, s58
	s_cselect_b32 s62, s69, s62
	s_cselect_b32 s59, s63, s59
	s_add_i32 s63, s62, 1
	s_cmp_ge_u32 s59, s58
	s_cselect_b32 s58, s63, s62
	s_xor_b32 s58, s58, s61
	s_sub_i32 s58, s58, s61
	s_mul_i32 s57, s58, s57
	s_sub_i32 s61, s56, s57
	s_cmp_lt_i32 s6, s61
	s_mul_i32 s59, s58, s6
	s_cselect_b64 s[56:57], -1, 0
	s_min_i32 s6, s6, s61
	s_add_i32 s6, s6, s59
	s_cmp_lg_u64 s[56:57], 0
	s_addc_u32 s69, s58, 0
	s_add_i32 s33, s33, 0x26c00
	v_mov_b32_e32 v1, s33
	ds_read_b32 v1, v1
	v_readfirstlane_b32 s58, v0
	s_lshr_b32 s62, s58, 6
	s_mul_hi_u32 s33, s58, 0xcccccccd
	s_lshl_b64 s[56:57], s[54:55], 14
	s_waitcnt lgkmcnt(0)
	v_add_u32_e32 v94, s6, v1
	s_lshl_b32 s6, s62, 3
	s_lshr_b32 s33, s33, 9
	v_mov_b32_e32 v3, s57
	v_ashrrev_i32_e32 v4, 31, v1
	v_sub_co_u32_e32 v2, vcc, s56, v1
	v_or_b32_e32 v1, s6, v130
	s_mul_i32 s56, s33, 0xffffffb0
	v_subb_co_u32_e32 v3, vcc, v3, v4, vcc
	v_add_u32_e32 v4, s56, v1
	v_lshlrev_b64 v[96:97], 2, v[2:3]
	v_lshl_add_u32 v6, v4, 2, s33
	v_lshl_add_u64 v[2:3], s[8:9], 0, v[96:97]
	v_cmp_gt_i32_e32 vcc, s69, v6
	v_mov_b32_e32 v4, 0
	s_and_saveexec_b64 s[56:57], vcc
	s_cbranch_execz .LBB0_691
	v_add_u32_e32 v6, v6, v94
	v_ashrrev_i32_e32 v7, 31, v6
	v_lshl_add_u64 v[6:7], v[6:7], 2, v[2:3]
	global_load_dword v5, v[6:7], off
	s_waitcnt vmcnt(0)
	v_lshlrev_b32_e32 v5, 13, v5

;     __device__ __forceinline__ unsigned row(const Unit& u, int r) const { return (unsigned)slot_tok[u.pm * 256 + r]; }
; #define MU_GLDS_A(buf, kt) do { _Pragma("unroll") for (int i = 0; i < NMU; ++i) \
;         __builtin_amdgcn_global_load_lds((const unsigned*)((const char*)A + aoff[i] + (size_t)(kt) * 128), (PG8_LAS unsigned*)(MU_SA(buf) + wid * 1024 + i * 8192), 16, 0, 0); } while (0)
; template <int MODE>
; __device__ __forceinline__ void moe_unit(PG8_LAS unsigned char* lds, int e, int cb, int slot0  , int nv  , const bf16_t* A, const int* slot_tok,
;                                          const float* W0, const float* W1, bf16_t* OUT, const float* slot_rs  , const int* slot_dst) {
;     ...
;     const int tid = threadIdx.x, wid = __builtin_amdgcn_readfirstlane(tid >> 6), lane = tid & 63, wr = wid >> 1, wc = wid & 1, fr = lane & 15, fq = lane >> 4;
;     unsigned aoff[NMU];
; #pragma unroll
;     for (int i = 0; i < NMU; ++i) { const int R = 8 * (wid + 8 * i) + (lane >> 3), C = 8 * ((lane & 7) ^ ((R >> 1) & 7)); const int w4 = R / RWU, r = 4 * (R - RWU * w4) + w4;
;         const unsigned row = r < nv ? (MODE == 0 ? (unsigned)slot_tok[slot0 + r] : (unsigned)(slot0 + r)) : (MODE == 0 ? 0u : (unsigned)slot0); aoff[i] = (row * (unsigned)K + (unsigned)C) * 2u; }
;     const int jj0 = 2 * (lane & 31), typ = lane >> 5;
;     const int R0 = MODE == 0 ? 64 * (jj0 >> 5) + 32 * typ + 16 * ((jj0 >> 2) & 1) + 4 * ((jj0 >> 3) & 3) + (jj0 & 3) : 2 * lane;
;     const char* Bb = MODE == 0 ? (const char*)((typ ? W1 : W0) + (size_t)e * K * LDB + 64 * cb + jj0) + (size_t)(8 * wid) * RB
;                                : (const char*)(W0 + (size_t)e * K * LDB + 128 * cb + 2 * lane) + (size_t)(8 * wid) * RB;
;     const unsigned bw0 = (unsigned)(R0 * 128 + ((wid ^ ((R0 >> 1) & 7)) * 16)), bw1 = bw0 + 128u;
;     const int nvw = (nv - wr + 3) >> 2, mcnt = nvw <= 0 ? 0 : (((nvw + 15) >> 4) > NMU ? NMU : ((nvw + 15) >> 4));
;     ...
;     MU_GLDS_A(0, 0); MU_B_ISSUE(s0, 0); MU_G_LOAD(g0, 0); MU_B_ISSUE(s1, 1);
;     MU_B_WAIT(s0, 8); MU_B_WRITE(s0, 0, g0); __builtin_amdgcn_sched_barrier(0); MU_B_ISSUE(s0, 2);
;     asm volatile("s_waitcnt vmcnt(16)" ::: "memory");
;     asm volatile("s_waitcnt lgkmcnt(0)" ::: "memory"); __builtin_amdgcn_s_barrier(); asm volatile("" ::: "memory");
.LBB0_699:
	s_or_b64 exec, exec, s[56:57]
	s_lshr_b32 s33, s58, 7
	s_bfe_u32 s70, s58, 0x10006
	v_bfe_u32 v166, v131, 1, 3
	v_xor_b32_e32 v166, v171, v166
	v_lshlrev_b32_e32 v166, 4, v166
	v_lshl_add_u32 v166, v170, 7, v166
	s_mul_i32 s56, s33, 0x2800
	v_add_u32_e32 v135, s56, v166
	v_xor_b32_e32 v137, 64, v135
	s_lshl_b32 s56, s70, 13
	s_add_i32 s56, s56, 0x1e000
	v_add_u32_e32 v139, s56, v166
	v_xor_b32_e32 v141, 64, v139
	v_xor_b32_e32 v1, s62, v177
	v_lshl_add_u32 v1, v1, 4, v172
	v_add_u32_e32 v1, 0x1e000, v1
	s_lshl_b32 s56, s62, 2
	v_add_u32_e32 v166, s56, v171
	v_xor_b32_e32 v166, v166, v131
	v_and_b32_e32 v166, 7, v166
	v_lshlrev_b32_e32 v166, 4, v166
	v_or_b32_e32 v86, v5, v166
	v_or_b32_e32 v134, v6, v166
	v_or_b32_e32 v136, v4, v166
	v_or_b32_e32 v138, v8, v166
	v_or_b32_e32 v140, v7, v166
	s_lshl_b64 s[56:57], s[54:55], 23
	s_lshl_b32 s59, s60, 8
	s_add_u32 s56, s56, s59
	s_addc_u32 s57, s57, 0
	s_lshl_b32 s59, s62, 14
	s_add_u32 s56, s56, s59
	s_addc_u32 s57, s57, 0
	v_mov_b32_e32 v91, 0
	v_lshl_add_u64 v[132:133], v[82:83], 0, s[56:57]
	v_lshl_add_u64 v[132:133], v[132:133], 0, v[90:91]
	s_lshl_b32 s54, s60, 6
	s_ashr_i32 s55, s54, 31
	v_readlane_b32 s28, v254, 9
	v_readlane_b32 s29, v254, 10
	s_lshl_b32 s56, s62, 5
	s_mov_b64 s[30:31], s[4:5]
	s_mov_b64 s[34:35], 0x1000
	s_mov_b64 s[36:37], 0x2000
	s_mov_b64 s[38:39], 0x3000
	s_mov_b64 s[40:41], 0x20000
	s_add_u32 s28, s28, s56
	s_addc_u32 s29, s29, 0
	s_mov_b32 s42, 0
	s_mov_b32 s43, 0xa000
	s_mov_b32 s44, 0x14000
	s_lshl_b32 s6, s62, 10
	s_load_dwordx8 s[12:19], s[28:29], 0x0
	s_load_dwordx8 s[20:27], s[28:29], 0x100
	s_add_u32 s28, s28, 0x200
	s_addc_u32 s29, s29, 0
	s_add_i32 m0, s6, 0x0
	s_nop 0
	global_load_lds_dwordx4 v86, s[30:31]
	s_add_i32 m0, s6, 0x2000
	s_nop 0
	global_load_lds_dwordx4 v134, s[30:31]
	s_add_i32 m0, s6, 0x4000
	s_nop 0
	global_load_lds_dwordx4 v136, s[30:31]
	s_add_i32 m0, s6, 0x6000
	s_nop 0
	global_load_lds_dwordx4 v138, s[30:31]
	s_add_i32 m0, s6, 0x8000
	s_nop 0
	global_load_lds_dwordx4 v140, s[30:31]
	s_add_u32 s30, s30, 0x80
	s_addc_u32 s31, s31, 0
	s_add_i32 m0, s6, 0xa000
	s_nop 0
	global_load_lds_dwordx4 v86, s[30:31]
	s_add_i32 m0, s6, 0xc000
	s_nop 0
	global_load_lds_dwordx4 v134, s[30:31]
	s_add_i32 m0, s6, 0xe000
	s_nop 0
	global_load_lds_dwordx4 v136, s[30:31]
	s_add_i32 m0, s6, 0x10000
	s_nop 0
	global_load_lds_dwordx4 v138, s[30:31]
	s_add_i32 m0, s6, 0x12000
	s_nop 0
	global_load_lds_dwordx4 v140, s[30:31]
	global_load_dwordx2 v[98:99], v[132:133], off
	global_load_dwordx2 v[100:101], v[132:133], off offset:2048
	v_lshl_add_u64 v[166:167], v[132:133], 0, s[34:35]
	global_load_dwordx2 v[102:103], v[166:167], off
	global_load_dwordx2 v[104:105], v[166:167], off offset:2048
	v_lshl_add_u64 v[166:167], v[132:133], 0, s[36:37]
	global_load_dwordx2 v[106:107], v[166:167], off
	global_load_dwordx2 v[108:109], v[166:167], off offset:2048
	v_lshl_add_u64 v[166:167], v[132:133], 0, s[38:39]
	global_load_dwordx2 v[110:111], v[166:167], off
	global_load_dwordx2 v[112:113], v[166:167], off offset:2048
	v_lshl_add_u64 v[132:133], v[132:133], 0, s[40:41]
	global_load_dwordx2 v[114:115], v[132:133], off
	global_load_dwordx2 v[116:117], v[132:133], off offset:2048
	v_lshl_add_u64 v[166:167], v[132:133], 0, s[34:35]
	global_load_dwordx2 v[118:119], v[166:167], off
	global_load_dwordx2 v[120:121], v[166:167], off offset:2048
	v_lshl_add_u64 v[166:167], v[132:133], 0, s[36:37]
	global_load_dwordx2 v[122:123], v[166:167], off
	global_load_dwordx2 v[124:125], v[166:167], off offset:2048
	v_lshl_add_u64 v[166:167], v[132:133], 0, s[38:39]
	global_load_dwordx2 v[126:127], v[166:167], off
	global_load_dwordx2 v[128:129], v[166:167], off offset:2048
	v_lshl_add_u64 v[132:133], v[132:133], 0, s[40:41]
	global_load_dwordx2 v[186:187], v[132:133], off
	global_load_dwordx2 v[188:189], v[132:133], off offset:2048
	v_lshl_add_u64 v[166:167], v[132:133], 0, s[34:35]
	global_load_dwordx2 v[190:191], v[166:167], off
	global_load_dwordx2 v[192:193], v[166:167], off offset:2048
	v_lshl_add_u64 v[166:167], v[132:133], 0, s[36:37]
	global_load_dwordx2 v[194:195], v[166:167], off
	global_load_dwordx2 v[196:197], v[166:167], off offset:2048
	v_lshl_add_u64 v[166:167], v[132:133], 0, s[38:39]
	global_load_dwordx2 v[198:199], v[166:167], off
	global_load_dwordx2 v[200:201], v[166:167], off offset:2048
	v_lshl_add_u64 v[132:133], v[132:133], 0, s[40:41]
	global_load_dwordx2 v[202:203], v[132:133], off
	global_load_dwordx2 v[204:205], v[132:133], off offset:2048
	v_lshl_add_u64 v[166:167], v[132:133], 0, s[34:35]
	global_load_dwordx2 v[206:207], v[166:167], off
	global_load_dwordx2 v[208:209], v[166:167], off offset:2048
	v_lshl_add_u64 v[166:167], v[132:133], 0, s[36:37]
	global_load_dwordx2 v[210:211], v[166:167], off
	global_load_dwordx2 v[212:213], v[166:167], off offset:2048
	v_lshl_add_u64 v[166:167], v[132:133], 0, s[38:39]
	global_load_dwordx2 v[214:215], v[166:167], off
	global_load_dwordx2 v[216:217], v[166:167], off offset:2048
	v_mov_b32_e32 v78, 0
	v_mov_b32_e32 v79, 0
	v_mov_b32_e32 v80, 0
	v_mov_b32_e32 v81, 0
	v_mov_b32_e32 v74, 0
	v_mov_b32_e32 v75, 0
	v_mov_b32_e32 v76, 0
	v_mov_b32_e32 v77, 0
	v_mov_b32_e32 v70, 0
	v_mov_b32_e32 v71, 0
	v_mov_b32_e32 v72, 0
	v_mov_b32_e32 v73, 0
	v_mov_b32_e32 v66, 0
	v_mov_b32_e32 v67, 0
	v_mov_b32_e32 v68, 0
	v_mov_b32_e32 v69, 0
	v_mov_b32_e32 v62, 0
	v_mov_b32_e32 v63, 0
	v_mov_b32_e32 v64, 0
	v_mov_b32_e32 v65, 0
	v_mov_b32_e32 v58, 0
	v_mov_b32_e32 v59, 0
	v_mov_b32_e32 v60, 0
	v_mov_b32_e32 v61, 0
	v_mov_b32_e32 v54, 0
	v_mov_b32_e32 v55, 0
	v_mov_b32_e32 v56, 0
	v_mov_b32_e32 v57, 0
	v_mov_b32_e32 v50, 0
	v_mov_b32_e32 v51, 0
	v_mov_b32_e32 v52, 0
	v_mov_b32_e32 v53, 0
	v_mov_b32_e32 v46, 0
	v_mov_b32_e32 v47, 0
	v_mov_b32_e32 v48, 0
	v_mov_b32_e32 v49, 0
	v_mov_b32_e32 v42, 0
	v_mov_b32_e32 v43, 0
	v_mov_b32_e32 v44, 0
	v_mov_b32_e32 v45, 0
	v_mov_b32_e32 v38, 0
	v_mov_b32_e32 v39, 0
	v_mov_b32_e32 v40, 0
	v_mov_b32_e32 v41, 0
	v_mov_b32_e32 v34, 0
	v_mov_b32_e32 v35, 0
	v_mov_b32_e32 v36, 0
	v_mov_b32_e32 v37, 0
	v_mov_b32_e32 v18, 0
	v_mov_b32_e32 v19, 0
	v_mov_b32_e32 v20, 0
	v_mov_b32_e32 v21, 0
	v_mov_b32_e32 v22, 0
	v_mov_b32_e32 v23, 0
	v_mov_b32_e32 v24, 0
	v_mov_b32_e32 v25, 0
	v_mov_b32_e32 v26, 0
	v_mov_b32_e32 v27, 0
	v_mov_b32_e32 v28, 0
	v_mov_b32_e32 v29, 0
	v_mov_b32_e32 v30, 0
	v_mov_b32_e32 v31, 0
	v_mov_b32_e32 v32, 0
	v_mov_b32_e32 v33, 0
	v_mov_b32_e32 v2, 0
	v_mov_b32_e32 v3, 0
	v_mov_b32_e32 v4, 0
	v_mov_b32_e32 v5, 0
	v_mov_b32_e32 v6, 0
	v_mov_b32_e32 v7, 0
	v_mov_b32_e32 v8, 0
	v_mov_b32_e32 v9, 0
	v_mov_b32_e32 v10, 0
	v_mov_b32_e32 v11, 0
	v_mov_b32_e32 v12, 0
	v_mov_b32_e32 v13, 0
	v_mov_b32_e32 v14, 0
	v_mov_b32_e32 v15, 0
	v_mov_b32_e32 v16, 0
	v_mov_b32_e32 v17, 0
	s_waitcnt vmcnt(24)
; #define MU_GLDS_A(buf, kt) do { _Pragma("unroll") for (int i = 0; i < NMU; ++i) \
;         __builtin_amdgcn_global_load_lds((const unsigned*)((const char*)A + aoff[i] + (size_t)(kt) * 128), (PG8_LAS unsigned*)(MU_SA(buf) + wid * 1024 + i * 8192), 16, 0, 0); } while (0)
; #define MU_B_ISSUE(sb, kt) do { const char* kb_ = Bb + (size_t)(kt) * (64 * (size_t)RB); _Pragma("unroll") for (int j = 0; j < 8; ++j) { const char* p_ = kb_ + (size_t)j * RB; \
;         asm volatile("global_load_dwordx2 %0, %1, off" : "=&v"(sb[j]) : "v"(p_) : "memory"); } } while (0)
; #define MU_B_WAIT(sb, N) asm volatile("s_waitcnt vmcnt(%8)" : "+v"(sb[0]), "+v"(sb[1]), "+v"(sb[2]), "+v"(sb[3]), "+v"(sb[4]), "+v"(sb[5]), "+v"(sb[6]), "+v"(sb[7]) : "n"(N) : "memory")
; #define MU_G_LOAD(ga, kt) do { const PG8_LAS f32x4* gk_ = (const PG8_LAS f32x4*)(lds + GAIN_OFF) + 16 * (kt) + 2 * wid; const f32x4 ga_ = gk_[0], gb_ = gk_[1]; \
;         ga[0] = ga_[0]; ga[1] = ga_[1]; ga[2] = ga_[2]; ga[3] = ga_[3]; ga[4] = gb_[0]; ga[5] = gb_[1]; ga[6] = gb_[2]; ga[7] = gb_[3]; } while (0)
; #define MU_COMPUTE(buf) MU_COMPUTE_N(buf, NMU)
; #define MU_END(last) do { if (last) asm volatile("s_waitcnt vmcnt(0)" ::: "memory"); else asm volatile("s_waitcnt vmcnt(8)" ::: "memory"); \
;         asm volatile("s_waitcnt lgkmcnt(0)" ::: "memory"); __builtin_amdgcn_s_barrier(); asm volatile("" ::: "memory"); } while (0)
; template <int MODE>
; __device__ __forceinline__ void moe_unit(PG8_LAS unsigned char* lds, int e, int cb, int slot0  , int nv  , const bf16_t* A, const int* slot_tok,
;                                          const float* W0, const float* W1, bf16_t* OUT, const float* slot_rs  , const int* slot_dst) {
;     ...
;         if (t + 2 < nt) MU_B_WAIT(s1, 8); else MU_B_WAIT(s1, 0);
;         MU_G_LOAD(g0, t + 1); MU_B_WRITE(s1, 1, g0); __builtin_amdgcn_sched_barrier(0); MU_GLDS_A(1, t + 1); __builtin_amdgcn_sched_barrier(0);
;         if (t + 3 < nt) { MU_B_ISSUE(s1, t + 3); }
;         MU_COMPUTE(0);
;         MU_END(t + 3 >= nt);
;         if (t + 2 < nt) { MU_B_WAIT(s0, 8); MU_G_LOAD(g0, t + 2); MU_B_WRITE(s0, 0, g0); __builtin_amdgcn_sched_barrier(0); MU_GLDS_A(0, t + 2); __builtin_amdgcn_sched_barrier(0); }
;         if (t + 4 < nt) { MU_B_ISSUE(s0, t + 4); }
;         MU_COMPUTE(1);
	s_waitcnt lgkmcnt(0)
	v_mul_f32_e32 v98, s12, v98
	v_mul_f32_e32 v99, s12, v99
	v_mul_f32_e32 v100, s13, v100
	v_mul_f32_e32 v101, s13, v101
	v_mul_f32_e32 v102, s14, v102
	v_mul_f32_e32 v103, s14, v103
	v_mul_f32_e32 v104, s15, v104
	v_mul_f32_e32 v105, s15, v105
	v_mul_f32_e32 v106, s16, v106
	v_mul_f32_e32 v107, s16, v107
	v_mul_f32_e32 v108, s17, v108
	v_mul_f32_e32 v109, s17, v109
	v_mul_f32_e32 v110, s18, v110
	v_mul_f32_e32 v111, s18, v111
	v_mul_f32_e32 v112, s19, v112
	v_mul_f32_e32 v113, s19, v113
	v_cvt_pk_bf16_f32 v158, v98, v100
	v_cvt_pk_bf16_f32 v159, v102, v104
	v_cvt_pk_bf16_f32 v160, v106, v108
	v_cvt_pk_bf16_f32 v161, v110, v112
	v_cvt_pk_bf16_f32 v162, v99, v101
	v_cvt_pk_bf16_f32 v163, v103, v105
	v_cvt_pk_bf16_f32 v164, v107, v109
	v_cvt_pk_bf16_f32 v165, v111, v113
	ds_write_b128 v1, v[158:161]
	ds_write_b128 v1, v[162:165] offset:128
	v_lshl_add_u64 v[132:133], v[132:133], 0, s[40:41]
	global_load_dwordx2 v[98:99], v[132:133], off
	global_load_dwordx2 v[100:101], v[132:133], off offset:2048
	v_lshl_add_u64 v[166:167], v[132:133], 0, s[34:35]
	global_load_dwordx2 v[102:103], v[166:167], off
	global_load_dwordx2 v[104:105], v[166:167], off offset:2048
	v_lshl_add_u64 v[166:167], v[132:133], 0, s[36:37]
	global_load_dwordx2 v[106:107], v[166:167], off
	global_load_dwordx2 v[108:109], v[166:167], off offset:2048
	v_lshl_add_u64 v[166:167], v[132:133], 0, s[38:39]
	global_load_dwordx2 v[110:111], v[166:167], off
	global_load_dwordx2 v[112:113], v[166:167], off offset:2048
	s_waitcnt lgkmcnt(0)
	s_barrier
	s_waitcnt vmcnt(24)
	v_mul_f32_e32 v114, s20, v114
	v_mul_f32_e32 v115, s20, v115
	v_mul_f32_e32 v116, s21, v116
	v_mul_f32_e32 v117, s21, v117
	v_mul_f32_e32 v118, s22, v118
	v_mul_f32_e32 v119, s22, v119
	v_mul_f32_e32 v120, s23, v120
	v_mul_f32_e32 v121, s23, v121
	v_mul_f32_e32 v122, s24, v122
	v_mul_f32_e32 v123, s24, v123
	v_mul_f32_e32 v124, s25, v124
	v_mul_f32_e32 v125, s25, v125
	v_mul_f32_e32 v126, s26, v126
	v_mul_f32_e32 v127, s26, v127
	v_mul_f32_e32 v128, s27, v128
	v_mul_f32_e32 v129, s27, v129
	v_cvt_pk_bf16_f32 v158, v114, v116
	v_cvt_pk_bf16_f32 v159, v118, v120
	v_cvt_pk_bf16_f32 v160, v122, v124
	v_cvt_pk_bf16_f32 v161, v126, v128
	v_cvt_pk_bf16_f32 v162, v115, v117
	v_cvt_pk_bf16_f32 v163, v119, v121
	v_cvt_pk_bf16_f32 v164, v123, v125
	v_cvt_pk_bf16_f32 v165, v127, v129
	ds_write_b128 v1, v[158:161] offset:19456
	ds_write_b128 v1, v[162:165] offset:19584
	v_add_u32_e32 v91, s42, v135
	v_add_u32_e32 v93, s42, v137
	ds_read_b128 v[238:241], v139 offset:0
	ds_read_b128 v[242:245], v139 offset:2048
	ds_read_b128 v[246:249], v139 offset:4096
	ds_read_b128 v[250:253], v139 offset:6144
	ds_read_b128 v[218:221], v91 offset:0
	ds_read_b128 v[222:225], v91 offset:2048
	ds_read_b128 v[226:229], v91 offset:4096
	ds_read_b128 v[230:233], v91 offset:6144
	ds_read_b128 v[234:237], v91 offset:8192
	s_add_i32 s47, s44, s6
	s_add_u32 s30, s30, 0x80
	s_addc_u32 s31, s31, 0
	s_waitcnt lgkmcnt(0)
	v_mfma_f32_16x16x32_bf16 v[78:81], v[238:241], v[218:221], v[78:81]
	v_mfma_f32_16x16x32_bf16 v[74:77], v[242:245], v[218:221], v[74:77]
	v_mfma_f32_16x16x32_bf16 v[70:73], v[246:249], v[218:221], v[70:73]
	v_mfma_f32_16x16x32_bf16 v[66:69], v[250:253], v[218:221], v[66:69]
	ds_read_b128 v[218:221], v93 offset:0
	ds_read_b128 v[142:145], v141 offset:0
	s_mov_b32 m0, s47
	s_nop 0
	global_load_lds_dwordx4 v86, s[30:31]
	v_mfma_f32_16x16x32_bf16 v[62:65], v[238:241], v[222:225], v[62:65]
	v_mfma_f32_16x16x32_bf16 v[58:61], v[242:245], v[222:225], v[58:61]
	v_mfma_f32_16x16x32_bf16 v[54:57], v[246:249], v[222:225], v[54:57]
	v_mfma_f32_16x16x32_bf16 v[50:53], v[250:253], v[222:225], v[50:53]
	ds_read_b128 v[222:225], v93 offset:2048
	ds_read_b128 v[146:149], v141 offset:2048
	s_add_i32 m0, s47, 0x2000
	s_nop 0
	global_load_lds_dwordx4 v134, s[30:31]
	v_mfma_f32_16x16x32_bf16 v[46:49], v[238:241], v[226:229], v[46:49]
	v_mfma_f32_16x16x32_bf16 v[42:45], v[242:245], v[226:229], v[42:45]
	v_mfma_f32_16x16x32_bf16 v[38:41], v[246:249], v[226:229], v[38:41]
	v_mfma_f32_16x16x32_bf16 v[34:37], v[250:253], v[226:229], v[34:37]
	ds_read_b128 v[226:229], v93 offset:4096
	ds_read_b128 v[150:153], v141 offset:4096
	s_add_i32 m0, s47, 0x4000
	s_nop 0
	global_load_lds_dwordx4 v136, s[30:31]
	v_mfma_f32_16x16x32_bf16 v[18:21], v[238:241], v[230:233], v[18:21]
	v_mfma_f32_16x16x32_bf16 v[22:25], v[242:245], v[230:233], v[22:25]
	v_mfma_f32_16x16x32_bf16 v[26:29], v[246:249], v[230:233], v[26:29]
	v_mfma_f32_16x16x32_bf16 v[30:33], v[250:253], v[230:233], v[30:33]
	ds_read_b128 v[230:233], v93 offset:6144
	ds_read_b128 v[154:157], v141 offset:6144
	s_add_i32 m0, s47, 0x6000
	s_nop 0
	global_load_lds_dwordx4 v138, s[30:31]
	v_mfma_f32_16x16x32_bf16 v[2:5], v[238:241], v[234:237], v[2:5]
	v_mfma_f32_16x16x32_bf16 v[6:9], v[242:245], v[234:237], v[6:9]
	v_mfma_f32_16x16x32_bf16 v[10:13], v[246:249], v[234:237], v[10:13]
	v_mfma_f32_16x16x32_bf16 v[14:17], v[250:253], v[234:237], v[14:17]
	ds_read_b128 v[234:237], v93 offset:8192
	s_add_i32 m0, s47, 0x8000
	s_nop 0
	global_load_lds_dwordx4 v140, s[30:31]
	s_waitcnt lgkmcnt(0)
; #define MU_GLDS_A(buf, kt) do { _Pragma("unroll") for (int i = 0; i < NMU; ++i) \
;         __builtin_amdgcn_global_load_lds((const unsigned*)((const char*)A + aoff[i] + (size_t)(kt) * 128), (PG8_LAS unsigned*)(MU_SA(buf) + wid * 1024 + i * 8192), 16, 0, 0); } while (0)
; #define MU_B_ISSUE(sb, kt) do { const char* kb_ = Bb + (size_t)(kt) * (64 * (size_t)RB); _Pragma("unroll") for (int j = 0; j < 8; ++j) { const char* p_ = kb_ + (size_t)j * RB; \
;         asm volatile("global_load_dwordx2 %0, %1, off" : "=&v"(sb[j]) : "v"(p_) : "memory"); } } while (0)
; #define MU_B_WAIT(sb, N) asm volatile("s_waitcnt vmcnt(%8)" : "+v"(sb[0]), "+v"(sb[1]), "+v"(sb[2]), "+v"(sb[3]), "+v"(sb[4]), "+v"(sb[5]), "+v"(sb[6]), "+v"(sb[7]) : "n"(N) : "memory")
; #define MU_G_LOAD(ga, kt) do { const PG8_LAS f32x4* gk_ = (const PG8_LAS f32x4*)(lds + GAIN_OFF) + 16 * (kt) + 2 * wid; const f32x4 ga_ = gk_[0], gb_ = gk_[1]; \
;         ga[0] = ga_[0]; ga[1] = ga_[1]; ga[2] = ga_[2]; ga[3] = ga_[3]; ga[4] = gb_[0]; ga[5] = gb_[1]; ga[6] = gb_[2]; ga[7] = gb_[3]; } while (0)
; #define MU_COMPUTE(buf) MU_COMPUTE_N(buf, NMU)
; #define MU_END(last) do { if (last) asm volatile("s_waitcnt vmcnt(0)" ::: "memory"); else asm volatile("s_waitcnt vmcnt(8)" ::: "memory"); \
;         asm volatile("s_waitcnt lgkmcnt(0)" ::: "memory"); __builtin_amdgcn_s_barrier(); asm volatile("" ::: "memory"); } while (0)
; template <int MODE>
; __device__ __forceinline__ void moe_unit(PG8_LAS unsigned char* lds, int e, int cb, int slot0  , int nv  , const bf16_t* A, const int* slot_tok,
;                                          const float* W0, const float* W1, bf16_t* OUT, const float* slot_rs  , const int* slot_dst) {
;     ...
;         if (t + 2 < nt) MU_B_WAIT(s1, 8); else MU_B_WAIT(s1, 0);
;         MU_G_LOAD(g0, t + 1); MU_B_WRITE(s1, 1, g0); __builtin_amdgcn_sched_barrier(0); MU_GLDS_A(1, t + 1); __builtin_amdgcn_sched_barrier(0);
;         if (t + 3 < nt) { MU_B_ISSUE(s1, t + 3); }
;         MU_COMPUTE(0);
;         MU_END(t + 3 >= nt);
;         if (t + 2 < nt) { MU_B_WAIT(s0, 8); MU_G_LOAD(g0, t + 2); MU_B_WRITE(s0, 0, g0); __builtin_amdgcn_sched_barrier(0); MU_GLDS_A(0, t + 2); __builtin_amdgcn_sched_barrier(0); }
;         if (t + 4 < nt) { MU_B_ISSUE(s0, t + 4); }
;         MU_COMPUTE(1);
;         MU_END(t + 4 >= nt);
	s_load_dwordx8 s[12:19], s[28:29], 0x0
	s_add_u32 s28, s28, 0x100
	s_addc_u32 s29, s29, 0
	v_mfma_f32_16x16x32_bf16 v[78:81], v[142:145], v[218:221], v[78:81]
	v_mfma_f32_16x16x32_bf16 v[74:77], v[146:149], v[218:221], v[74:77]
	v_mfma_f32_16x16x32_bf16 v[70:73], v[150:153], v[218:221], v[70:73]
	v_mfma_f32_16x16x32_bf16 v[66:69], v[154:157], v[218:221], v[66:69]
	v_lshl_add_u64 v[132:133], v[132:133], 0, s[40:41]
	global_load_dwordx2 v[114:115], v[132:133], off
	global_load_dwordx2 v[116:117], v[132:133], off offset:2048
	v_mfma_f32_16x16x32_bf16 v[62:65], v[142:145], v[222:225], v[62:65]
	v_mfma_f32_16x16x32_bf16 v[58:61], v[146:149], v[222:225], v[58:61]
	v_mfma_f32_16x16x32_bf16 v[54:57], v[150:153], v[222:225], v[54:57]
	v_mfma_f32_16x16x32_bf16 v[50:53], v[154:157], v[222:225], v[50:53]
	v_lshl_add_u64 v[166:167], v[132:133], 0, s[34:35]
	global_load_dwordx2 v[118:119], v[166:167], off
	global_load_dwordx2 v[120:121], v[166:167], off offset:2048
	v_mfma_f32_16x16x32_bf16 v[46:49], v[142:145], v[226:229], v[46:49]
	v_mfma_f32_16x16x32_bf16 v[42:45], v[146:149], v[226:229], v[42:45]
	v_mfma_f32_16x16x32_bf16 v[38:41], v[150:153], v[226:229], v[38:41]
	v_mfma_f32_16x16x32_bf16 v[34:37], v[154:157], v[226:229], v[34:37]
	v_lshl_add_u64 v[166:167], v[132:133], 0, s[36:37]
	global_load_dwordx2 v[122:123], v[166:167], off
	global_load_dwordx2 v[124:125], v[166:167], off offset:2048
	v_mfma_f32_16x16x32_bf16 v[18:21], v[142:145], v[230:233], v[18:21]
	v_mfma_f32_16x16x32_bf16 v[22:25], v[146:149], v[230:233], v[22:25]
	v_mfma_f32_16x16x32_bf16 v[26:29], v[150:153], v[230:233], v[26:29]
	v_mfma_f32_16x16x32_bf16 v[30:33], v[154:157], v[230:233], v[30:33]
	v_lshl_add_u64 v[166:167], v[132:133], 0, s[38:39]
	global_load_dwordx2 v[126:127], v[166:167], off
	global_load_dwordx2 v[128:129], v[166:167], off offset:2048
	v_mfma_f32_16x16x32_bf16 v[2:5], v[142:145], v[234:237], v[2:5]
	v_mfma_f32_16x16x32_bf16 v[6:9], v[146:149], v[234:237], v[6:9]
	v_mfma_f32_16x16x32_bf16 v[10:13], v[150:153], v[234:237], v[10:13]
	v_mfma_f32_16x16x32_bf16 v[14:17], v[154:157], v[234:237], v[14:17]
	s_waitcnt lgkmcnt(0)
	s_barrier
	s_mov_b32 s47, s42
	s_mov_b32 s42, s43
	s_mov_b32 s43, s44
	s_mov_b32 s44, s47
	s_waitcnt vmcnt(29)
	v_mul_f32_e32 v186, s12, v186
	v_mul_f32_e32 v187, s12, v187
	v_mul_f32_e32 v188, s13, v188
	v_mul_f32_e32 v189, s13, v189
	v_mul_f32_e32 v190, s14, v190
	v_mul_f32_e32 v191, s14, v191
	v_mul_f32_e32 v192, s15, v192
	v_mul_f32_e32 v193, s15, v193
	v_mul_f32_e32 v194, s16, v194
	v_mul_f32_e32 v195, s16, v195
	v_mul_f32_e32 v196, s17, v196
	v_mul_f32_e32 v197, s17, v197
	v_mul_f32_e32 v198, s18, v198
	v_mul_f32_e32 v199, s18, v199
	v_mul_f32_e32 v200, s19, v200
	v_mul_f32_e32 v201, s19, v201
	v_cvt_pk_bf16_f32 v158, v186, v188
	v_cvt_pk_bf16_f32 v159, v190, v192
	v_cvt_pk_bf16_f32 v160, v194, v196
	v_cvt_pk_bf16_f32 v161, v198, v200
	v_cvt_pk_bf16_f32 v162, v187, v189
	v_cvt_pk_bf16_f32 v163, v191, v193
	v_cvt_pk_bf16_f32 v164, v195, v197
	v_cvt_pk_bf16_f32 v165, v199, v201
	ds_write_b128 v1, v[158:161] offset:0
	ds_write_b128 v1, v[162:165] offset:128
	v_add_u32_e32 v91, s42, v135
	v_add_u32_e32 v93, s42, v137
	ds_read_b128 v[238:241], v139 offset:19456
	ds_read_b128 v[242:245], v139 offset:21504
	ds_read_b128 v[246:249], v139 offset:23552
	ds_read_b128 v[250:253], v139 offset:25600
	ds_read_b128 v[218:221], v91 offset:0
	ds_read_b128 v[222:225], v91 offset:2048
	ds_read_b128 v[226:229], v91 offset:4096
	ds_read_b128 v[230:233], v91 offset:6144
	ds_read_b128 v[234:237], v91 offset:8192
	s_add_i32 s47, s44, s6
	s_add_u32 s30, s30, 0x80
	s_addc_u32 s31, s31, 0
	s_waitcnt lgkmcnt(0)
	v_mfma_f32_16x16x32_bf16 v[78:81], v[238:241], v[218:221], v[78:81]
	v_mfma_f32_16x16x32_bf16 v[74:77], v[242:245], v[218:221], v[74:77]
	v_mfma_f32_16x16x32_bf16 v[70:73], v[246:249], v[218:221], v[70:73]
	v_mfma_f32_16x16x32_bf16 v[66:69], v[250:253], v[218:221], v[66:69]
	ds_read_b128 v[218:221], v93 offset:0
	ds_read_b128 v[142:145], v141 offset:19456
	s_mov_b32 m0, s47
	s_nop 0
	global_load_lds_dwordx4 v86, s[30:31]
	v_mfma_f32_16x16x32_bf16 v[62:65], v[238:241], v[222:225], v[62:65]
	v_mfma_f32_16x16x32_bf16 v[58:61], v[242:245], v[222:225], v[58:61]
	v_mfma_f32_16x16x32_bf16 v[54:57], v[246:249], v[222:225], v[54:57]
	v_mfma_f32_16x16x32_bf16 v[50:53], v[250:253], v[222:225], v[50:53]
	ds_read_b128 v[222:225], v93 offset:2048
	ds_read_b128 v[146:149], v141 offset:21504
	s_add_i32 m0, s47, 0x2000
	s_nop 0
	global_load_lds_dwordx4 v134, s[30:31]
	v_mfma_f32_16x16x32_bf16 v[46:49], v[238:241], v[226:229], v[46:49]
	v_mfma_f32_16x16x32_bf16 v[42:45], v[242:245], v[226:229], v[42:45]
	v_mfma_f32_16x16x32_bf16 v[38:41], v[246:249], v[226:229], v[38:41]
	v_mfma_f32_16x16x32_bf16 v[34:37], v[250:253], v[226:229], v[34:37]
	ds_read_b128 v[226:229], v93 offset:4096
	ds_read_b128 v[150:153], v141 offset:23552
	s_add_i32 m0, s47, 0x4000
	s_nop 0
	global_load_lds_dwordx4 v136, s[30:31]
	v_mfma_f32_16x16x32_bf16 v[18:21], v[238:241], v[230:233], v[18:21]
	v_mfma_f32_16x16x32_bf16 v[22:25], v[242:245], v[230:233], v[22:25]
	v_mfma_f32_16x16x32_bf16 v[26:29], v[246:249], v[230:233], v[26:29]
	v_mfma_f32_16x16x32_bf16 v[30:33], v[250:253], v[230:233], v[30:33]
	ds_read_b128 v[230:233], v93 offset:6144
	ds_read_b128 v[154:157], v141 offset:25600
	s_add_i32 m0, s47, 0x6000
	s_nop 0
	global_load_lds_dwordx4 v138, s[30:31]
	v_mfma_f32_16x16x32_bf16 v[2:5], v[238:241], v[234:237], v[2:5]
	v_mfma_f32_16x16x32_bf16 v[6:9], v[242:245], v[234:237], v[6:9]
	v_mfma_f32_16x16x32_bf16 v[10:13], v[246:249], v[234:237], v[10:13]
	v_mfma_f32_16x16x32_bf16 v[14:17], v[250:253], v[234:237], v[14:17]
	ds_read_b128 v[234:237], v93 offset:8192
	s_add_i32 m0, s47, 0x8000
	s_nop 0
	global_load_lds_dwordx4 v140, s[30:31]
	s_waitcnt lgkmcnt(0)
; #define MU_GLDS_A(buf, kt) do { _Pragma("unroll") for (int i = 0; i < NMU; ++i) \
;         __builtin_amdgcn_global_load_lds((const unsigned*)((const char*)A + aoff[i] + (size_t)(kt) * 128), (PG8_LAS unsigned*)(MU_SA(buf) + wid * 1024 + i * 8192), 16, 0, 0); } while (0)
; #define MU_B_ISSUE(sb, kt) do { const char* kb_ = Bb + (size_t)(kt) * (64 * (size_t)RB); _Pragma("unroll") for (int j = 0; j < 8; ++j) { const char* p_ = kb_ + (size_t)j * RB; \
;         asm volatile("global_load_dwordx2 %0, %1, off" : "=&v"(sb[j]) : "v"(p_) : "memory"); } } while (0)
; #define MU_B_WAIT(sb, N) asm volatile("s_waitcnt vmcnt(%8)" : "+v"(sb[0]), "+v"(sb[1]), "+v"(sb[2]), "+v"(sb[3]), "+v"(sb[4]), "+v"(sb[5]), "+v"(sb[6]), "+v"(sb[7]) : "n"(N) : "memory")
; #define MU_G_LOAD(ga, kt) do { const PG8_LAS f32x4* gk_ = (const PG8_LAS f32x4*)(lds + GAIN_OFF) + 16 * (kt) + 2 * wid; const f32x4 ga_ = gk_[0], gb_ = gk_[1]; \
;         ga[0] = ga_[0]; ga[1] = ga_[1]; ga[2] = ga_[2]; ga[3] = ga_[3]; ga[4] = gb_[0]; ga[5] = gb_[1]; ga[6] = gb_[2]; ga[7] = gb_[3]; } while (0)
; #define MU_COMPUTE(buf) MU_COMPUTE_N(buf, NMU)
; #define MU_END(last) do { if (last) asm volatile("s_waitcnt vmcnt(0)" ::: "memory"); else asm volatile("s_waitcnt vmcnt(8)" ::: "memory"); \
;         asm volatile("s_waitcnt lgkmcnt(0)" ::: "memory"); __builtin_amdgcn_s_barrier(); asm volatile("" ::: "memory"); } while (0)
; template <int MODE>
; __device__ __forceinline__ void moe_unit(PG8_LAS unsigned char* lds, int e, int cb, int slot0  , int nv  , const bf16_t* A, const int* slot_tok,
;                                          const float* W0, const float* W1, bf16_t* OUT, const float* slot_rs  , const int* slot_dst) {
;     ...
;         if (t + 2 < nt) MU_B_WAIT(s1, 8); else MU_B_WAIT(s1, 0);
;         MU_G_LOAD(g0, t + 1); MU_B_WRITE(s1, 1, g0); __builtin_amdgcn_sched_barrier(0); MU_GLDS_A(1, t + 1); __builtin_amdgcn_sched_barrier(0);
;         if (t + 3 < nt) { MU_B_ISSUE(s1, t + 3); }
;         MU_COMPUTE(0);
;         MU_END(t + 3 >= nt);
;         if (t + 2 < nt) { MU_B_WAIT(s0, 8); MU_G_LOAD(g0, t + 2); MU_B_WRITE(s0, 0, g0); __builtin_amdgcn_sched_barrier(0); MU_GLDS_A(0, t + 2); __builtin_amdgcn_sched_barrier(0); }
;         if (t + 4 < nt) { MU_B_ISSUE(s0, t + 4); }
;         MU_COMPUTE(1);
;         MU_END(t + 4 >= nt);
	s_load_dwordx8 s[20:27], s[28:29], 0x0
	s_add_u32 s28, s28, 0x100
	s_addc_u32 s29, s29, 0
	v_mfma_f32_16x16x32_bf16 v[78:81], v[142:145], v[218:221], v[78:81]
	v_mfma_f32_16x16x32_bf16 v[74:77], v[146:149], v[218:221], v[74:77]
	v_mfma_f32_16x16x32_bf16 v[70:73], v[150:153], v[218:221], v[70:73]
	v_mfma_f32_16x16x32_bf16 v[66:69], v[154:157], v[218:221], v[66:69]
	v_lshl_add_u64 v[132:133], v[132:133], 0, s[40:41]
	global_load_dwordx2 v[186:187], v[132:133], off
	global_load_dwordx2 v[188:189], v[132:133], off offset:2048
	v_mfma_f32_16x16x32_bf16 v[62:65], v[142:145], v[222:225], v[62:65]
	v_mfma_f32_16x16x32_bf16 v[58:61], v[146:149], v[222:225], v[58:61]
	v_mfma_f32_16x16x32_bf16 v[54:57], v[150:153], v[222:225], v[54:57]
	v_mfma_f32_16x16x32_bf16 v[50:53], v[154:157], v[222:225], v[50:53]
	v_lshl_add_u64 v[166:167], v[132:133], 0, s[34:35]
	global_load_dwordx2 v[190:191], v[166:167], off
	global_load_dwordx2 v[192:193], v[166:167], off offset:2048
	v_mfma_f32_16x16x32_bf16 v[46:49], v[142:145], v[226:229], v[46:49]
	v_mfma_f32_16x16x32_bf16 v[42:45], v[146:149], v[226:229], v[42:45]
	v_mfma_f32_16x16x32_bf16 v[38:41], v[150:153], v[226:229], v[38:41]
	v_mfma_f32_16x16x32_bf16 v[34:37], v[154:157], v[226:229], v[34:37]
	v_lshl_add_u64 v[166:167], v[132:133], 0, s[36:37]
	global_load_dwordx2 v[194:195], v[166:167], off
	global_load_dwordx2 v[196:197], v[166:167], off offset:2048
	v_mfma_f32_16x16x32_bf16 v[18:21], v[142:145], v[230:233], v[18:21]
	v_mfma_f32_16x16x32_bf16 v[22:25], v[146:149], v[230:233], v[22:25]
	v_mfma_f32_16x16x32_bf16 v[26:29], v[150:153], v[230:233], v[26:29]
	v_mfma_f32_16x16x32_bf16 v[30:33], v[154:157], v[230:233], v[30:33]
	v_lshl_add_u64 v[166:167], v[132:133], 0, s[38:39]
	global_load_dwordx2 v[198:199], v[166:167], off
	global_load_dwordx2 v[200:201], v[166:167], off offset:2048
	v_mfma_f32_16x16x32_bf16 v[2:5], v[142:145], v[234:237], v[2:5]
	v_mfma_f32_16x16x32_bf16 v[6:9], v[146:149], v[234:237], v[6:9]
	v_mfma_f32_16x16x32_bf16 v[10:13], v[150:153], v[234:237], v[10:13]
	v_mfma_f32_16x16x32_bf16 v[14:17], v[154:157], v[234:237], v[14:17]
	s_waitcnt vmcnt(21)
	s_waitcnt lgkmcnt(0)
	s_barrier
	s_mov_b32 s47, s42
	s_mov_b32 s42, s43
	s_mov_b32 s43, s44
	s_mov_b32 s44, s47
	v_mul_f32_e32 v202, s20, v202
	v_mul_f32_e32 v203, s20, v203
	v_mul_f32_e32 v204, s21, v204
	v_mul_f32_e32 v205, s21, v205
	v_mul_f32_e32 v206, s22, v206
	v_mul_f32_e32 v207, s22, v207
	v_mul_f32_e32 v208, s23, v208
	v_mul_f32_e32 v209, s23, v209
	v_mul_f32_e32 v210, s24, v210
	v_mul_f32_e32 v211, s24, v211
	v_mul_f32_e32 v212, s25, v212
	v_mul_f32_e32 v213, s25, v213
	v_mul_f32_e32 v214, s26, v214
	v_mul_f32_e32 v215, s26, v215
	v_mul_f32_e32 v216, s27, v216
	v_mul_f32_e32 v217, s27, v217
	v_cvt_pk_bf16_f32 v158, v202, v204
	v_cvt_pk_bf16_f32 v159, v206, v208
	v_cvt_pk_bf16_f32 v160, v210, v212
	v_cvt_pk_bf16_f32 v161, v214, v216
	v_cvt_pk_bf16_f32 v162, v203, v205
	v_cvt_pk_bf16_f32 v163, v207, v209
	v_cvt_pk_bf16_f32 v164, v211, v213
	v_cvt_pk_bf16_f32 v165, v215, v217
	ds_write_b128 v1, v[158:161] offset:19456
	ds_write_b128 v1, v[162:165] offset:19584
	v_add_u32_e32 v91, s42, v135
	v_add_u32_e32 v93, s42, v137
	ds_read_b128 v[238:241], v139 offset:0
	ds_read_b128 v[242:245], v139 offset:2048
	ds_read_b128 v[246:249], v139 offset:4096
	ds_read_b128 v[250:253], v139 offset:6144
	ds_read_b128 v[218:221], v91 offset:0
	ds_read_b128 v[222:225], v91 offset:2048
	ds_read_b128 v[226:229], v91 offset:4096
	ds_read_b128 v[230:233], v91 offset:6144
	ds_read_b128 v[234:237], v91 offset:8192
	s_add_i32 s47, s44, s6
	s_add_u32 s30, s30, 0x80
	s_addc_u32 s31, s31, 0
	s_waitcnt lgkmcnt(0)
	v_mfma_f32_16x16x32_bf16 v[78:81], v[238:241], v[218:221], v[78:81]
	v_mfma_f32_16x16x32_bf16 v[74:77], v[242:245], v[218:221], v[74:77]
	v_mfma_f32_16x16x32_bf16 v[70:73], v[246:249], v[218:221], v[70:73]
	v_mfma_f32_16x16x32_bf16 v[66:69], v[250:253], v[218:221], v[66:69]
	ds_read_b128 v[218:221], v93 offset:0
	ds_read_b128 v[142:145], v141 offset:0
	s_mov_b32 m0, s47
	s_nop 0
	global_load_lds_dwordx4 v86, s[30:31]
	v_mfma_f32_16x16x32_bf16 v[62:65], v[238:241], v[222:225], v[62:65]
	v_mfma_f32_16x16x32_bf16 v[58:61], v[242:245], v[222:225], v[58:61]
	v_mfma_f32_16x16x32_bf16 v[54:57], v[246:249], v[222:225], v[54:57]
	v_mfma_f32_16x16x32_bf16 v[50:53], v[250:253], v[222:225], v[50:53]
	ds_read_b128 v[222:225], v93 offset:2048
	ds_read_b128 v[146:149], v141 offset:2048
	s_add_i32 m0, s47, 0x2000
	s_nop 0
	global_load_lds_dwordx4 v134, s[30:31]
	v_mfma_f32_16x16x32_bf16 v[46:49], v[238:241], v[226:229], v[46:49]
	v_mfma_f32_16x16x32_bf16 v[42:45], v[242:245], v[226:229], v[42:45]
	v_mfma_f32_16x16x32_bf16 v[38:41], v[246:249], v[226:229], v[38:41]
	v_mfma_f32_16x16x32_bf16 v[34:37], v[250:253], v[226:229], v[34:37]
	ds_read_b128 v[226:229], v93 offset:4096
	ds_read_b128 v[150:153], v141 offset:4096
	s_add_i32 m0, s47, 0x4000
	s_nop 0
	global_load_lds_dwordx4 v136, s[30:31]
	v_mfma_f32_16x16x32_bf16 v[18:21], v[238:241], v[230:233], v[18:21]
	v_mfma_f32_16x16x32_bf16 v[22:25], v[242:245], v[230:233], v[22:25]
	v_mfma_f32_16x16x32_bf16 v[26:29], v[246:249], v[230:233], v[26:29]
	v_mfma_f32_16x16x32_bf16 v[30:33], v[250:253], v[230:233], v[30:33]
	ds_read_b128 v[230:233], v93 offset:6144
	ds_read_b128 v[154:157], v141 offset:6144
	s_add_i32 m0, s47, 0x6000
	s_nop 0
	global_load_lds_dwordx4 v138, s[30:31]
	v_mfma_f32_16x16x32_bf16 v[2:5], v[238:241], v[234:237], v[2:5]
	v_mfma_f32_16x16x32_bf16 v[6:9], v[242:245], v[234:237], v[6:9]
	v_mfma_f32_16x16x32_bf16 v[10:13], v[246:249], v[234:237], v[10:13]
	v_mfma_f32_16x16x32_bf16 v[14:17], v[250:253], v[234:237], v[14:17]
	ds_read_b128 v[234:237], v93 offset:8192
	s_add_i32 m0, s47, 0x8000
	s_nop 0
	global_load_lds_dwordx4 v140, s[30:31]
	s_waitcnt lgkmcnt(0)
; #define MU_GLDS_A(buf, kt) do { _Pragma("unroll") for (int i = 0; i < NMU; ++i) \
;         __builtin_amdgcn_global_load_lds((const unsigned*)((const char*)A + aoff[i] + (size_t)(kt) * 128), (PG8_LAS unsigned*)(MU_SA(buf) + wid * 1024 + i * 8192), 16, 0, 0); } while (0)
; #define MU_B_ISSUE(sb, kt) do { const char* kb_ = Bb + (size_t)(kt) * (64 * (size_t)RB); _Pragma("unroll") for (int j = 0; j < 8; ++j) { const char* p_ = kb_ + (size_t)j * RB; \
;         asm volatile("global_load_dwordx2 %0, %1, off" : "=&v"(sb[j]) : "v"(p_) : "memory"); } } while (0)
; #define MU_B_WAIT(sb, N) asm volatile("s_waitcnt vmcnt(%8)" : "+v"(sb[0]), "+v"(sb[1]), "+v"(sb[2]), "+v"(sb[3]), "+v"(sb[4]), "+v"(sb[5]), "+v"(sb[6]), "+v"(sb[7]) : "n"(N) : "memory")
; #define MU_G_LOAD(ga, kt) do { const PG8_LAS f32x4* gk_ = (const PG8_LAS f32x4*)(lds + GAIN_OFF) + 16 * (kt) + 2 * wid; const f32x4 ga_ = gk_[0], gb_ = gk_[1]; \
;         ga[0] = ga_[0]; ga[1] = ga_[1]; ga[2] = ga_[2]; ga[3] = ga_[3]; ga[4] = gb_[0]; ga[5] = gb_[1]; ga[6] = gb_[2]; ga[7] = gb_[3]; } while (0)
; #define MU_COMPUTE(buf) MU_COMPUTE_N(buf, NMU)
; #define MU_END(last) do { if (last) asm volatile("s_waitcnt vmcnt(0)" ::: "memory"); else asm volatile("s_waitcnt vmcnt(8)" ::: "memory"); \
;         asm volatile("s_waitcnt lgkmcnt(0)" ::: "memory"); __builtin_amdgcn_s_barrier(); asm volatile("" ::: "memory"); } while (0)
; template <int MODE>
; __device__ __forceinline__ void moe_unit(PG8_LAS unsigned char* lds, int e, int cb, int slot0  , int nv  , const bf16_t* A, const int* slot_tok,
;                                          const float* W0, const float* W1, bf16_t* OUT, const float* slot_rs  , const int* slot_dst) {
;     ...
;         if (t + 2 < nt) MU_B_WAIT(s1, 8); else MU_B_WAIT(s1, 0);
;         MU_G_LOAD(g0, t + 1); MU_B_WRITE(s1, 1, g0); __builtin_amdgcn_sched_barrier(0); MU_GLDS_A(1, t + 1); __builtin_amdgcn_sched_barrier(0);
;         if (t + 3 < nt) { MU_B_ISSUE(s1, t + 3); }
;         MU_COMPUTE(0);
;         MU_END(t + 3 >= nt);
;         if (t + 2 < nt) { MU_B_WAIT(s0, 8); MU_G_LOAD(g0, t + 2); MU_B_WRITE(s0, 0, g0); __builtin_amdgcn_sched_barrier(0); MU_GLDS_A(0, t + 2); __builtin_amdgcn_sched_barrier(0); }
;         if (t + 4 < nt) { MU_B_ISSUE(s0, t + 4); }
;         MU_COMPUTE(1);
;         MU_END(t + 4 >= nt);
	s_load_dwordx8 s[12:19], s[28:29], 0x0
	s_add_u32 s28, s28, 0x100
	s_addc_u32 s29, s29, 0
	v_mfma_f32_16x16x32_bf16 v[78:81], v[142:145], v[218:221], v[78:81]
	v_mfma_f32_16x16x32_bf16 v[74:77], v[146:149], v[218:221], v[74:77]
	v_mfma_f32_16x16x32_bf16 v[70:73], v[150:153], v[218:221], v[70:73]
	v_mfma_f32_16x16x32_bf16 v[66:69], v[154:157], v[218:221], v[66:69]
	v_lshl_add_u64 v[132:133], v[132:133], 0, s[40:41]
	global_load_dwordx2 v[202:203], v[132:133], off
	global_load_dwordx2 v[204:205], v[132:133], off offset:2048
	v_mfma_f32_16x16x32_bf16 v[62:65], v[142:145], v[222:225], v[62:65]
	v_mfma_f32_16x16x32_bf16 v[58:61], v[146:149], v[222:225], v[58:61]
	v_mfma_f32_16x16x32_bf16 v[54:57], v[150:153], v[222:225], v[54:57]
	v_mfma_f32_16x16x32_bf16 v[50:53], v[154:157], v[222:225], v[50:53]
	v_lshl_add_u64 v[166:167], v[132:133], 0, s[34:35]
	global_load_dwordx2 v[206:207], v[166:167], off
	global_load_dwordx2 v[208:209], v[166:167], off offset:2048
	v_mfma_f32_16x16x32_bf16 v[46:49], v[142:145], v[226:229], v[46:49]
	v_mfma_f32_16x16x32_bf16 v[42:45], v[146:149], v[226:229], v[42:45]
	v_mfma_f32_16x16x32_bf16 v[38:41], v[150:153], v[226:229], v[38:41]
	v_mfma_f32_16x16x32_bf16 v[34:37], v[154:157], v[226:229], v[34:37]
	v_lshl_add_u64 v[166:167], v[132:133], 0, s[36:37]
	global_load_dwordx2 v[210:211], v[166:167], off
	global_load_dwordx2 v[212:213], v[166:167], off offset:2048
	v_mfma_f32_16x16x32_bf16 v[18:21], v[142:145], v[230:233], v[18:21]
	v_mfma_f32_16x16x32_bf16 v[22:25], v[146:149], v[230:233], v[22:25]
	v_mfma_f32_16x16x32_bf16 v[26:29], v[150:153], v[230:233], v[26:29]
	v_mfma_f32_16x16x32_bf16 v[30:33], v[154:157], v[230:233], v[30:33]
	v_lshl_add_u64 v[166:167], v[132:133], 0, s[38:39]
	global_load_dwordx2 v[214:215], v[166:167], off
	global_load_dwordx2 v[216:217], v[166:167], off offset:2048
	v_mfma_f32_16x16x32_bf16 v[2:5], v[142:145], v[234:237], v[2:5]
	v_mfma_f32_16x16x32_bf16 v[6:9], v[146:149], v[234:237], v[6:9]
	v_mfma_f32_16x16x32_bf16 v[10:13], v[150:153], v[234:237], v[10:13]
	v_mfma_f32_16x16x32_bf16 v[14:17], v[154:157], v[234:237], v[14:17]
	s_waitcnt vmcnt(21)
	s_waitcnt lgkmcnt(0)
	s_barrier
	s_mov_b32 s47, s42
	s_mov_b32 s42, s43
	s_mov_b32 s43, s44
	s_mov_b32 s44, s47
	v_mul_f32_e32 v98, s12, v98
	v_mul_f32_e32 v99, s12, v99
	v_mul_f32_e32 v100, s13, v100
	v_mul_f32_e32 v101, s13, v101
	v_mul_f32_e32 v102, s14, v102
	v_mul_f32_e32 v103, s14, v103
	v_mul_f32_e32 v104, s15, v104
	v_mul_f32_e32 v105, s15, v105
	v_mul_f32_e32 v106, s16, v106
	v_mul_f32_e32 v107, s16, v107
	v_mul_f32_e32 v108, s17, v108
	v_mul_f32_e32 v109, s17, v109
	v_mul_f32_e32 v110, s18, v110
	v_mul_f32_e32 v111, s18, v111
	v_mul_f32_e32 v112, s19, v112
	v_mul_f32_e32 v113, s19, v113
	v_cvt_pk_bf16_f32 v158, v98, v100
	v_cvt_pk_bf16_f32 v159, v102, v104
	v_cvt_pk_bf16_f32 v160, v106, v108
	v_cvt_pk_bf16_f32 v161, v110, v112
	v_cvt_pk_bf16_f32 v162, v99, v101
	v_cvt_pk_bf16_f32 v163, v103, v105
	v_cvt_pk_bf16_f32 v164, v107, v109
	v_cvt_pk_bf16_f32 v165, v111, v113
	ds_write_b128 v1, v[158:161] offset:0
	ds_write_b128 v1, v[162:165] offset:128
	v_add_u32_e32 v91, s42, v135
	v_add_u32_e32 v93, s42, v137
	ds_read_b128 v[238:241], v139 offset:19456
	ds_read_b128 v[242:245], v139 offset:21504
	ds_read_b128 v[246:249], v139 offset:23552
	ds_read_b128 v[250:253], v139 offset:25600
	ds_read_b128 v[218:221], v91 offset:0
	ds_read_b128 v[222:225], v91 offset:2048
	ds_read_b128 v[226:229], v91 offset:4096
	ds_read_b128 v[230:233], v91 offset:6144
	ds_read_b128 v[234:237], v91 offset:8192
	s_add_i32 s47, s44, s6
	s_add_u32 s30, s30, 0x80
	s_addc_u32 s31, s31, 0
	s_waitcnt lgkmcnt(0)
	v_mfma_f32_16x16x32_bf16 v[78:81], v[238:241], v[218:221], v[78:81]
	v_mfma_f32_16x16x32_bf16 v[74:77], v[242:245], v[218:221], v[74:77]
	v_mfma_f32_16x16x32_bf16 v[70:73], v[246:249], v[218:221], v[70:73]
	v_mfma_f32_16x16x32_bf16 v[66:69], v[250:253], v[218:221], v[66:69]
	ds_read_b128 v[218:221], v93 offset:0
	ds_read_b128 v[142:145], v141 offset:19456
	s_mov_b32 m0, s47
	s_nop 0
	global_load_lds_dwordx4 v86, s[30:31]
	v_mfma_f32_16x16x32_bf16 v[62:65], v[238:241], v[222:225], v[62:65]
	v_mfma_f32_16x16x32_bf16 v[58:61], v[242:245], v[222:225], v[58:61]
	v_mfma_f32_16x16x32_bf16 v[54:57], v[246:249], v[222:225], v[54:57]
	v_mfma_f32_16x16x32_bf16 v[50:53], v[250:253], v[222:225], v[50:53]
	ds_read_b128 v[222:225], v93 offset:2048
	ds_read_b128 v[146:149], v141 offset:21504
	s_add_i32 m0, s47, 0x2000
	s_nop 0
	global_load_lds_dwordx4 v134, s[30:31]
	v_mfma_f32_16x16x32_bf16 v[46:49], v[238:241], v[226:229], v[46:49]
	v_mfma_f32_16x16x32_bf16 v[42:45], v[242:245], v[226:229], v[42:45]
	v_mfma_f32_16x16x32_bf16 v[38:41], v[246:249], v[226:229], v[38:41]
	v_mfma_f32_16x16x32_bf16 v[34:37], v[250:253], v[226:229], v[34:37]
	ds_read_b128 v[226:229], v93 offset:4096
	ds_read_b128 v[150:153], v141 offset:23552
	s_add_i32 m0, s47, 0x4000
	s_nop 0
	global_load_lds_dwordx4 v136, s[30:31]
	v_mfma_f32_16x16x32_bf16 v[18:21], v[238:241], v[230:233], v[18:21]
	v_mfma_f32_16x16x32_bf16 v[22:25], v[242:245], v[230:233], v[22:25]
	v_mfma_f32_16x16x32_bf16 v[26:29], v[246:249], v[230:233], v[26:29]
	v_mfma_f32_16x16x32_bf16 v[30:33], v[250:253], v[230:233], v[30:33]
	ds_read_b128 v[230:233], v93 offset:6144
	ds_read_b128 v[154:157], v141 offset:25600
	s_add_i32 m0, s47, 0x6000
	s_nop 0
	global_load_lds_dwordx4 v138, s[30:31]
	v_mfma_f32_16x16x32_bf16 v[2:5], v[238:241], v[234:237], v[2:5]
	v_mfma_f32_16x16x32_bf16 v[6:9], v[242:245], v[234:237], v[6:9]
	v_mfma_f32_16x16x32_bf16 v[10:13], v[246:249], v[234:237], v[10:13]
	v_mfma_f32_16x16x32_bf16 v[14:17], v[250:253], v[234:237], v[14:17]
	ds_read_b128 v[234:237], v93 offset:8192
	s_add_i32 m0, s47, 0x8000
	s_nop 0
	global_load_lds_dwordx4 v140, s[30:31]
	s_waitcnt lgkmcnt(0)
; #define MU_GLDS_A(buf, kt) do { _Pragma("unroll") for (int i = 0; i < NMU; ++i) \
;         __builtin_amdgcn_global_load_lds((const unsigned*)((const char*)A + aoff[i] + (size_t)(kt) * 128), (PG8_LAS unsigned*)(MU_SA(buf) + wid * 1024 + i * 8192), 16, 0, 0); } while (0)
; #define MU_B_ISSUE(sb, kt) do { const char* kb_ = Bb + (size_t)(kt) * (64 * (size_t)RB); _Pragma("unroll") for (int j = 0; j < 8; ++j) { const char* p_ = kb_ + (size_t)j * RB; \
;         asm volatile("global_load_dwordx2 %0, %1, off" : "=&v"(sb[j]) : "v"(p_) : "memory"); } } while (0)
; #define MU_B_WAIT(sb, N) asm volatile("s_waitcnt vmcnt(%8)" : "+v"(sb[0]), "+v"(sb[1]), "+v"(sb[2]), "+v"(sb[3]), "+v"(sb[4]), "+v"(sb[5]), "+v"(sb[6]), "+v"(sb[7]) : "n"(N) : "memory")
; #define MU_G_LOAD(ga, kt) do { const PG8_LAS f32x4* gk_ = (const PG8_LAS f32x4*)(lds + GAIN_OFF) + 16 * (kt) + 2 * wid; const f32x4 ga_ = gk_[0], gb_ = gk_[1]; \
;         ga[0] = ga_[0]; ga[1] = ga_[1]; ga[2] = ga_[2]; ga[3] = ga_[3]; ga[4] = gb_[0]; ga[5] = gb_[1]; ga[6] = gb_[2]; ga[7] = gb_[3]; } while (0)
; #define MU_COMPUTE(buf) MU_COMPUTE_N(buf, NMU)
; #define MU_END(last) do { if (last) asm volatile("s_waitcnt vmcnt(0)" ::: "memory"); else asm volatile("s_waitcnt vmcnt(8)" ::: "memory"); \
;         asm volatile("s_waitcnt lgkmcnt(0)" ::: "memory"); __builtin_amdgcn_s_barrier(); asm volatile("" ::: "memory"); } while (0)
; template <int MODE>
; __device__ __forceinline__ void moe_unit(PG8_LAS unsigned char* lds, int e, int cb, int slot0  , int nv  , const bf16_t* A, const int* slot_tok,
;                                          const float* W0, const float* W1, bf16_t* OUT, const float* slot_rs  , const int* slot_dst) {
;     ...
;     for (int t = 0; t < nt; t += 2) {
;         if (t + 2 < nt) MU_B_WAIT(s1, 8); else MU_B_WAIT(s1, 0);
;         MU_G_LOAD(g0, t + 1); MU_B_WRITE(s1, 1, g0); __builtin_amdgcn_sched_barrier(0); MU_GLDS_A(1, t + 1); __builtin_amdgcn_sched_barrier(0);
;         if (t + 3 < nt) { MU_B_ISSUE(s1, t + 3); }
;         MU_COMPUTE(0);
;         MU_END(t + 3 >= nt);
;         if (t + 2 < nt) { MU_B_WAIT(s0, 8); MU_G_LOAD(g0, t + 2); MU_B_WRITE(s0, 0, g0); __builtin_amdgcn_sched_barrier(0); MU_GLDS_A(0, t + 2); __builtin_amdgcn_sched_barrier(0); }
;         if (t + 4 < nt) { MU_B_ISSUE(s0, t + 4); }
;         MU_COMPUTE(1);
;         MU_END(t + 4 >= nt);
	s_load_dwordx8 s[20:27], s[28:29], 0x0
	s_add_u32 s28, s28, 0x100
	s_addc_u32 s29, s29, 0
	v_mfma_f32_16x16x32_bf16 v[78:81], v[142:145], v[218:221], v[78:81]
	v_mfma_f32_16x16x32_bf16 v[74:77], v[146:149], v[218:221], v[74:77]
	v_mfma_f32_16x16x32_bf16 v[70:73], v[150:153], v[218:221], v[70:73]
	v_mfma_f32_16x16x32_bf16 v[66:69], v[154:157], v[218:221], v[66:69]
	v_lshl_add_u64 v[132:133], v[132:133], 0, s[40:41]
	global_load_dwordx2 v[98:99], v[132:133], off
	global_load_dwordx2 v[100:101], v[132:133], off offset:2048
	v_mfma_f32_16x16x32_bf16 v[62:65], v[142:145], v[222:225], v[62:65]
	v_mfma_f32_16x16x32_bf16 v[58:61], v[146:149], v[222:225], v[58:61]
	v_mfma_f32_16x16x32_bf16 v[54:57], v[150:153], v[222:225], v[54:57]
	v_mfma_f32_16x16x32_bf16 v[50:53], v[154:157], v[222:225], v[50:53]
	v_lshl_add_u64 v[166:167], v[132:133], 0, s[34:35]
	global_load_dwordx2 v[102:103], v[166:167], off
	global_load_dwordx2 v[104:105], v[166:167], off offset:2048
	v_mfma_f32_16x16x32_bf16 v[46:49], v[142:145], v[226:229], v[46:49]
	v_mfma_f32_16x16x32_bf16 v[42:45], v[146:149], v[226:229], v[42:45]
	v_mfma_f32_16x16x32_bf16 v[38:41], v[150:153], v[226:229], v[38:41]
	v_mfma_f32_16x16x32_bf16 v[34:37], v[154:157], v[226:229], v[34:37]
	v_lshl_add_u64 v[166:167], v[132:133], 0, s[36:37]
	global_load_dwordx2 v[106:107], v[166:167], off
	global_load_dwordx2 v[108:109], v[166:167], off offset:2048
	v_mfma_f32_16x16x32_bf16 v[18:21], v[142:145], v[230:233], v[18:21]
	v_mfma_f32_16x16x32_bf16 v[22:25], v[146:149], v[230:233], v[22:25]
	v_mfma_f32_16x16x32_bf16 v[26:29], v[150:153], v[230:233], v[26:29]
	v_mfma_f32_16x16x32_bf16 v[30:33], v[154:157], v[230:233], v[30:33]
	v_lshl_add_u64 v[166:167], v[132:133], 0, s[38:39]
	global_load_dwordx2 v[110:111], v[166:167], off
	global_load_dwordx2 v[112:113], v[166:167], off offset:2048
	v_mfma_f32_16x16x32_bf16 v[2:5], v[142:145], v[234:237], v[2:5]
	v_mfma_f32_16x16x32_bf16 v[6:9], v[146:149], v[234:237], v[6:9]
	v_mfma_f32_16x16x32_bf16 v[10:13], v[150:153], v[234:237], v[10:13]
	v_mfma_f32_16x16x32_bf16 v[14:17], v[154:157], v[234:237], v[14:17]
	s_waitcnt vmcnt(21)
	s_waitcnt lgkmcnt(0)
	s_barrier
	s_mov_b32 s47, s42
	s_mov_b32 s42, s43
	s_mov_b32 s43, s44
	s_mov_b32 s44, s47
	s_mov_b32 s46, 13
.Lmu_loop:
	v_mul_f32_e32 v114, s20, v114
	v_mul_f32_e32 v115, s20, v115
	v_mul_f32_e32 v116, s21, v116
	v_mul_f32_e32 v117, s21, v117
	v_mul_f32_e32 v118, s22, v118
	v_mul_f32_e32 v119, s22, v119
	v_mul_f32_e32 v120, s23, v120
	v_mul_f32_e32 v121, s23, v121
	v_mul_f32_e32 v122, s24, v122
	v_mul_f32_e32 v123, s24, v123
	v_mul_f32_e32 v124, s25, v124
	v_mul_f32_e32 v125, s25, v125
	v_mul_f32_e32 v126, s26, v126
	v_mul_f32_e32 v127, s26, v127
	v_mul_f32_e32 v128, s27, v128
	v_mul_f32_e32 v129, s27, v129
	v_cvt_pk_bf16_f32 v158, v114, v116
	v_cvt_pk_bf16_f32 v159, v118, v120
	v_cvt_pk_bf16_f32 v160, v122, v124
	v_cvt_pk_bf16_f32 v161, v126, v128
	v_cvt_pk_bf16_f32 v162, v115, v117
	v_cvt_pk_bf16_f32 v163, v119, v121
	v_cvt_pk_bf16_f32 v164, v123, v125
	v_cvt_pk_bf16_f32 v165, v127, v129
	ds_write_b128 v1, v[158:161] offset:19456
	ds_write_b128 v1, v[162:165] offset:19584
	v_add_u32_e32 v91, s42, v135
	v_add_u32_e32 v93, s42, v137
	ds_read_b128 v[238:241], v139 offset:0
	ds_read_b128 v[242:245], v139 offset:2048
	ds_read_b128 v[246:249], v139 offset:4096
	ds_read_b128 v[250:253], v139 offset:6144
	ds_read_b128 v[218:221], v91 offset:0
	ds_read_b128 v[222:225], v91 offset:2048
	ds_read_b128 v[226:229], v91 offset:4096
	ds_read_b128 v[230:233], v91 offset:6144
	ds_read_b128 v[234:237], v91 offset:8192
	s_add_i32 s47, s44, s6
	s_add_u32 s30, s30, 0x80
	s_addc_u32 s31, s31, 0
	s_waitcnt lgkmcnt(0)
	v_mfma_f32_16x16x32_bf16 v[78:81], v[238:241], v[218:221], v[78:81]
	v_mfma_f32_16x16x32_bf16 v[74:77], v[242:245], v[218:221], v[74:77]
	v_mfma_f32_16x16x32_bf16 v[70:73], v[246:249], v[218:221], v[70:73]
	v_mfma_f32_16x16x32_bf16 v[66:69], v[250:253], v[218:221], v[66:69]
	ds_read_b128 v[218:221], v93 offset:0
	ds_read_b128 v[142:145], v141 offset:0
	s_mov_b32 m0, s47
	s_nop 0
	global_load_lds_dwordx4 v86, s[30:31]
	v_mfma_f32_16x16x32_bf16 v[62:65], v[238:241], v[222:225], v[62:65]
	v_mfma_f32_16x16x32_bf16 v[58:61], v[242:245], v[222:225], v[58:61]
	v_mfma_f32_16x16x32_bf16 v[54:57], v[246:249], v[222:225], v[54:57]
	v_mfma_f32_16x16x32_bf16 v[50:53], v[250:253], v[222:225], v[50:53]
	ds_read_b128 v[222:225], v93 offset:2048
	ds_read_b128 v[146:149], v141 offset:2048
	s_add_i32 m0, s47, 0x2000
	s_nop 0
	global_load_lds_dwordx4 v134, s[30:31]
	v_mfma_f32_16x16x32_bf16 v[46:49], v[238:241], v[226:229], v[46:49]
	v_mfma_f32_16x16x32_bf16 v[42:45], v[242:245], v[226:229], v[42:45]
	v_mfma_f32_16x16x32_bf16 v[38:41], v[246:249], v[226:229], v[38:41]
	v_mfma_f32_16x16x32_bf16 v[34:37], v[250:253], v[226:229], v[34:37]
	ds_read_b128 v[226:229], v93 offset:4096
	ds_read_b128 v[150:153], v141 offset:4096
	s_add_i32 m0, s47, 0x4000
	s_nop 0
	global_load_lds_dwordx4 v136, s[30:31]
	v_mfma_f32_16x16x32_bf16 v[18:21], v[238:241], v[230:233], v[18:21]
	v_mfma_f32_16x16x32_bf16 v[22:25], v[242:245], v[230:233], v[22:25]
	v_mfma_f32_16x16x32_bf16 v[26:29], v[246:249], v[230:233], v[26:29]
	v_mfma_f32_16x16x32_bf16 v[30:33], v[250:253], v[230:233], v[30:33]
	ds_read_b128 v[230:233], v93 offset:6144
	ds_read_b128 v[154:157], v141 offset:6144
	s_add_i32 m0, s47, 0x6000
	s_nop 0
	global_load_lds_dwordx4 v138, s[30:31]
	v_mfma_f32_16x16x32_bf16 v[2:5], v[238:241], v[234:237], v[2:5]
	v_mfma_f32_16x16x32_bf16 v[6:9], v[242:245], v[234:237], v[6:9]
	v_mfma_f32_16x16x32_bf16 v[10:13], v[246:249], v[234:237], v[10:13]
	v_mfma_f32_16x16x32_bf16 v[14:17], v[250:253], v[234:237], v[14:17]
	ds_read_b128 v[234:237], v93 offset:8192
	s_add_i32 m0, s47, 0x8000
	s_nop 0
	global_load_lds_dwordx4 v140, s[30:31]
	s_waitcnt lgkmcnt(0)
; #define MU_GLDS_A(buf, kt) do { _Pragma("unroll") for (int i = 0; i < NMU; ++i) \
;         __builtin_amdgcn_global_load_lds((const unsigned*)((const char*)A + aoff[i] + (size_t)(kt) * 128), (PG8_LAS unsigned*)(MU_SA(buf) + wid * 1024 + i * 8192), 16, 0, 0); } while (0)
; #define MU_B_ISSUE(sb, kt) do { const char* kb_ = Bb + (size_t)(kt) * (64 * (size_t)RB); _Pragma("unroll") for (int j = 0; j < 8; ++j) { const char* p_ = kb_ + (size_t)j * RB; \
;         asm volatile("global_load_dwordx2 %0, %1, off" : "=&v"(sb[j]) : "v"(p_) : "memory"); } } while (0)
; #define MU_B_WAIT(sb, N) asm volatile("s_waitcnt vmcnt(%8)" : "+v"(sb[0]), "+v"(sb[1]), "+v"(sb[2]), "+v"(sb[3]), "+v"(sb[4]), "+v"(sb[5]), "+v"(sb[6]), "+v"(sb[7]) : "n"(N) : "memory")
; #define MU_G_LOAD(ga, kt) do { const PG8_LAS f32x4* gk_ = (const PG8_LAS f32x4*)(lds + GAIN_OFF) + 16 * (kt) + 2 * wid; const f32x4 ga_ = gk_[0], gb_ = gk_[1]; \
;         ga[0] = ga_[0]; ga[1] = ga_[1]; ga[2] = ga_[2]; ga[3] = ga_[3]; ga[4] = gb_[0]; ga[5] = gb_[1]; ga[6] = gb_[2]; ga[7] = gb_[3]; } while (0)
; #define MU_COMPUTE(buf) MU_COMPUTE_N(buf, NMU)
; #define MU_END(last) do { if (last) asm volatile("s_waitcnt vmcnt(0)" ::: "memory"); else asm volatile("s_waitcnt vmcnt(8)" ::: "memory"); \
;         asm volatile("s_waitcnt lgkmcnt(0)" ::: "memory"); __builtin_amdgcn_s_barrier(); asm volatile("" ::: "memory"); } while (0)
; template <int MODE>
; __device__ __forceinline__ void moe_unit(PG8_LAS unsigned char* lds, int e, int cb, int slot0  , int nv  , const bf16_t* A, const int* slot_tok,
;                                          const float* W0, const float* W1, bf16_t* OUT, const float* slot_rs  , const int* slot_dst) {
;     ...
;         if (t + 2 < nt) MU_B_WAIT(s1, 8); else MU_B_WAIT(s1, 0);
;         MU_G_LOAD(g0, t + 1); MU_B_WRITE(s1, 1, g0); __builtin_amdgcn_sched_barrier(0); MU_GLDS_A(1, t + 1); __builtin_amdgcn_sched_barrier(0);
;         if (t + 3 < nt) { MU_B_ISSUE(s1, t + 3); }
;         MU_COMPUTE(0);
;         MU_END(t + 3 >= nt);
;         if (t + 2 < nt) { MU_B_WAIT(s0, 8); MU_G_LOAD(g0, t + 2); MU_B_WRITE(s0, 0, g0); __builtin_amdgcn_sched_barrier(0); MU_GLDS_A(0, t + 2); __builtin_amdgcn_sched_barrier(0); }
;         if (t + 4 < nt) { MU_B_ISSUE(s0, t + 4); }
;         MU_COMPUTE(1);
;         MU_END(t + 4 >= nt);
	s_load_dwordx8 s[12:19], s[28:29], 0x0
	s_add_u32 s28, s28, 0x100
	s_addc_u32 s29, s29, 0
	v_mfma_f32_16x16x32_bf16 v[78:81], v[142:145], v[218:221], v[78:81]
	v_mfma_f32_16x16x32_bf16 v[74:77], v[146:149], v[218:221], v[74:77]
	v_mfma_f32_16x16x32_bf16 v[70:73], v[150:153], v[218:221], v[70:73]
	v_mfma_f32_16x16x32_bf16 v[66:69], v[154:157], v[218:221], v[66:69]
	v_lshl_add_u64 v[132:133], v[132:133], 0, s[40:41]
	global_load_dwordx2 v[114:115], v[132:133], off
	global_load_dwordx2 v[116:117], v[132:133], off offset:2048
	v_mfma_f32_16x16x32_bf16 v[62:65], v[142:145], v[222:225], v[62:65]
	v_mfma_f32_16x16x32_bf16 v[58:61], v[146:149], v[222:225], v[58:61]
	v_mfma_f32_16x16x32_bf16 v[54:57], v[150:153], v[222:225], v[54:57]
	v_mfma_f32_16x16x32_bf16 v[50:53], v[154:157], v[222:225], v[50:53]
	v_lshl_add_u64 v[166:167], v[132:133], 0, s[34:35]
	global_load_dwordx2 v[118:119], v[166:167], off
	global_load_dwordx2 v[120:121], v[166:167], off offset:2048
	v_mfma_f32_16x16x32_bf16 v[46:49], v[142:145], v[226:229], v[46:49]
	v_mfma_f32_16x16x32_bf16 v[42:45], v[146:149], v[226:229], v[42:45]
	v_mfma_f32_16x16x32_bf16 v[38:41], v[150:153], v[226:229], v[38:41]
	v_mfma_f32_16x16x32_bf16 v[34:37], v[154:157], v[226:229], v[34:37]
	v_lshl_add_u64 v[166:167], v[132:133], 0, s[36:37]
	global_load_dwordx2 v[122:123], v[166:167], off
	global_load_dwordx2 v[124:125], v[166:167], off offset:2048
	v_mfma_f32_16x16x32_bf16 v[18:21], v[142:145], v[230:233], v[18:21]
	v_mfma_f32_16x16x32_bf16 v[22:25], v[146:149], v[230:233], v[22:25]
	v_mfma_f32_16x16x32_bf16 v[26:29], v[150:153], v[230:233], v[26:29]
	v_mfma_f32_16x16x32_bf16 v[30:33], v[154:157], v[230:233], v[30:33]
	v_lshl_add_u64 v[166:167], v[132:133], 0, s[38:39]
	global_load_dwordx2 v[126:127], v[166:167], off
	global_load_dwordx2 v[128:129], v[166:167], off offset:2048
	v_mfma_f32_16x16x32_bf16 v[2:5], v[142:145], v[234:237], v[2:5]
	v_mfma_f32_16x16x32_bf16 v[6:9], v[146:149], v[234:237], v[6:9]
	v_mfma_f32_16x16x32_bf16 v[10:13], v[150:153], v[234:237], v[10:13]
	v_mfma_f32_16x16x32_bf16 v[14:17], v[154:157], v[234:237], v[14:17]
	s_waitcnt vmcnt(21)
	s_waitcnt lgkmcnt(0)
	s_barrier
	s_mov_b32 s47, s42
	s_mov_b32 s42, s43
	s_mov_b32 s43, s44
	s_mov_b32 s44, s47
	v_mul_f32_e32 v186, s12, v186
	v_mul_f32_e32 v187, s12, v187
	v_mul_f32_e32 v188, s13, v188
	v_mul_f32_e32 v189, s13, v189
	v_mul_f32_e32 v190, s14, v190
	v_mul_f32_e32 v191, s14, v191
	v_mul_f32_e32 v192, s15, v192
	v_mul_f32_e32 v193, s15, v193
	v_mul_f32_e32 v194, s16, v194
	v_mul_f32_e32 v195, s16, v195
	v_mul_f32_e32 v196, s17, v196
	v_mul_f32_e32 v197, s17, v197
	v_mul_f32_e32 v198, s18, v198
	v_mul_f32_e32 v199, s18, v199
	v_mul_f32_e32 v200, s19, v200
	v_mul_f32_e32 v201, s19, v201
	v_cvt_pk_bf16_f32 v158, v186, v188
	v_cvt_pk_bf16_f32 v159, v190, v192
	v_cvt_pk_bf16_f32 v160, v194, v196
	v_cvt_pk_bf16_f32 v161, v198, v200
	v_cvt_pk_bf16_f32 v162, v187, v189
	v_cvt_pk_bf16_f32 v163, v191, v193
	v_cvt_pk_bf16_f32 v164, v195, v197
	v_cvt_pk_bf16_f32 v165, v199, v201
	ds_write_b128 v1, v[158:161] offset:0
	ds_write_b128 v1, v[162:165] offset:128
	v_add_u32_e32 v91, s42, v135
	v_add_u32_e32 v93, s42, v137
	ds_read_b128 v[238:241], v139 offset:19456
	ds_read_b128 v[242:245], v139 offset:21504
	ds_read_b128 v[246:249], v139 offset:23552
	ds_read_b128 v[250:253], v139 offset:25600
	ds_read_b128 v[218:221], v91 offset:0
	ds_read_b128 v[222:225], v91 offset:2048
	ds_read_b128 v[226:229], v91 offset:4096
	ds_read_b128 v[230:233], v91 offset:6144
	ds_read_b128 v[234:237], v91 offset:8192
	s_add_i32 s47, s44, s6
	s_add_u32 s30, s30, 0x80
	s_addc_u32 s31, s31, 0
	s_waitcnt lgkmcnt(0)
	v_mfma_f32_16x16x32_bf16 v[78:81], v[238:241], v[218:221], v[78:81]
	v_mfma_f32_16x16x32_bf16 v[74:77], v[242:245], v[218:221], v[74:77]
	v_mfma_f32_16x16x32_bf16 v[70:73], v[246:249], v[218:221], v[70:73]
	v_mfma_f32_16x16x32_bf16 v[66:69], v[250:253], v[218:221], v[66:69]
	ds_read_b128 v[218:221], v93 offset:0
	ds_read_b128 v[142:145], v141 offset:19456
	s_mov_b32 m0, s47
	s_nop 0
	global_load_lds_dwordx4 v86, s[30:31]
	v_mfma_f32_16x16x32_bf16 v[62:65], v[238:241], v[222:225], v[62:65]
	v_mfma_f32_16x16x32_bf16 v[58:61], v[242:245], v[222:225], v[58:61]
	v_mfma_f32_16x16x32_bf16 v[54:57], v[246:249], v[222:225], v[54:57]
	v_mfma_f32_16x16x32_bf16 v[50:53], v[250:253], v[222:225], v[50:53]
	ds_read_b128 v[222:225], v93 offset:2048
	ds_read_b128 v[146:149], v141 offset:21504
	s_add_i32 m0, s47, 0x2000
	s_nop 0
	global_load_lds_dwordx4 v134, s[30:31]
	v_mfma_f32_16x16x32_bf16 v[46:49], v[238:241], v[226:229], v[46:49]
	v_mfma_f32_16x16x32_bf16 v[42:45], v[242:245], v[226:229], v[42:45]
	v_mfma_f32_16x16x32_bf16 v[38:41], v[246:249], v[226:229], v[38:41]
	v_mfma_f32_16x16x32_bf16 v[34:37], v[250:253], v[226:229], v[34:37]
	ds_read_b128 v[226:229], v93 offset:4096
	ds_read_b128 v[150:153], v141 offset:23552
	s_add_i32 m0, s47, 0x4000
	s_nop 0
	global_load_lds_dwordx4 v136, s[30:31]
	v_mfma_f32_16x16x32_bf16 v[18:21], v[238:241], v[230:233], v[18:21]
	v_mfma_f32_16x16x32_bf16 v[22:25], v[242:245], v[230:233], v[22:25]
	v_mfma_f32_16x16x32_bf16 v[26:29], v[246:249], v[230:233], v[26:29]
	v_mfma_f32_16x16x32_bf16 v[30:33], v[250:253], v[230:233], v[30:33]
	ds_read_b128 v[230:233], v93 offset:6144
	ds_read_b128 v[154:157], v141 offset:25600
	s_add_i32 m0, s47, 0x6000
	s_nop 0
	global_load_lds_dwordx4 v138, s[30:31]
	v_mfma_f32_16x16x32_bf16 v[2:5], v[238:241], v[234:237], v[2:5]
	v_mfma_f32_16x16x32_bf16 v[6:9], v[242:245], v[234:237], v[6:9]
	v_mfma_f32_16x16x32_bf16 v[10:13], v[246:249], v[234:237], v[10:13]
	v_mfma_f32_16x16x32_bf16 v[14:17], v[250:253], v[234:237], v[14:17]
	ds_read_b128 v[234:237], v93 offset:8192
	s_add_i32 m0, s47, 0x8000
	s_nop 0
	global_load_lds_dwordx4 v140, s[30:31]
	s_waitcnt lgkmcnt(0)
; #define MU_GLDS_A(buf, kt) do { _Pragma("unroll") for (int i = 0; i < NMU; ++i) \
;         __builtin_amdgcn_global_load_lds((const unsigned*)((const char*)A + aoff[i] + (size_t)(kt) * 128), (PG8_LAS unsigned*)(MU_SA(buf) + wid * 1024 + i * 8192), 16, 0, 0); } while (0)
; #define MU_B_ISSUE(sb, kt) do { const char* kb_ = Bb + (size_t)(kt) * (64 * (size_t)RB); _Pragma("unroll") for (int j = 0; j < 8; ++j) { const char* p_ = kb_ + (size_t)j * RB; \
;         asm volatile("global_load_dwordx2 %0, %1, off" : "=&v"(sb[j]) : "v"(p_) : "memory"); } } while (0)
; #define MU_B_WAIT(sb, N) asm volatile("s_waitcnt vmcnt(%8)" : "+v"(sb[0]), "+v"(sb[1]), "+v"(sb[2]), "+v"(sb[3]), "+v"(sb[4]), "+v"(sb[5]), "+v"(sb[6]), "+v"(sb[7]) : "n"(N) : "memory")
; #define MU_G_LOAD(ga, kt) do { const PG8_LAS f32x4* gk_ = (const PG8_LAS f32x4*)(lds + GAIN_OFF) + 16 * (kt) + 2 * wid; const f32x4 ga_ = gk_[0], gb_ = gk_[1]; \
;         ga[0] = ga_[0]; ga[1] = ga_[1]; ga[2] = ga_[2]; ga[3] = ga_[3]; ga[4] = gb_[0]; ga[5] = gb_[1]; ga[6] = gb_[2]; ga[7] = gb_[3]; } while (0)
; #define MU_COMPUTE(buf) MU_COMPUTE_N(buf, NMU)
; #define MU_END(last) do { if (last) asm volatile("s_waitcnt vmcnt(0)" ::: "memory"); else asm volatile("s_waitcnt vmcnt(8)" ::: "memory"); \
;         asm volatile("s_waitcnt lgkmcnt(0)" ::: "memory"); __builtin_amdgcn_s_barrier(); asm volatile("" ::: "memory"); } while (0)
; template <int MODE>
; __device__ __forceinline__ void moe_unit(PG8_LAS unsigned char* lds, int e, int cb, int slot0  , int nv  , const bf16_t* A, const int* slot_tok,
;                                          const float* W0, const float* W1, bf16_t* OUT, const float* slot_rs  , const int* slot_dst) {
;     ...
;         if (t + 2 < nt) MU_B_WAIT(s1, 8); else MU_B_WAIT(s1, 0);
;         MU_G_LOAD(g0, t + 1); MU_B_WRITE(s1, 1, g0); __builtin_amdgcn_sched_barrier(0); MU_GLDS_A(1, t + 1); __builtin_amdgcn_sched_barrier(0);
;         if (t + 3 < nt) { MU_B_ISSUE(s1, t + 3); }
;         MU_COMPUTE(0);
;         MU_END(t + 3 >= nt);
;         if (t + 2 < nt) { MU_B_WAIT(s0, 8); MU_G_LOAD(g0, t + 2); MU_B_WRITE(s0, 0, g0); __builtin_amdgcn_sched_barrier(0); MU_GLDS_A(0, t + 2); __builtin_amdgcn_sched_barrier(0); }
;         if (t + 4 < nt) { MU_B_ISSUE(s0, t + 4); }
;         MU_COMPUTE(1);
;         MU_END(t + 4 >= nt);
	s_load_dwordx8 s[20:27], s[28:29], 0x0
	s_add_u32 s28, s28, 0x100
	s_addc_u32 s29, s29, 0
	v_mfma_f32_16x16x32_bf16 v[78:81], v[142:145], v[218:221], v[78:81]
	v_mfma_f32_16x16x32_bf16 v[74:77], v[146:149], v[218:221], v[74:77]
	v_mfma_f32_16x16x32_bf16 v[70:73], v[150:153], v[218:221], v[70:73]
	v_mfma_f32_16x16x32_bf16 v[66:69], v[154:157], v[218:221], v[66:69]
	v_lshl_add_u64 v[132:133], v[132:133], 0, s[40:41]
	global_load_dwordx2 v[186:187], v[132:133], off
	global_load_dwordx2 v[188:189], v[132:133], off offset:2048
	v_mfma_f32_16x16x32_bf16 v[62:65], v[142:145], v[222:225], v[62:65]
	v_mfma_f32_16x16x32_bf16 v[58:61], v[146:149], v[222:225], v[58:61]
	v_mfma_f32_16x16x32_bf16 v[54:57], v[150:153], v[222:225], v[54:57]
	v_mfma_f32_16x16x32_bf16 v[50:53], v[154:157], v[222:225], v[50:53]
	v_lshl_add_u64 v[166:167], v[132:133], 0, s[34:35]
	global_load_dwordx2 v[190:191], v[166:167], off
	global_load_dwordx2 v[192:193], v[166:167], off offset:2048
	v_mfma_f32_16x16x32_bf16 v[46:49], v[142:145], v[226:229], v[46:49]
	v_mfma_f32_16x16x32_bf16 v[42:45], v[146:149], v[226:229], v[42:45]
	v_mfma_f32_16x16x32_bf16 v[38:41], v[150:153], v[226:229], v[38:41]
	v_mfma_f32_16x16x32_bf16 v[34:37], v[154:157], v[226:229], v[34:37]
	v_lshl_add_u64 v[166:167], v[132:133], 0, s[36:37]
	global_load_dwordx2 v[194:195], v[166:167], off
	global_load_dwordx2 v[196:197], v[166:167], off offset:2048
	v_mfma_f32_16x16x32_bf16 v[18:21], v[142:145], v[230:233], v[18:21]
	v_mfma_f32_16x16x32_bf16 v[22:25], v[146:149], v[230:233], v[22:25]
	v_mfma_f32_16x16x32_bf16 v[26:29], v[150:153], v[230:233], v[26:29]
	v_mfma_f32_16x16x32_bf16 v[30:33], v[154:157], v[230:233], v[30:33]
	v_lshl_add_u64 v[166:167], v[132:133], 0, s[38:39]
	global_load_dwordx2 v[198:199], v[166:167], off
	global_load_dwordx2 v[200:201], v[166:167], off offset:2048
	v_mfma_f32_16x16x32_bf16 v[2:5], v[142:145], v[234:237], v[2:5]
	v_mfma_f32_16x16x32_bf16 v[6:9], v[146:149], v[234:237], v[6:9]
	v_mfma_f32_16x16x32_bf16 v[10:13], v[150:153], v[234:237], v[10:13]
	v_mfma_f32_16x16x32_bf16 v[14:17], v[154:157], v[234:237], v[14:17]
	s_waitcnt vmcnt(21)
	s_waitcnt lgkmcnt(0)
	s_barrier
	s_mov_b32 s47, s42
	s_mov_b32 s42, s43
	s_mov_b32 s43, s44
	s_mov_b32 s44, s47
	v_mul_f32_e32 v202, s20, v202
	v_mul_f32_e32 v203, s20, v203
	v_mul_f32_e32 v204, s21, v204
	v_mul_f32_e32 v205, s21, v205
	v_mul_f32_e32 v206, s22, v206
	v_mul_f32_e32 v207, s22, v207
	v_mul_f32_e32 v208, s23, v208
	v_mul_f32_e32 v209, s23, v209
	v_mul_f32_e32 v210, s24, v210
	v_mul_f32_e32 v211, s24, v211
	v_mul_f32_e32 v212, s25, v212
	v_mul_f32_e32 v213, s25, v213
	v_mul_f32_e32 v214, s26, v214
	v_mul_f32_e32 v215, s26, v215
	v_mul_f32_e32 v216, s27, v216
	v_mul_f32_e32 v217, s27, v217
	v_cvt_pk_bf16_f32 v158, v202, v204
	v_cvt_pk_bf16_f32 v159, v206, v208
	v_cvt_pk_bf16_f32 v160, v210, v212
	v_cvt_pk_bf16_f32 v161, v214, v216
	v_cvt_pk_bf16_f32 v162, v203, v205
	v_cvt_pk_bf16_f32 v163, v207, v209
	v_cvt_pk_bf16_f32 v164, v211, v213
	v_cvt_pk_bf16_f32 v165, v215, v217
	ds_write_b128 v1, v[158:161] offset:19456
	ds_write_b128 v1, v[162:165] offset:19584
	v_add_u32_e32 v91, s42, v135
	v_add_u32_e32 v93, s42, v137
	ds_read_b128 v[238:241], v139 offset:0
	ds_read_b128 v[242:245], v139 offset:2048
	ds_read_b128 v[246:249], v139 offset:4096
	ds_read_b128 v[250:253], v139 offset:6144
	ds_read_b128 v[218:221], v91 offset:0
	ds_read_b128 v[222:225], v91 offset:2048
	ds_read_b128 v[226:229], v91 offset:4096
	ds_read_b128 v[230:233], v91 offset:6144
	ds_read_b128 v[234:237], v91 offset:8192
	s_add_i32 s47, s44, s6
	s_add_u32 s30, s30, 0x80
	s_addc_u32 s31, s31, 0
	s_waitcnt lgkmcnt(0)
	v_mfma_f32_16x16x32_bf16 v[78:81], v[238:241], v[218:221], v[78:81]
	v_mfma_f32_16x16x32_bf16 v[74:77], v[242:245], v[218:221], v[74:77]
	v_mfma_f32_16x16x32_bf16 v[70:73], v[246:249], v[218:221], v[70:73]
	v_mfma_f32_16x16x32_bf16 v[66:69], v[250:253], v[218:221], v[66:69]
	ds_read_b128 v[218:221], v93 offset:0
	ds_read_b128 v[142:145], v141 offset:0
	s_mov_b32 m0, s47
	s_nop 0
	global_load_lds_dwordx4 v86, s[30:31]
	v_mfma_f32_16x16x32_bf16 v[62:65], v[238:241], v[222:225], v[62:65]
	v_mfma_f32_16x16x32_bf16 v[58:61], v[242:245], v[222:225], v[58:61]
	v_mfma_f32_16x16x32_bf16 v[54:57], v[246:249], v[222:225], v[54:57]
	v_mfma_f32_16x16x32_bf16 v[50:53], v[250:253], v[222:225], v[50:53]
	ds_read_b128 v[222:225], v93 offset:2048
	ds_read_b128 v[146:149], v141 offset:2048
	s_add_i32 m0, s47, 0x2000
	s_nop 0
	global_load_lds_dwordx4 v134, s[30:31]
	v_mfma_f32_16x16x32_bf16 v[46:49], v[238:241], v[226:229], v[46:49]
	v_mfma_f32_16x16x32_bf16 v[42:45], v[242:245], v[226:229], v[42:45]
	v_mfma_f32_16x16x32_bf16 v[38:41], v[246:249], v[226:229], v[38:41]
	v_mfma_f32_16x16x32_bf16 v[34:37], v[250:253], v[226:229], v[34:37]
	ds_read_b128 v[226:229], v93 offset:4096
	ds_read_b128 v[150:153], v141 offset:4096
	s_add_i32 m0, s47, 0x4000
	s_nop 0
	global_load_lds_dwordx4 v136, s[30:31]
	v_mfma_f32_16x16x32_bf16 v[18:21], v[238:241], v[230:233], v[18:21]
	v_mfma_f32_16x16x32_bf16 v[22:25], v[242:245], v[230:233], v[22:25]
	v_mfma_f32_16x16x32_bf16 v[26:29], v[246:249], v[230:233], v[26:29]
	v_mfma_f32_16x16x32_bf16 v[30:33], v[250:253], v[230:233], v[30:33]
	ds_read_b128 v[230:233], v93 offset:6144
	ds_read_b128 v[154:157], v141 offset:6144
	s_add_i32 m0, s47, 0x6000
	s_nop 0
	global_load_lds_dwordx4 v138, s[30:31]
	v_mfma_f32_16x16x32_bf16 v[2:5], v[238:241], v[234:237], v[2:5]
	v_mfma_f32_16x16x32_bf16 v[6:9], v[242:245], v[234:237], v[6:9]
	v_mfma_f32_16x16x32_bf16 v[10:13], v[246:249], v[234:237], v[10:13]
	v_mfma_f32_16x16x32_bf16 v[14:17], v[250:253], v[234:237], v[14:17]
	ds_read_b128 v[234:237], v93 offset:8192
	s_add_i32 m0, s47, 0x8000
	s_nop 0
	global_load_lds_dwordx4 v140, s[30:31]
	s_waitcnt lgkmcnt(0)
; #define MU_GLDS_A(buf, kt) do { _Pragma("unroll") for (int i = 0; i < NMU; ++i) \
;         __builtin_amdgcn_global_load_lds((const unsigned*)((const char*)A + aoff[i] + (size_t)(kt) * 128), (PG8_LAS unsigned*)(MU_SA(buf) + wid * 1024 + i * 8192), 16, 0, 0); } while (0)
; #define MU_B_ISSUE(sb, kt) do { const char* kb_ = Bb + (size_t)(kt) * (64 * (size_t)RB); _Pragma("unroll") for (int j = 0; j < 8; ++j) { const char* p_ = kb_ + (size_t)j * RB; \
;         asm volatile("global_load_dwordx2 %0, %1, off" : "=&v"(sb[j]) : "v"(p_) : "memory"); } } while (0)
; #define MU_B_WAIT(sb, N) asm volatile("s_waitcnt vmcnt(%8)" : "+v"(sb[0]), "+v"(sb[1]), "+v"(sb[2]), "+v"(sb[3]), "+v"(sb[4]), "+v"(sb[5]), "+v"(sb[6]), "+v"(sb[7]) : "n"(N) : "memory")
; #define MU_G_LOAD(ga, kt) do { const PG8_LAS f32x4* gk_ = (const PG8_LAS f32x4*)(lds + GAIN_OFF) + 16 * (kt) + 2 * wid; const f32x4 ga_ = gk_[0], gb_ = gk_[1]; \
;         ga[0] = ga_[0]; ga[1] = ga_[1]; ga[2] = ga_[2]; ga[3] = ga_[3]; ga[4] = gb_[0]; ga[5] = gb_[1]; ga[6] = gb_[2]; ga[7] = gb_[3]; } while (0)
; #define MU_COMPUTE(buf) MU_COMPUTE_N(buf, NMU)
; #define MU_END(last) do { if (last) asm volatile("s_waitcnt vmcnt(0)" ::: "memory"); else asm volatile("s_waitcnt vmcnt(8)" ::: "memory"); \
;         asm volatile("s_waitcnt lgkmcnt(0)" ::: "memory"); __builtin_amdgcn_s_barrier(); asm volatile("" ::: "memory"); } while (0)
; template <int MODE>
; __device__ __forceinline__ void moe_unit(PG8_LAS unsigned char* lds, int e, int cb, int slot0  , int nv  , const bf16_t* A, const int* slot_tok,
;                                          const float* W0, const float* W1, bf16_t* OUT, const float* slot_rs  , const int* slot_dst) {
;     ...
;         if (t + 2 < nt) MU_B_WAIT(s1, 8); else MU_B_WAIT(s1, 0);
;         MU_G_LOAD(g0, t + 1); MU_B_WRITE(s1, 1, g0); __builtin_amdgcn_sched_barrier(0); MU_GLDS_A(1, t + 1); __builtin_amdgcn_sched_barrier(0);
;         if (t + 3 < nt) { MU_B_ISSUE(s1, t + 3); }
;         MU_COMPUTE(0);
;         MU_END(t + 3 >= nt);
;         if (t + 2 < nt) { MU_B_WAIT(s0, 8); MU_G_LOAD(g0, t + 2); MU_B_WRITE(s0, 0, g0); __builtin_amdgcn_sched_barrier(0); MU_GLDS_A(0, t + 2); __builtin_amdgcn_sched_barrier(0); }
;         if (t + 4 < nt) { MU_B_ISSUE(s0, t + 4); }
;         MU_COMPUTE(1);
;         MU_END(t + 4 >= nt);
	s_load_dwordx8 s[12:19], s[28:29], 0x0
	s_add_u32 s28, s28, 0x100
	s_addc_u32 s29, s29, 0
	v_mfma_f32_16x16x32_bf16 v[78:81], v[142:145], v[218:221], v[78:81]
	v_mfma_f32_16x16x32_bf16 v[74:77], v[146:149], v[218:221], v[74:77]
	v_mfma_f32_16x16x32_bf16 v[70:73], v[150:153], v[218:221], v[70:73]
	v_mfma_f32_16x16x32_bf16 v[66:69], v[154:157], v[218:221], v[66:69]
	v_lshl_add_u64 v[132:133], v[132:133], 0, s[40:41]
	global_load_dwordx2 v[202:203], v[132:133], off
	global_load_dwordx2 v[204:205], v[132:133], off offset:2048
	v_mfma_f32_16x16x32_bf16 v[62:65], v[142:145], v[222:225], v[62:65]
	v_mfma_f32_16x16x32_bf16 v[58:61], v[146:149], v[222:225], v[58:61]
	v_mfma_f32_16x16x32_bf16 v[54:57], v[150:153], v[222:225], v[54:57]
	v_mfma_f32_16x16x32_bf16 v[50:53], v[154:157], v[222:225], v[50:53]
	v_lshl_add_u64 v[166:167], v[132:133], 0, s[34:35]
	global_load_dwordx2 v[206:207], v[166:167], off
	global_load_dwordx2 v[208:209], v[166:167], off offset:2048
	v_mfma_f32_16x16x32_bf16 v[46:49], v[142:145], v[226:229], v[46:49]
	v_mfma_f32_16x16x32_bf16 v[42:45], v[146:149], v[226:229], v[42:45]
	v_mfma_f32_16x16x32_bf16 v[38:41], v[150:153], v[226:229], v[38:41]
	v_mfma_f32_16x16x32_bf16 v[34:37], v[154:157], v[226:229], v[34:37]
	v_lshl_add_u64 v[166:167], v[132:133], 0, s[36:37]
	global_load_dwordx2 v[210:211], v[166:167], off
	global_load_dwordx2 v[212:213], v[166:167], off offset:2048
	v_mfma_f32_16x16x32_bf16 v[18:21], v[142:145], v[230:233], v[18:21]
	v_mfma_f32_16x16x32_bf16 v[22:25], v[146:149], v[230:233], v[22:25]
	v_mfma_f32_16x16x32_bf16 v[26:29], v[150:153], v[230:233], v[26:29]
	v_mfma_f32_16x16x32_bf16 v[30:33], v[154:157], v[230:233], v[30:33]
	v_lshl_add_u64 v[166:167], v[132:133], 0, s[38:39]
	global_load_dwordx2 v[214:215], v[166:167], off
	global_load_dwordx2 v[216:217], v[166:167], off offset:2048
	v_mfma_f32_16x16x32_bf16 v[2:5], v[142:145], v[234:237], v[2:5]
	v_mfma_f32_16x16x32_bf16 v[6:9], v[146:149], v[234:237], v[6:9]
	v_mfma_f32_16x16x32_bf16 v[10:13], v[150:153], v[234:237], v[10:13]
	v_mfma_f32_16x16x32_bf16 v[14:17], v[154:157], v[234:237], v[14:17]
	s_waitcnt vmcnt(21)
	s_waitcnt lgkmcnt(0)
	s_barrier
	s_mov_b32 s47, s42
	s_mov_b32 s42, s43
	s_mov_b32 s43, s44
	s_mov_b32 s44, s47
	v_mul_f32_e32 v98, s12, v98
	v_mul_f32_e32 v99, s12, v99
	v_mul_f32_e32 v100, s13, v100
	v_mul_f32_e32 v101, s13, v101
	v_mul_f32_e32 v102, s14, v102
	v_mul_f32_e32 v103, s14, v103
	v_mul_f32_e32 v104, s15, v104
	v_mul_f32_e32 v105, s15, v105
	v_mul_f32_e32 v106, s16, v106
	v_mul_f32_e32 v107, s16, v107
	v_mul_f32_e32 v108, s17, v108
	v_mul_f32_e32 v109, s17, v109
	v_mul_f32_e32 v110, s18, v110
	v_mul_f32_e32 v111, s18, v111
	v_mul_f32_e32 v112, s19, v112
	v_mul_f32_e32 v113, s19, v113
	v_cvt_pk_bf16_f32 v158, v98, v100
	v_cvt_pk_bf16_f32 v159, v102, v104
	v_cvt_pk_bf16_f32 v160, v106, v108
	v_cvt_pk_bf16_f32 v161, v110, v112
	v_cvt_pk_bf16_f32 v162, v99, v101
	v_cvt_pk_bf16_f32 v163, v103, v105
	v_cvt_pk_bf16_f32 v164, v107, v109
	v_cvt_pk_bf16_f32 v165, v111, v113
	ds_write_b128 v1, v[158:161] offset:0
	ds_write_b128 v1, v[162:165] offset:128
	v_add_u32_e32 v91, s42, v135
	v_add_u32_e32 v93, s42, v137
	ds_read_b128 v[238:241], v139 offset:19456
	ds_read_b128 v[242:245], v139 offset:21504
	ds_read_b128 v[246:249], v139 offset:23552
	ds_read_b128 v[250:253], v139 offset:25600
	ds_read_b128 v[218:221], v91 offset:0
	ds_read_b128 v[222:225], v91 offset:2048
	ds_read_b128 v[226:229], v91 offset:4096
	ds_read_b128 v[230:233], v91 offset:6144
	ds_read_b128 v[234:237], v91 offset:8192
	s_add_i32 s47, s44, s6
	s_add_u32 s30, s30, 0x80
	s_addc_u32 s31, s31, 0
	s_waitcnt lgkmcnt(0)
	v_mfma_f32_16x16x32_bf16 v[78:81], v[238:241], v[218:221], v[78:81]
	v_mfma_f32_16x16x32_bf16 v[74:77], v[242:245], v[218:221], v[74:77]
	v_mfma_f32_16x16x32_bf16 v[70:73], v[246:249], v[218:221], v[70:73]
	v_mfma_f32_16x16x32_bf16 v[66:69], v[250:253], v[218:221], v[66:69]
	ds_read_b128 v[218:221], v93 offset:0
	ds_read_b128 v[142:145], v141 offset:19456
	s_mov_b32 m0, s47
	s_nop 0
	global_load_lds_dwordx4 v86, s[30:31]
	v_mfma_f32_16x16x32_bf16 v[62:65], v[238:241], v[222:225], v[62:65]
	v_mfma_f32_16x16x32_bf16 v[58:61], v[242:245], v[222:225], v[58:61]
	v_mfma_f32_16x16x32_bf16 v[54:57], v[246:249], v[222:225], v[54:57]
	v_mfma_f32_16x16x32_bf16 v[50:53], v[250:253], v[222:225], v[50:53]
	ds_read_b128 v[222:225], v93 offset:2048
	ds_read_b128 v[146:149], v141 offset:21504
	s_add_i32 m0, s47, 0x2000
	s_nop 0
	global_load_lds_dwordx4 v134, s[30:31]
	v_mfma_f32_16x16x32_bf16 v[46:49], v[238:241], v[226:229], v[46:49]
	v_mfma_f32_16x16x32_bf16 v[42:45], v[242:245], v[226:229], v[42:45]
	v_mfma_f32_16x16x32_bf16 v[38:41], v[246:249], v[226:229], v[38:41]
	v_mfma_f32_16x16x32_bf16 v[34:37], v[250:253], v[226:229], v[34:37]
	ds_read_b128 v[226:229], v93 offset:4096
	ds_read_b128 v[150:153], v141 offset:23552
	s_add_i32 m0, s47, 0x4000
	s_nop 0
	global_load_lds_dwordx4 v136, s[30:31]
	v_mfma_f32_16x16x32_bf16 v[18:21], v[238:241], v[230:233], v[18:21]
	v_mfma_f32_16x16x32_bf16 v[22:25], v[242:245], v[230:233], v[22:25]
	v_mfma_f32_16x16x32_bf16 v[26:29], v[246:249], v[230:233], v[26:29]
	v_mfma_f32_16x16x32_bf16 v[30:33], v[250:253], v[230:233], v[30:33]
	ds_read_b128 v[230:233], v93 offset:6144
	ds_read_b128 v[154:157], v141 offset:25600
	s_add_i32 m0, s47, 0x6000
	s_nop 0
	global_load_lds_dwordx4 v138, s[30:31]
	v_mfma_f32_16x16x32_bf16 v[2:5], v[238:241], v[234:237], v[2:5]
	v_mfma_f32_16x16x32_bf16 v[6:9], v[242:245], v[234:237], v[6:9]
	v_mfma_f32_16x16x32_bf16 v[10:13], v[246:249], v[234:237], v[10:13]
	v_mfma_f32_16x16x32_bf16 v[14:17], v[250:253], v[234:237], v[14:17]
	ds_read_b128 v[234:237], v93 offset:8192
	s_add_i32 m0, s47, 0x8000
	s_nop 0
	global_load_lds_dwordx4 v140, s[30:31]
	s_waitcnt lgkmcnt(0)
; #define MU_GLDS_A(buf, kt) do { _Pragma("unroll") for (int i = 0; i < NMU; ++i) \
;         __builtin_amdgcn_global_load_lds((const unsigned*)((const char*)A + aoff[i] + (size_t)(kt) * 128), (PG8_LAS unsigned*)(MU_SA(buf) + wid * 1024 + i * 8192), 16, 0, 0); } while (0)
; #define MU_B_ISSUE(sb, kt) do { const char* kb_ = Bb + (size_t)(kt) * (64 * (size_t)RB); _Pragma("unroll") for (int j = 0; j < 8; ++j) { const char* p_ = kb_ + (size_t)j * RB; \
;         asm volatile("global_load_dwordx2 %0, %1, off" : "=&v"(sb[j]) : "v"(p_) : "memory"); } } while (0)
; #define MU_B_WAIT(sb, N) asm volatile("s_waitcnt vmcnt(%8)" : "+v"(sb[0]), "+v"(sb[1]), "+v"(sb[2]), "+v"(sb[3]), "+v"(sb[4]), "+v"(sb[5]), "+v"(sb[6]), "+v"(sb[7]) : "n"(N) : "memory")
; #define MU_G_LOAD(ga, kt) do { const PG8_LAS f32x4* gk_ = (const PG8_LAS f32x4*)(lds + GAIN_OFF) + 16 * (kt) + 2 * wid; const f32x4 ga_ = gk_[0], gb_ = gk_[1]; \
;         ga[0] = ga_[0]; ga[1] = ga_[1]; ga[2] = ga_[2]; ga[3] = ga_[3]; ga[4] = gb_[0]; ga[5] = gb_[1]; ga[6] = gb_[2]; ga[7] = gb_[3]; } while (0)
; #define MU_COMPUTE(buf) MU_COMPUTE_N(buf, NMU)
; #define MU_END(last) do { if (last) asm volatile("s_waitcnt vmcnt(0)" ::: "memory"); else asm volatile("s_waitcnt vmcnt(8)" ::: "memory"); \
;         asm volatile("s_waitcnt lgkmcnt(0)" ::: "memory"); __builtin_amdgcn_s_barrier(); asm volatile("" ::: "memory"); } while (0)
; template <int MODE>
; __device__ __forceinline__ void moe_unit(PG8_LAS unsigned char* lds, int e, int cb, int slot0  , int nv  , const bf16_t* A, const int* slot_tok,
;                                          const float* W0, const float* W1, bf16_t* OUT, const float* slot_rs  , const int* slot_dst) {
;     ...
;     for (int t = 0; t < nt; t += 2) {
;         if (t + 2 < nt) MU_B_WAIT(s1, 8); else MU_B_WAIT(s1, 0);
;         MU_G_LOAD(g0, t + 1); MU_B_WRITE(s1, 1, g0); __builtin_amdgcn_sched_barrier(0); MU_GLDS_A(1, t + 1); __builtin_amdgcn_sched_barrier(0);
;         if (t + 3 < nt) { MU_B_ISSUE(s1, t + 3); }
;         MU_COMPUTE(0);
;         MU_END(t + 3 >= nt);
;         if (t + 2 < nt) { MU_B_WAIT(s0, 8); MU_G_LOAD(g0, t + 2); MU_B_WRITE(s0, 0, g0); __builtin_amdgcn_sched_barrier(0); MU_GLDS_A(0, t + 2); __builtin_amdgcn_sched_barrier(0); }
;         if (t + 4 < nt) { MU_B_ISSUE(s0, t + 4); }
;         MU_COMPUTE(1);
;         MU_END(t + 4 >= nt);
	s_load_dwordx8 s[20:27], s[28:29], 0x0
	s_add_u32 s28, s28, 0x100
	s_addc_u32 s29, s29, 0
	v_mfma_f32_16x16x32_bf16 v[78:81], v[142:145], v[218:221], v[78:81]
	v_mfma_f32_16x16x32_bf16 v[74:77], v[146:149], v[218:221], v[74:77]
	v_mfma_f32_16x16x32_bf16 v[70:73], v[150:153], v[218:221], v[70:73]
	v_mfma_f32_16x16x32_bf16 v[66:69], v[154:157], v[218:221], v[66:69]
	v_lshl_add_u64 v[132:133], v[132:133], 0, s[40:41]
	global_load_dwordx2 v[98:99], v[132:133], off
	global_load_dwordx2 v[100:101], v[132:133], off offset:2048
	v_mfma_f32_16x16x32_bf16 v[62:65], v[142:145], v[222:225], v[62:65]
	v_mfma_f32_16x16x32_bf16 v[58:61], v[146:149], v[222:225], v[58:61]
	v_mfma_f32_16x16x32_bf16 v[54:57], v[150:153], v[222:225], v[54:57]
	v_mfma_f32_16x16x32_bf16 v[50:53], v[154:157], v[222:225], v[50:53]
	v_lshl_add_u64 v[166:167], v[132:133], 0, s[34:35]
	global_load_dwordx2 v[102:103], v[166:167], off
	global_load_dwordx2 v[104:105], v[166:167], off offset:2048
	v_mfma_f32_16x16x32_bf16 v[46:49], v[142:145], v[226:229], v[46:49]
	v_mfma_f32_16x16x32_bf16 v[42:45], v[146:149], v[226:229], v[42:45]
	v_mfma_f32_16x16x32_bf16 v[38:41], v[150:153], v[226:229], v[38:41]
	v_mfma_f32_16x16x32_bf16 v[34:37], v[154:157], v[226:229], v[34:37]
	v_lshl_add_u64 v[166:167], v[132:133], 0, s[36:37]
	global_load_dwordx2 v[106:107], v[166:167], off
	global_load_dwordx2 v[108:109], v[166:167], off offset:2048
	v_mfma_f32_16x16x32_bf16 v[18:21], v[142:145], v[230:233], v[18:21]
	v_mfma_f32_16x16x32_bf16 v[22:25], v[146:149], v[230:233], v[22:25]
	v_mfma_f32_16x16x32_bf16 v[26:29], v[150:153], v[230:233], v[26:29]
	v_mfma_f32_16x16x32_bf16 v[30:33], v[154:157], v[230:233], v[30:33]
	v_lshl_add_u64 v[166:167], v[132:133], 0, s[38:39]
	global_load_dwordx2 v[110:111], v[166:167], off
	global_load_dwordx2 v[112:113], v[166:167], off offset:2048
	v_mfma_f32_16x16x32_bf16 v[2:5], v[142:145], v[234:237], v[2:5]
	v_mfma_f32_16x16x32_bf16 v[6:9], v[146:149], v[234:237], v[6:9]
	v_mfma_f32_16x16x32_bf16 v[10:13], v[150:153], v[234:237], v[10:13]
	v_mfma_f32_16x16x32_bf16 v[14:17], v[154:157], v[234:237], v[14:17]
	s_waitcnt vmcnt(21)
	s_waitcnt lgkmcnt(0)
	s_barrier
	s_mov_b32 s47, s42
	s_mov_b32 s42, s43
	s_mov_b32 s43, s44
	s_mov_b32 s44, s47
	s_sub_u32 s46, s46, 1
	s_cmp_lg_u32 s46, 0
	s_cbranch_scc1 .Lmu_loop
	v_mul_f32_e32 v114, s20, v114
	v_mul_f32_e32 v115, s20, v115
	v_mul_f32_e32 v116, s21, v116
	v_mul_f32_e32 v117, s21, v117
	v_mul_f32_e32 v118, s22, v118
	v_mul_f32_e32 v119, s22, v119
	v_mul_f32_e32 v120, s23, v120
	v_mul_f32_e32 v121, s23, v121
	v_mul_f32_e32 v122, s24, v122
	v_mul_f32_e32 v123, s24, v123
	v_mul_f32_e32 v124, s25, v124
	v_mul_f32_e32 v125, s25, v125
	v_mul_f32_e32 v126, s26, v126
	v_mul_f32_e32 v127, s26, v127
	v_mul_f32_e32 v128, s27, v128
	v_mul_f32_e32 v129, s27, v129
	v_cvt_pk_bf16_f32 v158, v114, v116
	v_cvt_pk_bf16_f32 v159, v118, v120
	v_cvt_pk_bf16_f32 v160, v122, v124
	v_cvt_pk_bf16_f32 v161, v126, v128
	v_cvt_pk_bf16_f32 v162, v115, v117
	v_cvt_pk_bf16_f32 v163, v119, v121
	v_cvt_pk_bf16_f32 v164, v123, v125
	v_cvt_pk_bf16_f32 v165, v127, v129
	ds_write_b128 v1, v[158:161] offset:19456
	ds_write_b128 v1, v[162:165] offset:19584
	v_add_u32_e32 v91, s42, v135
	v_add_u32_e32 v93, s42, v137
	ds_read_b128 v[238:241], v139 offset:0
	ds_read_b128 v[242:245], v139 offset:2048
	ds_read_b128 v[246:249], v139 offset:4096
	ds_read_b128 v[250:253], v139 offset:6144
	ds_read_b128 v[218:221], v91 offset:0
	ds_read_b128 v[222:225], v91 offset:2048
	ds_read_b128 v[226:229], v91 offset:4096
	ds_read_b128 v[230:233], v91 offset:6144
	ds_read_b128 v[234:237], v91 offset:8192
	s_add_i32 s47, s44, s6
	s_add_u32 s30, s30, 0x80
	s_addc_u32 s31, s31, 0
	s_waitcnt lgkmcnt(0)
	v_mfma_f32_16x16x32_bf16 v[78:81], v[238:241], v[218:221], v[78:81]
	v_mfma_f32_16x16x32_bf16 v[74:77], v[242:245], v[218:221], v[74:77]
	v_mfma_f32_16x16x32_bf16 v[70:73], v[246:249], v[218:221], v[70:73]
	v_mfma_f32_16x16x32_bf16 v[66:69], v[250:253], v[218:221], v[66:69]
	ds_read_b128 v[218:221], v93 offset:0
	ds_read_b128 v[142:145], v141 offset:0
	s_mov_b32 m0, s47
	s_nop 0
	global_load_lds_dwordx4 v86, s[30:31]
	v_mfma_f32_16x16x32_bf16 v[62:65], v[238:241], v[222:225], v[62:65]
	v_mfma_f32_16x16x32_bf16 v[58:61], v[242:245], v[222:225], v[58:61]
	v_mfma_f32_16x16x32_bf16 v[54:57], v[246:249], v[222:225], v[54:57]
	v_mfma_f32_16x16x32_bf16 v[50:53], v[250:253], v[222:225], v[50:53]
	ds_read_b128 v[222:225], v93 offset:2048
	ds_read_b128 v[146:149], v141 offset:2048
	s_add_i32 m0, s47, 0x2000
	s_nop 0
	global_load_lds_dwordx4 v134, s[30:31]
	v_mfma_f32_16x16x32_bf16 v[46:49], v[238:241], v[226:229], v[46:49]
	v_mfma_f32_16x16x32_bf16 v[42:45], v[242:245], v[226:229], v[42:45]
	v_mfma_f32_16x16x32_bf16 v[38:41], v[246:249], v[226:229], v[38:41]
	v_mfma_f32_16x16x32_bf16 v[34:37], v[250:253], v[226:229], v[34:37]
	ds_read_b128 v[226:229], v93 offset:4096
	ds_read_b128 v[150:153], v141 offset:4096
	s_add_i32 m0, s47, 0x4000
	s_nop 0
	global_load_lds_dwordx4 v136, s[30:31]
	v_mfma_f32_16x16x32_bf16 v[18:21], v[238:241], v[230:233], v[18:21]
	v_mfma_f32_16x16x32_bf16 v[22:25], v[242:245], v[230:233], v[22:25]
	v_mfma_f32_16x16x32_bf16 v[26:29], v[246:249], v[230:233], v[26:29]
	v_mfma_f32_16x16x32_bf16 v[30:33], v[250:253], v[230:233], v[30:33]
	ds_read_b128 v[230:233], v93 offset:6144
	ds_read_b128 v[154:157], v141 offset:6144
	s_add_i32 m0, s47, 0x6000
	s_nop 0
	global_load_lds_dwordx4 v138, s[30:31]
	v_mfma_f32_16x16x32_bf16 v[2:5], v[238:241], v[234:237], v[2:5]
	v_mfma_f32_16x16x32_bf16 v[6:9], v[242:245], v[234:237], v[6:9]
	v_mfma_f32_16x16x32_bf16 v[10:13], v[246:249], v[234:237], v[10:13]
	v_mfma_f32_16x16x32_bf16 v[14:17], v[250:253], v[234:237], v[14:17]
	ds_read_b128 v[234:237], v93 offset:8192
	s_add_i32 m0, s47, 0x8000
	s_nop 0
	global_load_lds_dwordx4 v140, s[30:31]
	s_waitcnt lgkmcnt(0)
; #define MU_GLDS_A(buf, kt) do { _Pragma("unroll") for (int i = 0; i < NMU; ++i) \
;         __builtin_amdgcn_global_load_lds((const unsigned*)((const char*)A + aoff[i] + (size_t)(kt) * 128), (PG8_LAS unsigned*)(MU_SA(buf) + wid * 1024 + i * 8192), 16, 0, 0); } while (0)
; #define MU_B_ISSUE(sb, kt) do { const char* kb_ = Bb + (size_t)(kt) * (64 * (size_t)RB); _Pragma("unroll") for (int j = 0; j < 8; ++j) { const char* p_ = kb_ + (size_t)j * RB; \
;         asm volatile("global_load_dwordx2 %0, %1, off" : "=&v"(sb[j]) : "v"(p_) : "memory"); } } while (0)
; #define MU_B_WAIT(sb, N) asm volatile("s_waitcnt vmcnt(%8)" : "+v"(sb[0]), "+v"(sb[1]), "+v"(sb[2]), "+v"(sb[3]), "+v"(sb[4]), "+v"(sb[5]), "+v"(sb[6]), "+v"(sb[7]) : "n"(N) : "memory")
; #define MU_G_LOAD(ga, kt) do { const PG8_LAS f32x4* gk_ = (const PG8_LAS f32x4*)(lds + GAIN_OFF) + 16 * (kt) + 2 * wid; const f32x4 ga_ = gk_[0], gb_ = gk_[1]; \
;         ga[0] = ga_[0]; ga[1] = ga_[1]; ga[2] = ga_[2]; ga[3] = ga_[3]; ga[4] = gb_[0]; ga[5] = gb_[1]; ga[6] = gb_[2]; ga[7] = gb_[3]; } while (0)
; #define MU_COMPUTE(buf) MU_COMPUTE_N(buf, NMU)
; #define MU_END(last) do { if (last) asm volatile("s_waitcnt vmcnt(0)" ::: "memory"); else asm volatile("s_waitcnt vmcnt(8)" ::: "memory"); \
;         asm volatile("s_waitcnt lgkmcnt(0)" ::: "memory"); __builtin_amdgcn_s_barrier(); asm volatile("" ::: "memory"); } while (0)
; template <int MODE>
; __device__ __forceinline__ void moe_unit(PG8_LAS unsigned char* lds, int e, int cb, int slot0  , int nv  , const bf16_t* A, const int* slot_tok,
;                                          const float* W0, const float* W1, bf16_t* OUT, const float* slot_rs  , const int* slot_dst) {
;     ...
;         if (t + 2 < nt) MU_B_WAIT(s1, 8); else MU_B_WAIT(s1, 0);
;         MU_G_LOAD(g0, t + 1); MU_B_WRITE(s1, 1, g0); __builtin_amdgcn_sched_barrier(0); MU_GLDS_A(1, t + 1); __builtin_amdgcn_sched_barrier(0);
;         if (t + 3 < nt) { MU_B_ISSUE(s1, t + 3); }
;         MU_COMPUTE(0);
;         MU_END(t + 3 >= nt);
;         if (t + 2 < nt) { MU_B_WAIT(s0, 8); MU_G_LOAD(g0, t + 2); MU_B_WRITE(s0, 0, g0); __builtin_amdgcn_sched_barrier(0); MU_GLDS_A(0, t + 2); __builtin_amdgcn_sched_barrier(0); }
;         if (t + 4 < nt) { MU_B_ISSUE(s0, t + 4); }
;         MU_COMPUTE(1);
;         MU_END(t + 4 >= nt);
	s_load_dwordx8 s[12:19], s[28:29], 0x0
	s_add_u32 s28, s28, 0x100
	s_addc_u32 s29, s29, 0
	v_mfma_f32_16x16x32_bf16 v[78:81], v[142:145], v[218:221], v[78:81]
	v_mfma_f32_16x16x32_bf16 v[74:77], v[146:149], v[218:221], v[74:77]
	v_mfma_f32_16x16x32_bf16 v[70:73], v[150:153], v[218:221], v[70:73]
	v_mfma_f32_16x16x32_bf16 v[66:69], v[154:157], v[218:221], v[66:69]
	v_lshl_add_u64 v[132:133], v[132:133], 0, s[40:41]
	global_load_dwordx2 v[114:115], v[132:133], off
	global_load_dwordx2 v[116:117], v[132:133], off offset:2048
	v_mfma_f32_16x16x32_bf16 v[62:65], v[142:145], v[222:225], v[62:65]
	v_mfma_f32_16x16x32_bf16 v[58:61], v[146:149], v[222:225], v[58:61]
	v_mfma_f32_16x16x32_bf16 v[54:57], v[150:153], v[222:225], v[54:57]
	v_mfma_f32_16x16x32_bf16 v[50:53], v[154:157], v[222:225], v[50:53]
	v_lshl_add_u64 v[166:167], v[132:133], 0, s[34:35]
	global_load_dwordx2 v[118:119], v[166:167], off
	global_load_dwordx2 v[120:121], v[166:167], off offset:2048
	v_mfma_f32_16x16x32_bf16 v[46:49], v[142:145], v[226:229], v[46:49]
	v_mfma_f32_16x16x32_bf16 v[42:45], v[146:149], v[226:229], v[42:45]
	v_mfma_f32_16x16x32_bf16 v[38:41], v[150:153], v[226:229], v[38:41]
	v_mfma_f32_16x16x32_bf16 v[34:37], v[154:157], v[226:229], v[34:37]
	v_lshl_add_u64 v[166:167], v[132:133], 0, s[36:37]
	global_load_dwordx2 v[122:123], v[166:167], off
	global_load_dwordx2 v[124:125], v[166:167], off offset:2048
	v_mfma_f32_16x16x32_bf16 v[18:21], v[142:145], v[230:233], v[18:21]
	v_mfma_f32_16x16x32_bf16 v[22:25], v[146:149], v[230:233], v[22:25]
	v_mfma_f32_16x16x32_bf16 v[26:29], v[150:153], v[230:233], v[26:29]
	v_mfma_f32_16x16x32_bf16 v[30:33], v[154:157], v[230:233], v[30:33]
	v_lshl_add_u64 v[166:167], v[132:133], 0, s[38:39]
	global_load_dwordx2 v[126:127], v[166:167], off
	global_load_dwordx2 v[128:129], v[166:167], off offset:2048
	v_mfma_f32_16x16x32_bf16 v[2:5], v[142:145], v[234:237], v[2:5]
	v_mfma_f32_16x16x32_bf16 v[6:9], v[146:149], v[234:237], v[6:9]
	v_mfma_f32_16x16x32_bf16 v[10:13], v[150:153], v[234:237], v[10:13]
	v_mfma_f32_16x16x32_bf16 v[14:17], v[154:157], v[234:237], v[14:17]
	s_waitcnt vmcnt(21)
	s_waitcnt lgkmcnt(0)
	s_barrier
	s_mov_b32 s47, s42
	s_mov_b32 s42, s43
	s_mov_b32 s43, s44
	s_mov_b32 s44, s47
	v_mul_f32_e32 v186, s12, v186
	v_mul_f32_e32 v187, s12, v187
	v_mul_f32_e32 v188, s13, v188
	v_mul_f32_e32 v189, s13, v189
	v_mul_f32_e32 v190, s14, v190
	v_mul_f32_e32 v191, s14, v191
	v_mul_f32_e32 v192, s15, v192
	v_mul_f32_e32 v193, s15, v193
	v_mul_f32_e32 v194, s16, v194
	v_mul_f32_e32 v195, s16, v195
	v_mul_f32_e32 v196, s17, v196
	v_mul_f32_e32 v197, s17, v197
	v_mul_f32_e32 v198, s18, v198
	v_mul_f32_e32 v199, s18, v199
	v_mul_f32_e32 v200, s19, v200
	v_mul_f32_e32 v201, s19, v201
	v_cvt_pk_bf16_f32 v158, v186, v188
	v_cvt_pk_bf16_f32 v159, v190, v192
	v_cvt_pk_bf16_f32 v160, v194, v196
	v_cvt_pk_bf16_f32 v161, v198, v200
	v_cvt_pk_bf16_f32 v162, v187, v189
	v_cvt_pk_bf16_f32 v163, v191, v193
	v_cvt_pk_bf16_f32 v164, v195, v197
	v_cvt_pk_bf16_f32 v165, v199, v201
	ds_write_b128 v1, v[158:161] offset:0
	ds_write_b128 v1, v[162:165] offset:128
	v_add_u32_e32 v91, s42, v135
	v_add_u32_e32 v93, s42, v137
	ds_read_b128 v[238:241], v139 offset:19456
	ds_read_b128 v[242:245], v139 offset:21504
	ds_read_b128 v[246:249], v139 offset:23552
	ds_read_b128 v[250:253], v139 offset:25600
	ds_read_b128 v[218:221], v91 offset:0
	ds_read_b128 v[222:225], v91 offset:2048
	ds_read_b128 v[226:229], v91 offset:4096
	ds_read_b128 v[230:233], v91 offset:6144
	ds_read_b128 v[234:237], v91 offset:8192
	s_add_i32 s47, s44, s6
	s_add_u32 s30, s30, 0x80
	s_addc_u32 s31, s31, 0
	s_waitcnt lgkmcnt(0)
	v_mfma_f32_16x16x32_bf16 v[78:81], v[238:241], v[218:221], v[78:81]
	v_mfma_f32_16x16x32_bf16 v[74:77], v[242:245], v[218:221], v[74:77]
	v_mfma_f32_16x16x32_bf16 v[70:73], v[246:249], v[218:221], v[70:73]
	v_mfma_f32_16x16x32_bf16 v[66:69], v[250:253], v[218:221], v[66:69]
	ds_read_b128 v[218:221], v93 offset:0
	ds_read_b128 v[142:145], v141 offset:19456
	s_mov_b32 m0, s47
	s_nop 0
	global_load_lds_dwordx4 v86, s[30:31]
	v_mfma_f32_16x16x32_bf16 v[62:65], v[238:241], v[222:225], v[62:65]
	v_mfma_f32_16x16x32_bf16 v[58:61], v[242:245], v[222:225], v[58:61]
	v_mfma_f32_16x16x32_bf16 v[54:57], v[246:249], v[222:225], v[54:57]
	v_mfma_f32_16x16x32_bf16 v[50:53], v[250:253], v[222:225], v[50:53]
	ds_read_b128 v[222:225], v93 offset:2048
	ds_read_b128 v[146:149], v141 offset:21504
	s_add_i32 m0, s47, 0x2000
	s_nop 0
	global_load_lds_dwordx4 v134, s[30:31]
	v_mfma_f32_16x16x32_bf16 v[46:49], v[238:241], v[226:229], v[46:49]
	v_mfma_f32_16x16x32_bf16 v[42:45], v[242:245], v[226:229], v[42:45]
	v_mfma_f32_16x16x32_bf16 v[38:41], v[246:249], v[226:229], v[38:41]
	v_mfma_f32_16x16x32_bf16 v[34:37], v[250:253], v[226:229], v[34:37]
	ds_read_b128 v[226:229], v93 offset:4096
	ds_read_b128 v[150:153], v141 offset:23552
	s_add_i32 m0, s47, 0x4000
	s_nop 0
	global_load_lds_dwordx4 v136, s[30:31]
	v_mfma_f32_16x16x32_bf16 v[18:21], v[238:241], v[230:233], v[18:21]
	v_mfma_f32_16x16x32_bf16 v[22:25], v[242:245], v[230:233], v[22:25]
	v_mfma_f32_16x16x32_bf16 v[26:29], v[246:249], v[230:233], v[26:29]
	v_mfma_f32_16x16x32_bf16 v[30:33], v[250:253], v[230:233], v[30:33]
	ds_read_b128 v[230:233], v93 offset:6144
	ds_read_b128 v[154:157], v141 offset:25600
	s_add_i32 m0, s47, 0x6000
	s_nop 0
	global_load_lds_dwordx4 v138, s[30:31]
	v_mfma_f32_16x16x32_bf16 v[2:5], v[238:241], v[234:237], v[2:5]
	v_mfma_f32_16x16x32_bf16 v[6:9], v[242:245], v[234:237], v[6:9]
	v_mfma_f32_16x16x32_bf16 v[10:13], v[246:249], v[234:237], v[10:13]
	v_mfma_f32_16x16x32_bf16 v[14:17], v[250:253], v[234:237], v[14:17]
	ds_read_b128 v[234:237], v93 offset:8192
	s_add_i32 m0, s47, 0x8000
	s_nop 0
	global_load_lds_dwordx4 v140, s[30:31]
	s_waitcnt lgkmcnt(0)
; #define MU_GLDS_A(buf, kt) do { _Pragma("unroll") for (int i = 0; i < NMU; ++i) \
;         __builtin_amdgcn_global_load_lds((const unsigned*)((const char*)A + aoff[i] + (size_t)(kt) * 128), (PG8_LAS unsigned*)(MU_SA(buf) + wid * 1024 + i * 8192), 16, 0, 0); } while (0)
; #define MU_B_ISSUE(sb, kt) do { const char* kb_ = Bb + (size_t)(kt) * (64 * (size_t)RB); _Pragma("unroll") for (int j = 0; j < 8; ++j) { const char* p_ = kb_ + (size_t)j * RB; \
;         asm volatile("global_load_dwordx2 %0, %1, off" : "=&v"(sb[j]) : "v"(p_) : "memory"); } } while (0)
; #define MU_B_WAIT(sb, N) asm volatile("s_waitcnt vmcnt(%8)" : "+v"(sb[0]), "+v"(sb[1]), "+v"(sb[2]), "+v"(sb[3]), "+v"(sb[4]), "+v"(sb[5]), "+v"(sb[6]), "+v"(sb[7]) : "n"(N) : "memory")
; #define MU_G_LOAD(ga, kt) do { const PG8_LAS f32x4* gk_ = (const PG8_LAS f32x4*)(lds + GAIN_OFF) + 16 * (kt) + 2 * wid; const f32x4 ga_ = gk_[0], gb_ = gk_[1]; \
;         ga[0] = ga_[0]; ga[1] = ga_[1]; ga[2] = ga_[2]; ga[3] = ga_[3]; ga[4] = gb_[0]; ga[5] = gb_[1]; ga[6] = gb_[2]; ga[7] = gb_[3]; } while (0)
; #define MU_COMPUTE(buf) MU_COMPUTE_N(buf, NMU)
; #define MU_END(last) do { if (last) asm volatile("s_waitcnt vmcnt(0)" ::: "memory"); else asm volatile("s_waitcnt vmcnt(8)" ::: "memory"); \
;         asm volatile("s_waitcnt lgkmcnt(0)" ::: "memory"); __builtin_amdgcn_s_barrier(); asm volatile("" ::: "memory"); } while (0)
; template <int MODE>
; __device__ __forceinline__ void moe_unit(PG8_LAS unsigned char* lds, int e, int cb, int slot0  , int nv  , const bf16_t* A, const int* slot_tok,
;                                          const float* W0, const float* W1, bf16_t* OUT, const float* slot_rs  , const int* slot_dst) {
;     ...
;         if (t + 2 < nt) MU_B_WAIT(s1, 8); else MU_B_WAIT(s1, 0);
;         MU_G_LOAD(g0, t + 1); MU_B_WRITE(s1, 1, g0); __builtin_amdgcn_sched_barrier(0); MU_GLDS_A(1, t + 1); __builtin_amdgcn_sched_barrier(0);
;         if (t + 3 < nt) { MU_B_ISSUE(s1, t + 3); }
;         MU_COMPUTE(0);
;         MU_END(t + 3 >= nt);
;         if (t + 2 < nt) { MU_B_WAIT(s0, 8); MU_G_LOAD(g0, t + 2); MU_B_WRITE(s0, 0, g0); __builtin_amdgcn_sched_barrier(0); MU_GLDS_A(0, t + 2); __builtin_amdgcn_sched_barrier(0); }
;         if (t + 4 < nt) { MU_B_ISSUE(s0, t + 4); }
;         MU_COMPUTE(1);
;         MU_END(t + 4 >= nt);
	s_load_dwordx8 s[20:27], s[28:29], 0x0
	s_add_u32 s28, s28, 0x100
	s_addc_u32 s29, s29, 0
	v_mfma_f32_16x16x32_bf16 v[78:81], v[142:145], v[218:221], v[78:81]
	v_mfma_f32_16x16x32_bf16 v[74:77], v[146:149], v[218:221], v[74:77]
	v_mfma_f32_16x16x32_bf16 v[70:73], v[150:153], v[218:221], v[70:73]
	v_mfma_f32_16x16x32_bf16 v[66:69], v[154:157], v[218:221], v[66:69]
	v_lshl_add_u64 v[132:133], v[132:133], 0, s[40:41]
	global_load_dwordx2 v[186:187], v[132:133], off
	global_load_dwordx2 v[188:189], v[132:133], off offset:2048
	v_mfma_f32_16x16x32_bf16 v[62:65], v[142:145], v[222:225], v[62:65]
	v_mfma_f32_16x16x32_bf16 v[58:61], v[146:149], v[222:225], v[58:61]
	v_mfma_f32_16x16x32_bf16 v[54:57], v[150:153], v[222:225], v[54:57]
	v_mfma_f32_16x16x32_bf16 v[50:53], v[154:157], v[222:225], v[50:53]
	v_lshl_add_u64 v[166:167], v[132:133], 0, s[34:35]
	global_load_dwordx2 v[190:191], v[166:167], off
	global_load_dwordx2 v[192:193], v[166:167], off offset:2048
	v_mfma_f32_16x16x32_bf16 v[46:49], v[142:145], v[226:229], v[46:49]
	v_mfma_f32_16x16x32_bf16 v[42:45], v[146:149], v[226:229], v[42:45]
	v_mfma_f32_16x16x32_bf16 v[38:41], v[150:153], v[226:229], v[38:41]
	v_mfma_f32_16x16x32_bf16 v[34:37], v[154:157], v[226:229], v[34:37]
	v_lshl_add_u64 v[166:167], v[132:133], 0, s[36:37]
	global_load_dwordx2 v[194:195], v[166:167], off
	global_load_dwordx2 v[196:197], v[166:167], off offset:2048
	v_mfma_f32_16x16x32_bf16 v[18:21], v[142:145], v[230:233], v[18:21]
	v_mfma_f32_16x16x32_bf16 v[22:25], v[146:149], v[230:233], v[22:25]
	v_mfma_f32_16x16x32_bf16 v[26:29], v[150:153], v[230:233], v[26:29]
	v_mfma_f32_16x16x32_bf16 v[30:33], v[154:157], v[230:233], v[30:33]
	v_lshl_add_u64 v[166:167], v[132:133], 0, s[38:39]
	global_load_dwordx2 v[198:199], v[166:167], off
	global_load_dwordx2 v[200:201], v[166:167], off offset:2048
	v_mfma_f32_16x16x32_bf16 v[2:5], v[142:145], v[234:237], v[2:5]
	v_mfma_f32_16x16x32_bf16 v[6:9], v[146:149], v[234:237], v[6:9]
	v_mfma_f32_16x16x32_bf16 v[10:13], v[150:153], v[234:237], v[10:13]
	v_mfma_f32_16x16x32_bf16 v[14:17], v[154:157], v[234:237], v[14:17]
	s_waitcnt vmcnt(21)
	s_waitcnt lgkmcnt(0)
	s_barrier
	s_mov_b32 s47, s42
	s_mov_b32 s42, s43
	s_mov_b32 s43, s44
	s_mov_b32 s44, s47
	v_mul_f32_e32 v202, s20, v202
	v_mul_f32_e32 v203, s20, v203
	v_mul_f32_e32 v204, s21, v204
	v_mul_f32_e32 v205, s21, v205
	v_mul_f32_e32 v206, s22, v206
	v_mul_f32_e32 v207, s22, v207
	v_mul_f32_e32 v208, s23, v208
	v_mul_f32_e32 v209, s23, v209
	v_mul_f32_e32 v210, s24, v210
	v_mul_f32_e32 v211, s24, v211
	v_mul_f32_e32 v212, s25, v212
	v_mul_f32_e32 v213, s25, v213
	v_mul_f32_e32 v214, s26, v214
	v_mul_f32_e32 v215, s26, v215
	v_mul_f32_e32 v216, s27, v216
	v_mul_f32_e32 v217, s27, v217
	v_cvt_pk_bf16_f32 v158, v202, v204
	v_cvt_pk_bf16_f32 v159, v206, v208
	v_cvt_pk_bf16_f32 v160, v210, v212
	v_cvt_pk_bf16_f32 v161, v214, v216
	v_cvt_pk_bf16_f32 v162, v203, v205
	v_cvt_pk_bf16_f32 v163, v207, v209
	v_cvt_pk_bf16_f32 v164, v211, v213
	v_cvt_pk_bf16_f32 v165, v215, v217
	ds_write_b128 v1, v[158:161] offset:19456
	ds_write_b128 v1, v[162:165] offset:19584
	v_add_u32_e32 v91, s42, v135
	v_add_u32_e32 v93, s42, v137
	ds_read_b128 v[238:241], v139 offset:0
	ds_read_b128 v[242:245], v139 offset:2048
	ds_read_b128 v[246:249], v139 offset:4096
	ds_read_b128 v[250:253], v139 offset:6144
	ds_read_b128 v[218:221], v91 offset:0
	ds_read_b128 v[222:225], v91 offset:2048
	ds_read_b128 v[226:229], v91 offset:4096
	ds_read_b128 v[230:233], v91 offset:6144
	ds_read_b128 v[234:237], v91 offset:8192
	s_add_i32 s47, s44, s6
	s_add_u32 s30, s30, 0x80
	s_addc_u32 s31, s31, 0
	s_waitcnt lgkmcnt(0)
	v_mfma_f32_16x16x32_bf16 v[78:81], v[238:241], v[218:221], v[78:81]
	v_mfma_f32_16x16x32_bf16 v[74:77], v[242:245], v[218:221], v[74:77]
	v_mfma_f32_16x16x32_bf16 v[70:73], v[246:249], v[218:221], v[70:73]
	v_mfma_f32_16x16x32_bf16 v[66:69], v[250:253], v[218:221], v[66:69]
	ds_read_b128 v[218:221], v93 offset:0
	ds_read_b128 v[142:145], v141 offset:0
	s_mov_b32 m0, s47
	s_nop 0
	global_load_lds_dwordx4 v86, s[30:31]
	v_mfma_f32_16x16x32_bf16 v[62:65], v[238:241], v[222:225], v[62:65]
	v_mfma_f32_16x16x32_bf16 v[58:61], v[242:245], v[222:225], v[58:61]
	v_mfma_f32_16x16x32_bf16 v[54:57], v[246:249], v[222:225], v[54:57]
	v_mfma_f32_16x16x32_bf16 v[50:53], v[250:253], v[222:225], v[50:53]
	ds_read_b128 v[222:225], v93 offset:2048
	ds_read_b128 v[146:149], v141 offset:2048
	s_add_i32 m0, s47, 0x2000
	s_nop 0
	global_load_lds_dwordx4 v134, s[30:31]
	v_mfma_f32_16x16x32_bf16 v[46:49], v[238:241], v[226:229], v[46:49]
	v_mfma_f32_16x16x32_bf16 v[42:45], v[242:245], v[226:229], v[42:45]
	v_mfma_f32_16x16x32_bf16 v[38:41], v[246:249], v[226:229], v[38:41]
	v_mfma_f32_16x16x32_bf16 v[34:37], v[250:253], v[226:229], v[34:37]
	ds_read_b128 v[226:229], v93 offset:4096
	ds_read_b128 v[150:153], v141 offset:4096
	s_add_i32 m0, s47, 0x4000
	s_nop 0
	global_load_lds_dwordx4 v136, s[30:31]
	v_mfma_f32_16x16x32_bf16 v[18:21], v[238:241], v[230:233], v[18:21]
	v_mfma_f32_16x16x32_bf16 v[22:25], v[242:245], v[230:233], v[22:25]
	v_mfma_f32_16x16x32_bf16 v[26:29], v[246:249], v[230:233], v[26:29]
	v_mfma_f32_16x16x32_bf16 v[30:33], v[250:253], v[230:233], v[30:33]
	ds_read_b128 v[230:233], v93 offset:6144
	ds_read_b128 v[154:157], v141 offset:6144
	s_add_i32 m0, s47, 0x6000
	s_nop 0
	global_load_lds_dwordx4 v138, s[30:31]
	v_mfma_f32_16x16x32_bf16 v[2:5], v[238:241], v[234:237], v[2:5]
	v_mfma_f32_16x16x32_bf16 v[6:9], v[242:245], v[234:237], v[6:9]
	v_mfma_f32_16x16x32_bf16 v[10:13], v[246:249], v[234:237], v[10:13]
	v_mfma_f32_16x16x32_bf16 v[14:17], v[250:253], v[234:237], v[14:17]
	ds_read_b128 v[234:237], v93 offset:8192
	s_add_i32 m0, s47, 0x8000
	s_nop 0
	global_load_lds_dwordx4 v140, s[30:31]
	s_waitcnt lgkmcnt(0)
; #define MU_GLDS_A(buf, kt) do { _Pragma("unroll") for (int i = 0; i < NMU; ++i) \
;         __builtin_amdgcn_global_load_lds((const unsigned*)((const char*)A + aoff[i] + (size_t)(kt) * 128), (PG8_LAS unsigned*)(MU_SA(buf) + wid * 1024 + i * 8192), 16, 0, 0); } while (0)
; #define MU_B_ISSUE(sb, kt) do { const char* kb_ = Bb + (size_t)(kt) * (64 * (size_t)RB); _Pragma("unroll") for (int j = 0; j < 8; ++j) { const char* p_ = kb_ + (size_t)j * RB; \
;         asm volatile("global_load_dwordx2 %0, %1, off" : "=&v"(sb[j]) : "v"(p_) : "memory"); } } while (0)
; #define MU_B_WAIT(sb, N) asm volatile("s_waitcnt vmcnt(%8)" : "+v"(sb[0]), "+v"(sb[1]), "+v"(sb[2]), "+v"(sb[3]), "+v"(sb[4]), "+v"(sb[5]), "+v"(sb[6]), "+v"(sb[7]) : "n"(N) : "memory")
; #define MU_G_LOAD(ga, kt) do { const PG8_LAS f32x4* gk_ = (const PG8_LAS f32x4*)(lds + GAIN_OFF) + 16 * (kt) + 2 * wid; const f32x4 ga_ = gk_[0], gb_ = gk_[1]; \
;         ga[0] = ga_[0]; ga[1] = ga_[1]; ga[2] = ga_[2]; ga[3] = ga_[3]; ga[4] = gb_[0]; ga[5] = gb_[1]; ga[6] = gb_[2]; ga[7] = gb_[3]; } while (0)
; #define MU_COMPUTE(buf) MU_COMPUTE_N(buf, NMU)
; #define MU_END(last) do { if (last) asm volatile("s_waitcnt vmcnt(0)" ::: "memory"); else asm volatile("s_waitcnt vmcnt(8)" ::: "memory"); \
;         asm volatile("s_waitcnt lgkmcnt(0)" ::: "memory"); __builtin_amdgcn_s_barrier(); asm volatile("" ::: "memory"); } while (0)
; template <int MODE>
; __device__ __forceinline__ void moe_unit(PG8_LAS unsigned char* lds, int e, int cb, int slot0  , int nv  , const bf16_t* A, const int* slot_tok,
;                                          const float* W0, const float* W1, bf16_t* OUT, const float* slot_rs  , const int* slot_dst) {
;     ...
;         if (t + 2 < nt) MU_B_WAIT(s1, 8); else MU_B_WAIT(s1, 0);
;         MU_G_LOAD(g0, t + 1); MU_B_WRITE(s1, 1, g0); __builtin_amdgcn_sched_barrier(0); MU_GLDS_A(1, t + 1); __builtin_amdgcn_sched_barrier(0);
;         if (t + 3 < nt) { MU_B_ISSUE(s1, t + 3); }
;         MU_COMPUTE(0);
;         MU_END(t + 3 >= nt);
;         if (t + 2 < nt) { MU_B_WAIT(s0, 8); MU_G_LOAD(g0, t + 2); MU_B_WRITE(s0, 0, g0); __builtin_amdgcn_sched_barrier(0); MU_GLDS_A(0, t + 2); __builtin_amdgcn_sched_barrier(0); }
;         if (t + 4 < nt) { MU_B_ISSUE(s0, t + 4); }
;         MU_COMPUTE(1);
;         MU_END(t + 4 >= nt);
	s_load_dwordx8 s[12:19], s[28:29], 0x0
	s_add_u32 s28, s28, 0x100
	s_addc_u32 s29, s29, 0
	v_mfma_f32_16x16x32_bf16 v[78:81], v[142:145], v[218:221], v[78:81]
	v_mfma_f32_16x16x32_bf16 v[74:77], v[146:149], v[218:221], v[74:77]
	v_mfma_f32_16x16x32_bf16 v[70:73], v[150:153], v[218:221], v[70:73]
	v_mfma_f32_16x16x32_bf16 v[66:69], v[154:157], v[218:221], v[66:69]
	v_lshl_add_u64 v[132:133], v[132:133], 0, s[40:41]
	global_load_dwordx2 v[202:203], v[132:133], off
	global_load_dwordx2 v[204:205], v[132:133], off offset:2048
	v_mfma_f32_16x16x32_bf16 v[62:65], v[142:145], v[222:225], v[62:65]
	v_mfma_f32_16x16x32_bf16 v[58:61], v[146:149], v[222:225], v[58:61]
	v_mfma_f32_16x16x32_bf16 v[54:57], v[150:153], v[222:225], v[54:57]
	v_mfma_f32_16x16x32_bf16 v[50:53], v[154:157], v[222:225], v[50:53]
	v_lshl_add_u64 v[166:167], v[132:133], 0, s[34:35]
	global_load_dwordx2 v[206:207], v[166:167], off
	global_load_dwordx2 v[208:209], v[166:167], off offset:2048
	v_mfma_f32_16x16x32_bf16 v[46:49], v[142:145], v[226:229], v[46:49]
	v_mfma_f32_16x16x32_bf16 v[42:45], v[146:149], v[226:229], v[42:45]
	v_mfma_f32_16x16x32_bf16 v[38:41], v[150:153], v[226:229], v[38:41]
	v_mfma_f32_16x16x32_bf16 v[34:37], v[154:157], v[226:229], v[34:37]
	v_lshl_add_u64 v[166:167], v[132:133], 0, s[36:37]
	global_load_dwordx2 v[210:211], v[166:167], off
	global_load_dwordx2 v[212:213], v[166:167], off offset:2048
	v_mfma_f32_16x16x32_bf16 v[18:21], v[142:145], v[230:233], v[18:21]
	v_mfma_f32_16x16x32_bf16 v[22:25], v[146:149], v[230:233], v[22:25]
	v_mfma_f32_16x16x32_bf16 v[26:29], v[150:153], v[230:233], v[26:29]
	v_mfma_f32_16x16x32_bf16 v[30:33], v[154:157], v[230:233], v[30:33]
	v_lshl_add_u64 v[166:167], v[132:133], 0, s[38:39]
	global_load_dwordx2 v[214:215], v[166:167], off
	global_load_dwordx2 v[216:217], v[166:167], off offset:2048
	v_mfma_f32_16x16x32_bf16 v[2:5], v[142:145], v[234:237], v[2:5]
	v_mfma_f32_16x16x32_bf16 v[6:9], v[146:149], v[234:237], v[6:9]
	v_mfma_f32_16x16x32_bf16 v[10:13], v[150:153], v[234:237], v[10:13]
	v_mfma_f32_16x16x32_bf16 v[14:17], v[154:157], v[234:237], v[14:17]
	s_waitcnt vmcnt(21)
	s_waitcnt lgkmcnt(0)
	s_barrier
	s_mov_b32 s47, s42
	s_mov_b32 s42, s43
	s_mov_b32 s43, s44
	s_mov_b32 s44, s47
	v_mul_f32_e32 v98, s12, v98
	v_mul_f32_e32 v99, s12, v99
	v_mul_f32_e32 v100, s13, v100
	v_mul_f32_e32 v101, s13, v101
	v_mul_f32_e32 v102, s14, v102
	v_mul_f32_e32 v103, s14, v103
	v_mul_f32_e32 v104, s15, v104
	v_mul_f32_e32 v105, s15, v105
	v_mul_f32_e32 v106, s16, v106
	v_mul_f32_e32 v107, s16, v107
	v_mul_f32_e32 v108, s17, v108
	v_mul_f32_e32 v109, s17, v109
	v_mul_f32_e32 v110, s18, v110
	v_mul_f32_e32 v111, s18, v111
	v_mul_f32_e32 v112, s19, v112
	v_mul_f32_e32 v113, s19, v113
	v_cvt_pk_bf16_f32 v158, v98, v100
	v_cvt_pk_bf16_f32 v159, v102, v104
	v_cvt_pk_bf16_f32 v160, v106, v108
	v_cvt_pk_bf16_f32 v161, v110, v112
	v_cvt_pk_bf16_f32 v162, v99, v101
	v_cvt_pk_bf16_f32 v163, v103, v105
	v_cvt_pk_bf16_f32 v164, v107, v109
	v_cvt_pk_bf16_f32 v165, v111, v113
	ds_write_b128 v1, v[158:161] offset:0
	ds_write_b128 v1, v[162:165] offset:128
	v_add_u32_e32 v91, s42, v135
	v_add_u32_e32 v93, s42, v137
	ds_read_b128 v[238:241], v139 offset:19456
	ds_read_b128 v[242:245], v139 offset:21504
	ds_read_b128 v[246:249], v139 offset:23552
	ds_read_b128 v[250:253], v139 offset:25600
	ds_read_b128 v[218:221], v91 offset:0
	ds_read_b128 v[222:225], v91 offset:2048
	ds_read_b128 v[226:229], v91 offset:4096
	ds_read_b128 v[230:233], v91 offset:6144
	ds_read_b128 v[234:237], v91 offset:8192
	s_add_i32 s47, s44, s6
	s_add_u32 s30, s30, 0x80
	s_addc_u32 s31, s31, 0
	s_waitcnt lgkmcnt(0)
	v_mfma_f32_16x16x32_bf16 v[78:81], v[238:241], v[218:221], v[78:81]
	v_mfma_f32_16x16x32_bf16 v[74:77], v[242:245], v[218:221], v[74:77]
	v_mfma_f32_16x16x32_bf16 v[70:73], v[246:249], v[218:221], v[70:73]
	v_mfma_f32_16x16x32_bf16 v[66:69], v[250:253], v[218:221], v[66:69]
	ds_read_b128 v[218:221], v93 offset:0
	ds_read_b128 v[142:145], v141 offset:19456
	s_mov_b32 m0, s47
	s_nop 0
	global_load_lds_dwordx4 v86, s[30:31]
	v_mfma_f32_16x16x32_bf16 v[62:65], v[238:241], v[222:225], v[62:65]
	v_mfma_f32_16x16x32_bf16 v[58:61], v[242:245], v[222:225], v[58:61]
	v_mfma_f32_16x16x32_bf16 v[54:57], v[246:249], v[222:225], v[54:57]
	v_mfma_f32_16x16x32_bf16 v[50:53], v[250:253], v[222:225], v[50:53]
	ds_read_b128 v[222:225], v93 offset:2048
	ds_read_b128 v[146:149], v141 offset:21504
	s_add_i32 m0, s47, 0x2000
	s_nop 0
	global_load_lds_dwordx4 v134, s[30:31]
	v_mfma_f32_16x16x32_bf16 v[46:49], v[238:241], v[226:229], v[46:49]
	v_mfma_f32_16x16x32_bf16 v[42:45], v[242:245], v[226:229], v[42:45]
	v_mfma_f32_16x16x32_bf16 v[38:41], v[246:249], v[226:229], v[38:41]
	v_mfma_f32_16x16x32_bf16 v[34:37], v[250:253], v[226:229], v[34:37]
	ds_read_b128 v[226:229], v93 offset:4096
	ds_read_b128 v[150:153], v141 offset:23552
	s_add_i32 m0, s47, 0x4000
	s_nop 0
	global_load_lds_dwordx4 v136, s[30:31]
	v_mfma_f32_16x16x32_bf16 v[18:21], v[238:241], v[230:233], v[18:21]
	v_mfma_f32_16x16x32_bf16 v[22:25], v[242:245], v[230:233], v[22:25]
	v_mfma_f32_16x16x32_bf16 v[26:29], v[246:249], v[230:233], v[26:29]
	v_mfma_f32_16x16x32_bf16 v[30:33], v[250:253], v[230:233], v[30:33]
	ds_read_b128 v[230:233], v93 offset:6144
	ds_read_b128 v[154:157], v141 offset:25600
	s_add_i32 m0, s47, 0x6000
	s_nop 0
	global_load_lds_dwordx4 v138, s[30:31]
	v_mfma_f32_16x16x32_bf16 v[2:5], v[238:241], v[234:237], v[2:5]
	v_mfma_f32_16x16x32_bf16 v[6:9], v[242:245], v[234:237], v[6:9]
	v_mfma_f32_16x16x32_bf16 v[10:13], v[246:249], v[234:237], v[10:13]
	v_mfma_f32_16x16x32_bf16 v[14:17], v[250:253], v[234:237], v[14:17]
	ds_read_b128 v[234:237], v93 offset:8192
	s_add_i32 m0, s47, 0x8000
	s_nop 0
	global_load_lds_dwordx4 v140, s[30:31]
	s_waitcnt lgkmcnt(0)
; #define MU_GLDS_A(buf, kt) do { _Pragma("unroll") for (int i = 0; i < NMU; ++i) \
;         __builtin_amdgcn_global_load_lds((const unsigned*)((const char*)A + aoff[i] + (size_t)(kt) * 128), (PG8_LAS unsigned*)(MU_SA(buf) + wid * 1024 + i * 8192), 16, 0, 0); } while (0)
; #define MU_B_ISSUE(sb, kt) do { const char* kb_ = Bb + (size_t)(kt) * (64 * (size_t)RB); _Pragma("unroll") for (int j = 0; j < 8; ++j) { const char* p_ = kb_ + (size_t)j * RB; \
;         asm volatile("global_load_dwordx2 %0, %1, off" : "=&v"(sb[j]) : "v"(p_) : "memory"); } } while (0)
; #define MU_B_WAIT(sb, N) asm volatile("s_waitcnt vmcnt(%8)" : "+v"(sb[0]), "+v"(sb[1]), "+v"(sb[2]), "+v"(sb[3]), "+v"(sb[4]), "+v"(sb[5]), "+v"(sb[6]), "+v"(sb[7]) : "n"(N) : "memory")
; #define MU_G_LOAD(ga, kt) do { const PG8_LAS f32x4* gk_ = (const PG8_LAS f32x4*)(lds + GAIN_OFF) + 16 * (kt) + 2 * wid; const f32x4 ga_ = gk_[0], gb_ = gk_[1]; \
;         ga[0] = ga_[0]; ga[1] = ga_[1]; ga[2] = ga_[2]; ga[3] = ga_[3]; ga[4] = gb_[0]; ga[5] = gb_[1]; ga[6] = gb_[2]; ga[7] = gb_[3]; } while (0)
; #define MU_COMPUTE(buf) MU_COMPUTE_N(buf, NMU)
; #define MU_END(last) do { if (last) asm volatile("s_waitcnt vmcnt(0)" ::: "memory"); else asm volatile("s_waitcnt vmcnt(8)" ::: "memory"); \
;         asm volatile("s_waitcnt lgkmcnt(0)" ::: "memory"); __builtin_amdgcn_s_barrier(); asm volatile("" ::: "memory"); } while (0)
; template <int MODE>
; __device__ __forceinline__ void moe_unit(PG8_LAS unsigned char* lds, int e, int cb, int slot0  , int nv  , const bf16_t* A, const int* slot_tok,
;                                          const float* W0, const float* W1, bf16_t* OUT, const float* slot_rs  , const int* slot_dst) {
;     ...
;         if (t + 2 < nt) MU_B_WAIT(s1, 8); else MU_B_WAIT(s1, 0);
;         MU_G_LOAD(g0, t + 1); MU_B_WRITE(s1, 1, g0); __builtin_amdgcn_sched_barrier(0); MU_GLDS_A(1, t + 1); __builtin_amdgcn_sched_barrier(0);
;         if (t + 3 < nt) { MU_B_ISSUE(s1, t + 3); }
;         MU_COMPUTE(0);
;         MU_END(t + 3 >= nt);
;         if (t + 2 < nt) { MU_B_WAIT(s0, 8); MU_G_LOAD(g0, t + 2); MU_B_WRITE(s0, 0, g0); __builtin_amdgcn_sched_barrier(0); MU_GLDS_A(0, t + 2); __builtin_amdgcn_sched_barrier(0); }
;         if (t + 4 < nt) { MU_B_ISSUE(s0, t + 4); }
;         MU_COMPUTE(1);
;         MU_END(t + 4 >= nt);
	s_load_dwordx8 s[20:27], s[28:29], 0x0
	s_add_u32 s28, s28, 0x100
	s_addc_u32 s29, s29, 0
	v_mfma_f32_16x16x32_bf16 v[78:81], v[142:145], v[218:221], v[78:81]
	v_mfma_f32_16x16x32_bf16 v[74:77], v[146:149], v[218:221], v[74:77]
	v_mfma_f32_16x16x32_bf16 v[70:73], v[150:153], v[218:221], v[70:73]
	v_mfma_f32_16x16x32_bf16 v[66:69], v[154:157], v[218:221], v[66:69]
	v_mfma_f32_16x16x32_bf16 v[62:65], v[142:145], v[222:225], v[62:65]
	v_mfma_f32_16x16x32_bf16 v[58:61], v[146:149], v[222:225], v[58:61]
	v_mfma_f32_16x16x32_bf16 v[54:57], v[150:153], v[222:225], v[54:57]
	v_mfma_f32_16x16x32_bf16 v[50:53], v[154:157], v[222:225], v[50:53]
	v_mfma_f32_16x16x32_bf16 v[46:49], v[142:145], v[226:229], v[46:49]
	v_mfma_f32_16x16x32_bf16 v[42:45], v[146:149], v[226:229], v[42:45]
	v_mfma_f32_16x16x32_bf16 v[38:41], v[150:153], v[226:229], v[38:41]
	v_mfma_f32_16x16x32_bf16 v[34:37], v[154:157], v[226:229], v[34:37]
	v_mfma_f32_16x16x32_bf16 v[18:21], v[142:145], v[230:233], v[18:21]
	v_mfma_f32_16x16x32_bf16 v[22:25], v[146:149], v[230:233], v[22:25]
	v_mfma_f32_16x16x32_bf16 v[26:29], v[150:153], v[230:233], v[26:29]
	v_mfma_f32_16x16x32_bf16 v[30:33], v[154:157], v[230:233], v[30:33]
	v_mfma_f32_16x16x32_bf16 v[2:5], v[142:145], v[234:237], v[2:5]
	v_mfma_f32_16x16x32_bf16 v[6:9], v[146:149], v[234:237], v[6:9]
	v_mfma_f32_16x16x32_bf16 v[10:13], v[150:153], v[234:237], v[10:13]
	v_mfma_f32_16x16x32_bf16 v[14:17], v[154:157], v[234:237], v[14:17]
	s_waitcnt vmcnt(13)
	s_waitcnt lgkmcnt(0)
	s_barrier
	s_mov_b32 s47, s42
	s_mov_b32 s42, s43
	s_mov_b32 s43, s44
	s_mov_b32 s44, s47
	v_mul_f32_e32 v114, s20, v114
	v_mul_f32_e32 v115, s20, v115
	v_mul_f32_e32 v116, s21, v116
	v_mul_f32_e32 v117, s21, v117
	v_mul_f32_e32 v118, s22, v118
	v_mul_f32_e32 v119, s22, v119
	v_mul_f32_e32 v120, s23, v120
	v_mul_f32_e32 v121, s23, v121
	v_mul_f32_e32 v122, s24, v122
	v_mul_f32_e32 v123, s24, v123
	v_mul_f32_e32 v124, s25, v124
	v_mul_f32_e32 v125, s25, v125
	v_mul_f32_e32 v126, s26, v126
	v_mul_f32_e32 v127, s26, v127
	v_mul_f32_e32 v128, s27, v128
	v_mul_f32_e32 v129, s27, v129
	v_cvt_pk_bf16_f32 v158, v114, v116
	v_cvt_pk_bf16_f32 v159, v118, v120
	v_cvt_pk_bf16_f32 v160, v122, v124
	v_cvt_pk_bf16_f32 v161, v126, v128
	v_cvt_pk_bf16_f32 v162, v115, v117
	v_cvt_pk_bf16_f32 v163, v119, v121
	v_cvt_pk_bf16_f32 v164, v123, v125
	v_cvt_pk_bf16_f32 v165, v127, v129
	ds_write_b128 v1, v[158:161] offset:19456
	ds_write_b128 v1, v[162:165] offset:19584
	v_add_u32_e32 v91, s42, v135
	v_add_u32_e32 v93, s42, v137
	ds_read_b128 v[238:241], v139 offset:0
	ds_read_b128 v[242:245], v139 offset:2048
	ds_read_b128 v[246:249], v139 offset:4096
	ds_read_b128 v[250:253], v139 offset:6144
	ds_read_b128 v[218:221], v91 offset:0
	ds_read_b128 v[222:225], v91 offset:2048
	ds_read_b128 v[226:229], v91 offset:4096
	ds_read_b128 v[230:233], v91 offset:6144
	ds_read_b128 v[234:237], v91 offset:8192
	s_add_i32 s47, s44, s6
	s_add_u32 s30, s30, 0x80
	s_addc_u32 s31, s31, 0
	s_waitcnt lgkmcnt(0)
	v_mfma_f32_16x16x32_bf16 v[78:81], v[238:241], v[218:221], v[78:81]
	v_mfma_f32_16x16x32_bf16 v[74:77], v[242:245], v[218:221], v[74:77]
	v_mfma_f32_16x16x32_bf16 v[70:73], v[246:249], v[218:221], v[70:73]
	v_mfma_f32_16x16x32_bf16 v[66:69], v[250:253], v[218:221], v[66:69]
	ds_read_b128 v[218:221], v93 offset:0
	ds_read_b128 v[142:145], v141 offset:0
	s_mov_b32 m0, s47
	s_nop 0
	global_load_lds_dwordx4 v86, s[30:31]
	v_mfma_f32_16x16x32_bf16 v[62:65], v[238:241], v[222:225], v[62:65]
	v_mfma_f32_16x16x32_bf16 v[58:61], v[242:245], v[222:225], v[58:61]
	v_mfma_f32_16x16x32_bf16 v[54:57], v[246:249], v[222:225], v[54:57]
	v_mfma_f32_16x16x32_bf16 v[50:53], v[250:253], v[222:225], v[50:53]
	ds_read_b128 v[222:225], v93 offset:2048
	ds_read_b128 v[146:149], v141 offset:2048
	s_add_i32 m0, s47, 0x2000
	s_nop 0
	global_load_lds_dwordx4 v134, s[30:31]
	v_mfma_f32_16x16x32_bf16 v[46:49], v[238:241], v[226:229], v[46:49]
	v_mfma_f32_16x16x32_bf16 v[42:45], v[242:245], v[226:229], v[42:45]
	v_mfma_f32_16x16x32_bf16 v[38:41], v[246:249], v[226:229], v[38:41]
	v_mfma_f32_16x16x32_bf16 v[34:37], v[250:253], v[226:229], v[34:37]
	ds_read_b128 v[226:229], v93 offset:4096
	ds_read_b128 v[150:153], v141 offset:4096
	s_add_i32 m0, s47, 0x4000
	s_nop 0
	global_load_lds_dwordx4 v136, s[30:31]
	v_mfma_f32_16x16x32_bf16 v[18:21], v[238:241], v[230:233], v[18:21]
	v_mfma_f32_16x16x32_bf16 v[22:25], v[242:245], v[230:233], v[22:25]
	v_mfma_f32_16x16x32_bf16 v[26:29], v[246:249], v[230:233], v[26:29]
	v_mfma_f32_16x16x32_bf16 v[30:33], v[250:253], v[230:233], v[30:33]
	ds_read_b128 v[230:233], v93 offset:6144
	ds_read_b128 v[154:157], v141 offset:6144
	s_add_i32 m0, s47, 0x6000
	s_nop 0
	global_load_lds_dwordx4 v138, s[30:31]
	v_mfma_f32_16x16x32_bf16 v[2:5], v[238:241], v[234:237], v[2:5]
	v_mfma_f32_16x16x32_bf16 v[6:9], v[242:245], v[234:237], v[6:9]
	v_mfma_f32_16x16x32_bf16 v[10:13], v[246:249], v[234:237], v[10:13]
	v_mfma_f32_16x16x32_bf16 v[14:17], v[250:253], v[234:237], v[14:17]
	ds_read_b128 v[234:237], v93 offset:8192
	s_add_i32 m0, s47, 0x8000
	s_nop 0
	global_load_lds_dwordx4 v140, s[30:31]
	s_waitcnt lgkmcnt(0)
	s_load_dwordx8 s[12:19], s[28:29], 0x0
	s_add_u32 s28, s28, 0x100
	s_addc_u32 s29, s29, 0
	v_mfma_f32_16x16x32_bf16 v[78:81], v[142:145], v[218:221], v[78:81]
	v_mfma_f32_16x16x32_bf16 v[74:77], v[146:149], v[218:221], v[74:77]
	v_mfma_f32_16x16x32_bf16 v[70:73], v[150:153], v[218:221], v[70:73]
	v_mfma_f32_16x16x32_bf16 v[66:69], v[154:157], v[218:221], v[66:69]
	v_mfma_f32_16x16x32_bf16 v[62:65], v[142:145], v[222:225], v[62:65]
	v_mfma_f32_16x16x32_bf16 v[58:61], v[146:149], v[222:225], v[58:61]
	v_mfma_f32_16x16x32_bf16 v[54:57], v[150:153], v[222:225], v[54:57]
	v_mfma_f32_16x16x32_bf16 v[50:53], v[154:157], v[222:225], v[50:53]
	v_mfma_f32_16x16x32_bf16 v[46:49], v[142:145], v[226:229], v[46:49]
	v_mfma_f32_16x16x32_bf16 v[42:45], v[146:149], v[226:229], v[42:45]
	v_mfma_f32_16x16x32_bf16 v[38:41], v[150:153], v[226:229], v[38:41]
	v_mfma_f32_16x16x32_bf16 v[34:37], v[154:157], v[226:229], v[34:37]
	v_mfma_f32_16x16x32_bf16 v[18:21], v[142:145], v[230:233], v[18:21]
	v_mfma_f32_16x16x32_bf16 v[22:25], v[146:149], v[230:233], v[22:25]
	v_mfma_f32_16x16x32_bf16 v[26:29], v[150:153], v[230:233], v[26:29]
	v_mfma_f32_16x16x32_bf16 v[30:33], v[154:157], v[230:233], v[30:33]
	v_mfma_f32_16x16x32_bf16 v[2:5], v[142:145], v[234:237], v[2:5]
	v_mfma_f32_16x16x32_bf16 v[6:9], v[146:149], v[234:237], v[6:9]
	v_mfma_f32_16x16x32_bf16 v[10:13], v[150:153], v[234:237], v[10:13]
	v_mfma_f32_16x16x32_bf16 v[14:17], v[154:157], v[234:237], v[14:17]
	s_waitcnt vmcnt(5)
	s_waitcnt lgkmcnt(0)
	s_barrier
; #define MU_GLDS_A(buf, kt) do { _Pragma("unroll") for (int i = 0; i < NMU; ++i) \
;         __builtin_amdgcn_global_load_lds((const unsigned*)((const char*)A + aoff[i] + (size_t)(kt) * 128), (PG8_LAS unsigned*)(MU_SA(buf) + wid * 1024 + i * 8192), 16, 0, 0); } while (0)
; #define MU_B_ISSUE(sb, kt) do { const char* kb_ = Bb + (size_t)(kt) * (64 * (size_t)RB); _Pragma("unroll") for (int j = 0; j < 8; ++j) { const char* p_ = kb_ + (size_t)j * RB; \
;         asm volatile("global_load_dwordx2 %0, %1, off" : "=&v"(sb[j]) : "v"(p_) : "memory"); } } while (0)
; #define MU_B_WAIT(sb, N) asm volatile("s_waitcnt vmcnt(%8)" : "+v"(sb[0]), "+v"(sb[1]), "+v"(sb[2]), "+v"(sb[3]), "+v"(sb[4]), "+v"(sb[5]), "+v"(sb[6]), "+v"(sb[7]) : "n"(N) : "memory")
; #define MU_G_LOAD(ga, kt) do { const PG8_LAS f32x4* gk_ = (const PG8_LAS f32x4*)(lds + GAIN_OFF) + 16 * (kt) + 2 * wid; const f32x4 ga_ = gk_[0], gb_ = gk_[1]; \
;         ga[0] = ga_[0]; ga[1] = ga_[1]; ga[2] = ga_[2]; ga[3] = ga_[3]; ga[4] = gb_[0]; ga[5] = gb_[1]; ga[6] = gb_[2]; ga[7] = gb_[3]; } while (0)
; #define MU_COMPUTE(buf) MU_COMPUTE_N(buf, NMU)
; #define MU_END(last) do { if (last) asm volatile("s_waitcnt vmcnt(0)" ::: "memory"); else asm volatile("s_waitcnt vmcnt(8)" ::: "memory"); \
;         asm volatile("s_waitcnt lgkmcnt(0)" ::: "memory"); __builtin_amdgcn_s_barrier(); asm volatile("" ::: "memory"); } while (0)
; template <int MODE>
; __device__ __forceinline__ void moe_unit(PG8_LAS unsigned char* lds, int e, int cb, int slot0  , int nv  , const bf16_t* A, const int* slot_tok,
;                                          const float* W0, const float* W1, bf16_t* OUT, const float* slot_rs  , const int* slot_dst) {
;     ...
;         if (t + 2 < nt) MU_B_WAIT(s1, 8); else MU_B_WAIT(s1, 0);
;         MU_G_LOAD(g0, t + 1); MU_B_WRITE(s1, 1, g0); __builtin_amdgcn_sched_barrier(0); MU_GLDS_A(1, t + 1); __builtin_amdgcn_sched_barrier(0);
;         if (t + 3 < nt) { MU_B_ISSUE(s1, t + 3); }
;         MU_COMPUTE(0);
;         MU_END(t + 3 >= nt);
;         if (t + 2 < nt) { MU_B_WAIT(s0, 8); MU_G_LOAD(g0, t + 2); MU_B_WRITE(s0, 0, g0); __builtin_amdgcn_sched_barrier(0); MU_GLDS_A(0, t + 2); __builtin_amdgcn_sched_barrier(0); }
;         if (t + 4 < nt) { MU_B_ISSUE(s0, t + 4); }
;         MU_COMPUTE(1);
;         MU_END(t + 4 >= nt);
	s_mov_b32 s47, s42
	s_mov_b32 s42, s43
	s_mov_b32 s43, s44
	s_mov_b32 s44, s47
	v_mul_f32_e32 v186, s12, v186
	v_mul_f32_e32 v187, s12, v187
	v_mul_f32_e32 v188, s13, v188
	v_mul_f32_e32 v189, s13, v189
	v_mul_f32_e32 v190, s14, v190
	v_mul_f32_e32 v191, s14, v191
	v_mul_f32_e32 v192, s15, v192
	v_mul_f32_e32 v193, s15, v193
	v_mul_f32_e32 v194, s16, v194
	v_mul_f32_e32 v195, s16, v195
	v_mul_f32_e32 v196, s17, v196
	v_mul_f32_e32 v197, s17, v197
	v_mul_f32_e32 v198, s18, v198
	v_mul_f32_e32 v199, s18, v199
	v_mul_f32_e32 v200, s19, v200
	v_mul_f32_e32 v201, s19, v201
	v_cvt_pk_bf16_f32 v158, v186, v188
	v_cvt_pk_bf16_f32 v159, v190, v192
	v_cvt_pk_bf16_f32 v160, v194, v196
	v_cvt_pk_bf16_f32 v161, v198, v200
	v_cvt_pk_bf16_f32 v162, v187, v189
	v_cvt_pk_bf16_f32 v163, v191, v193
	v_cvt_pk_bf16_f32 v164, v195, v197
	v_cvt_pk_bf16_f32 v165, v199, v201
	ds_write_b128 v1, v[158:161] offset:0
	ds_write_b128 v1, v[162:165] offset:128
	v_add_u32_e32 v91, s42, v135
	v_add_u32_e32 v93, s42, v137
	ds_read_b128 v[238:241], v139 offset:19456
	ds_read_b128 v[242:245], v139 offset:21504
	ds_read_b128 v[246:249], v139 offset:23552
	ds_read_b128 v[250:253], v139 offset:25600
	ds_read_b128 v[218:221], v91 offset:0
	ds_read_b128 v[222:225], v91 offset:2048
	ds_read_b128 v[226:229], v91 offset:4096
	ds_read_b128 v[230:233], v91 offset:6144
	ds_read_b128 v[234:237], v91 offset:8192
	s_add_i32 s47, s44, s6
	s_add_u32 s30, s30, 0x80
	s_addc_u32 s31, s31, 0
	s_waitcnt lgkmcnt(0)
	v_mfma_f32_16x16x32_bf16 v[78:81], v[238:241], v[218:221], v[78:81]
	v_mfma_f32_16x16x32_bf16 v[74:77], v[242:245], v[218:221], v[74:77]
	v_mfma_f32_16x16x32_bf16 v[70:73], v[246:249], v[218:221], v[70:73]
	v_mfma_f32_16x16x32_bf16 v[66:69], v[250:253], v[218:221], v[66:69]
	ds_read_b128 v[218:221], v93 offset:0
	ds_read_b128 v[142:145], v141 offset:19456
	s_mov_b32 m0, s47
	s_nop 0
	global_load_lds_dwordx4 v86, s[30:31]
	v_mfma_f32_16x16x32_bf16 v[62:65], v[238:241], v[222:225], v[62:65]
	v_mfma_f32_16x16x32_bf16 v[58:61], v[242:245], v[222:225], v[58:61]
	v_mfma_f32_16x16x32_bf16 v[54:57], v[246:249], v[222:225], v[54:57]
	v_mfma_f32_16x16x32_bf16 v[50:53], v[250:253], v[222:225], v[50:53]
	ds_read_b128 v[222:225], v93 offset:2048
	ds_read_b128 v[146:149], v141 offset:21504
	s_add_i32 m0, s47, 0x2000
	s_nop 0
	global_load_lds_dwordx4 v134, s[30:31]
	v_mfma_f32_16x16x32_bf16 v[46:49], v[238:241], v[226:229], v[46:49]
	v_mfma_f32_16x16x32_bf16 v[42:45], v[242:245], v[226:229], v[42:45]
	v_mfma_f32_16x16x32_bf16 v[38:41], v[246:249], v[226:229], v[38:41]
	v_mfma_f32_16x16x32_bf16 v[34:37], v[250:253], v[226:229], v[34:37]
	ds_read_b128 v[226:229], v93 offset:4096
	ds_read_b128 v[150:153], v141 offset:23552
	s_add_i32 m0, s47, 0x4000
	s_nop 0
	global_load_lds_dwordx4 v136, s[30:31]
	v_mfma_f32_16x16x32_bf16 v[18:21], v[238:241], v[230:233], v[18:21]
	v_mfma_f32_16x16x32_bf16 v[22:25], v[242:245], v[230:233], v[22:25]
	v_mfma_f32_16x16x32_bf16 v[26:29], v[246:249], v[230:233], v[26:29]
	v_mfma_f32_16x16x32_bf16 v[30:33], v[250:253], v[230:233], v[30:33]
	ds_read_b128 v[230:233], v93 offset:6144
	ds_read_b128 v[154:157], v141 offset:25600
	s_add_i32 m0, s47, 0x6000
	s_nop 0
	global_load_lds_dwordx4 v138, s[30:31]
	v_mfma_f32_16x16x32_bf16 v[2:5], v[238:241], v[234:237], v[2:5]
	v_mfma_f32_16x16x32_bf16 v[6:9], v[242:245], v[234:237], v[6:9]
	v_mfma_f32_16x16x32_bf16 v[10:13], v[246:249], v[234:237], v[10:13]
	v_mfma_f32_16x16x32_bf16 v[14:17], v[250:253], v[234:237], v[14:17]
	ds_read_b128 v[234:237], v93 offset:8192
	s_add_i32 m0, s47, 0x8000
	s_nop 0
	global_load_lds_dwordx4 v140, s[30:31]
	s_waitcnt lgkmcnt(0)
	s_load_dwordx8 s[20:27], s[28:29], 0x0
	s_add_u32 s28, s28, 0x100
	s_addc_u32 s29, s29, 0
	v_mfma_f32_16x16x32_bf16 v[78:81], v[142:145], v[218:221], v[78:81]
	v_mfma_f32_16x16x32_bf16 v[74:77], v[146:149], v[218:221], v[74:77]
	v_mfma_f32_16x16x32_bf16 v[70:73], v[150:153], v[218:221], v[70:73]
	v_mfma_f32_16x16x32_bf16 v[66:69], v[154:157], v[218:221], v[66:69]
	v_mfma_f32_16x16x32_bf16 v[62:65], v[142:145], v[222:225], v[62:65]
	v_mfma_f32_16x16x32_bf16 v[58:61], v[146:149], v[222:225], v[58:61]
	v_mfma_f32_16x16x32_bf16 v[54:57], v[150:153], v[222:225], v[54:57]
	v_mfma_f32_16x16x32_bf16 v[50:53], v[154:157], v[222:225], v[50:53]
	v_mfma_f32_16x16x32_bf16 v[46:49], v[142:145], v[226:229], v[46:49]
	v_mfma_f32_16x16x32_bf16 v[42:45], v[146:149], v[226:229], v[42:45]
	v_mfma_f32_16x16x32_bf16 v[38:41], v[150:153], v[226:229], v[38:41]
	v_mfma_f32_16x16x32_bf16 v[34:37], v[154:157], v[226:229], v[34:37]
	v_mfma_f32_16x16x32_bf16 v[18:21], v[142:145], v[230:233], v[18:21]
	v_mfma_f32_16x16x32_bf16 v[22:25], v[146:149], v[230:233], v[22:25]
	v_mfma_f32_16x16x32_bf16 v[26:29], v[150:153], v[230:233], v[26:29]
	v_mfma_f32_16x16x32_bf16 v[30:33], v[154:157], v[230:233], v[30:33]
	v_mfma_f32_16x16x32_bf16 v[2:5], v[142:145], v[234:237], v[2:5]
	v_mfma_f32_16x16x32_bf16 v[6:9], v[146:149], v[234:237], v[6:9]
	v_mfma_f32_16x16x32_bf16 v[10:13], v[150:153], v[234:237], v[10:13]
	v_mfma_f32_16x16x32_bf16 v[14:17], v[154:157], v[234:237], v[14:17]
	s_waitcnt vmcnt(5)
	s_waitcnt lgkmcnt(0)
	s_barrier
; #define MU_GLDS_A(buf, kt) do { _Pragma("unroll") for (int i = 0; i < NMU; ++i) \
;         __builtin_amdgcn_global_load_lds((const unsigned*)((const char*)A + aoff[i] + (size_t)(kt) * 128), (PG8_LAS unsigned*)(MU_SA(buf) + wid * 1024 + i * 8192), 16, 0, 0); } while (0)
; #define MU_B_ISSUE(sb, kt) do { const char* kb_ = Bb + (size_t)(kt) * (64 * (size_t)RB); _Pragma("unroll") for (int j = 0; j < 8; ++j) { const char* p_ = kb_ + (size_t)j * RB; \
;         asm volatile("global_load_dwordx2 %0, %1, off" : "=&v"(sb[j]) : "v"(p_) : "memory"); } } while (0)
; #define MU_B_WAIT(sb, N) asm volatile("s_waitcnt vmcnt(%8)" : "+v"(sb[0]), "+v"(sb[1]), "+v"(sb[2]), "+v"(sb[3]), "+v"(sb[4]), "+v"(sb[5]), "+v"(sb[6]), "+v"(sb[7]) : "n"(N) : "memory")
; #define MU_G_LOAD(ga, kt) do { const PG8_LAS f32x4* gk_ = (const PG8_LAS f32x4*)(lds + GAIN_OFF) + 16 * (kt) + 2 * wid; const f32x4 ga_ = gk_[0], gb_ = gk_[1]; \
;         ga[0] = ga_[0]; ga[1] = ga_[1]; ga[2] = ga_[2]; ga[3] = ga_[3]; ga[4] = gb_[0]; ga[5] = gb_[1]; ga[6] = gb_[2]; ga[7] = gb_[3]; } while (0)
; #define MU_COMPUTE(buf) MU_COMPUTE_N(buf, NMU)
; #define MU_END(last) do { if (last) asm volatile("s_waitcnt vmcnt(0)" ::: "memory"); else asm volatile("s_waitcnt vmcnt(8)" ::: "memory"); \
;         asm volatile("s_waitcnt lgkmcnt(0)" ::: "memory"); __builtin_amdgcn_s_barrier(); asm volatile("" ::: "memory"); } while (0)
; template <int MODE>
; __device__ __forceinline__ void moe_unit(PG8_LAS unsigned char* lds, int e, int cb, int slot0  , int nv  , const bf16_t* A, const int* slot_tok,
;                                          const float* W0, const float* W1, bf16_t* OUT, const float* slot_rs  , const int* slot_dst) {
;     ...
;         if (t + 2 < nt) MU_B_WAIT(s1, 8); else MU_B_WAIT(s1, 0);
;         MU_G_LOAD(g0, t + 1); MU_B_WRITE(s1, 1, g0); __builtin_amdgcn_sched_barrier(0); MU_GLDS_A(1, t + 1); __builtin_amdgcn_sched_barrier(0);
;         if (t + 3 < nt) { MU_B_ISSUE(s1, t + 3); }
;         MU_COMPUTE(0);
;         MU_END(t + 3 >= nt);
;         if (t + 2 < nt) { MU_B_WAIT(s0, 8); MU_G_LOAD(g0, t + 2); MU_B_WRITE(s0, 0, g0); __builtin_amdgcn_sched_barrier(0); MU_GLDS_A(0, t + 2); __builtin_amdgcn_sched_barrier(0); }
;         if (t + 4 < nt) { MU_B_ISSUE(s0, t + 4); }
;         MU_COMPUTE(1);
;         MU_END(t + 4 >= nt);
	s_mov_b32 s47, s42
	s_mov_b32 s42, s43
	s_mov_b32 s43, s44
	s_mov_b32 s44, s47
	v_mul_f32_e32 v202, s20, v202
	v_mul_f32_e32 v203, s20, v203
	v_mul_f32_e32 v204, s21, v204
	v_mul_f32_e32 v205, s21, v205
	v_mul_f32_e32 v206, s22, v206
	v_mul_f32_e32 v207, s22, v207
	v_mul_f32_e32 v208, s23, v208
	v_mul_f32_e32 v209, s23, v209
	v_mul_f32_e32 v210, s24, v210
	v_mul_f32_e32 v211, s24, v211
	v_mul_f32_e32 v212, s25, v212
	v_mul_f32_e32 v213, s25, v213
	v_mul_f32_e32 v214, s26, v214
	v_mul_f32_e32 v215, s26, v215
	v_mul_f32_e32 v216, s27, v216
	v_mul_f32_e32 v217, s27, v217
	v_cvt_pk_bf16_f32 v158, v202, v204
	v_cvt_pk_bf16_f32 v159, v206, v208
	v_cvt_pk_bf16_f32 v160, v210, v212
	v_cvt_pk_bf16_f32 v161, v214, v216
	v_cvt_pk_bf16_f32 v162, v203, v205
	v_cvt_pk_bf16_f32 v163, v207, v209
	v_cvt_pk_bf16_f32 v164, v211, v213
	v_cvt_pk_bf16_f32 v165, v215, v217
	ds_write_b128 v1, v[158:161] offset:19456
	ds_write_b128 v1, v[162:165] offset:19584
	v_add_u32_e32 v91, s42, v135
	v_add_u32_e32 v93, s42, v137
	ds_read_b128 v[238:241], v139 offset:0
	ds_read_b128 v[242:245], v139 offset:2048
	ds_read_b128 v[246:249], v139 offset:4096
	ds_read_b128 v[250:253], v139 offset:6144
	ds_read_b128 v[218:221], v91 offset:0
	ds_read_b128 v[222:225], v91 offset:2048
	ds_read_b128 v[226:229], v91 offset:4096
	ds_read_b128 v[230:233], v91 offset:6144
	ds_read_b128 v[234:237], v91 offset:8192
	s_waitcnt lgkmcnt(0)
	v_mfma_f32_16x16x32_bf16 v[78:81], v[238:241], v[218:221], v[78:81]
	v_mfma_f32_16x16x32_bf16 v[74:77], v[242:245], v[218:221], v[74:77]
	v_mfma_f32_16x16x32_bf16 v[70:73], v[246:249], v[218:221], v[70:73]
	v_mfma_f32_16x16x32_bf16 v[66:69], v[250:253], v[218:221], v[66:69]
	ds_read_b128 v[218:221], v93 offset:0
	ds_read_b128 v[142:145], v141 offset:0
	v_mfma_f32_16x16x32_bf16 v[62:65], v[238:241], v[222:225], v[62:65]
	v_mfma_f32_16x16x32_bf16 v[58:61], v[242:245], v[222:225], v[58:61]
	v_mfma_f32_16x16x32_bf16 v[54:57], v[246:249], v[222:225], v[54:57]
	v_mfma_f32_16x16x32_bf16 v[50:53], v[250:253], v[222:225], v[50:53]
	ds_read_b128 v[222:225], v93 offset:2048
	ds_read_b128 v[146:149], v141 offset:2048
	v_mfma_f32_16x16x32_bf16 v[46:49], v[238:241], v[226:229], v[46:49]
	v_mfma_f32_16x16x32_bf16 v[42:45], v[242:245], v[226:229], v[42:45]
	v_mfma_f32_16x16x32_bf16 v[38:41], v[246:249], v[226:229], v[38:41]
	v_mfma_f32_16x16x32_bf16 v[34:37], v[250:253], v[226:229], v[34:37]
	ds_read_b128 v[226:229], v93 offset:4096
	ds_read_b128 v[150:153], v141 offset:4096
	v_mfma_f32_16x16x32_bf16 v[18:21], v[238:241], v[230:233], v[18:21]
	v_mfma_f32_16x16x32_bf16 v[22:25], v[242:245], v[230:233], v[22:25]
	v_mfma_f32_16x16x32_bf16 v[26:29], v[246:249], v[230:233], v[26:29]
	v_mfma_f32_16x16x32_bf16 v[30:33], v[250:253], v[230:233], v[30:33]
	ds_read_b128 v[230:233], v93 offset:6144
	ds_read_b128 v[154:157], v141 offset:6144
	v_mfma_f32_16x16x32_bf16 v[2:5], v[238:241], v[234:237], v[2:5]
	v_mfma_f32_16x16x32_bf16 v[6:9], v[242:245], v[234:237], v[6:9]
	v_mfma_f32_16x16x32_bf16 v[10:13], v[246:249], v[234:237], v[10:13]
	v_mfma_f32_16x16x32_bf16 v[14:17], v[250:253], v[234:237], v[14:17]
	ds_read_b128 v[234:237], v93 offset:8192
	s_waitcnt lgkmcnt(0)
	v_mfma_f32_16x16x32_bf16 v[78:81], v[142:145], v[218:221], v[78:81]
	v_mfma_f32_16x16x32_bf16 v[74:77], v[146:149], v[218:221], v[74:77]
	v_mfma_f32_16x16x32_bf16 v[70:73], v[150:153], v[218:221], v[70:73]
	v_mfma_f32_16x16x32_bf16 v[66:69], v[154:157], v[218:221], v[66:69]
	v_mfma_f32_16x16x32_bf16 v[62:65], v[142:145], v[222:225], v[62:65]
	v_mfma_f32_16x16x32_bf16 v[58:61], v[146:149], v[222:225], v[58:61]
	v_mfma_f32_16x16x32_bf16 v[54:57], v[150:153], v[222:225], v[54:57]
	v_mfma_f32_16x16x32_bf16 v[50:53], v[154:157], v[222:225], v[50:53]
	v_mfma_f32_16x16x32_bf16 v[46:49], v[142:145], v[226:229], v[46:49]
	v_mfma_f32_16x16x32_bf16 v[42:45], v[146:149], v[226:229], v[42:45]
	v_mfma_f32_16x16x32_bf16 v[38:41], v[150:153], v[226:229], v[38:41]
	v_mfma_f32_16x16x32_bf16 v[34:37], v[154:157], v[226:229], v[34:37]
	v_mfma_f32_16x16x32_bf16 v[18:21], v[142:145], v[230:233], v[18:21]
	v_mfma_f32_16x16x32_bf16 v[22:25], v[146:149], v[230:233], v[22:25]
	v_mfma_f32_16x16x32_bf16 v[26:29], v[150:153], v[230:233], v[26:29]
	v_mfma_f32_16x16x32_bf16 v[30:33], v[154:157], v[230:233], v[30:33]
	v_mfma_f32_16x16x32_bf16 v[2:5], v[142:145], v[234:237], v[2:5]
	v_mfma_f32_16x16x32_bf16 v[6:9], v[146:149], v[234:237], v[6:9]
	v_mfma_f32_16x16x32_bf16 v[10:13], v[150:153], v[234:237], v[10:13]
	v_mfma_f32_16x16x32_bf16 v[14:17], v[154:157], v[234:237], v[14:17]
	s_waitcnt vmcnt(0)
	s_waitcnt lgkmcnt(0)
	s_barrier
; #define MU_GLDS_A(buf, kt) do { _Pragma("unroll") for (int i = 0; i < NMU; ++i) \
;         __builtin_amdgcn_global_load_lds((const unsigned*)((const char*)A + aoff[i] + (size_t)(kt) * 128), (PG8_LAS unsigned*)(MU_SA(buf) + wid * 1024 + i * 8192), 16, 0, 0); } while (0)
; #define MU_B_ISSUE(sb, kt) do { const char* kb_ = Bb + (size_t)(kt) * (64 * (size_t)RB); _Pragma("unroll") for (int j = 0; j < 8; ++j) { const char* p_ = kb_ + (size_t)j * RB; \
;         asm volatile("global_load_dwordx2 %0, %1, off" : "=&v"(sb[j]) : "v"(p_) : "memory"); } } while (0)
; #define MU_B_WAIT(sb, N) asm volatile("s_waitcnt vmcnt(%8)" : "+v"(sb[0]), "+v"(sb[1]), "+v"(sb[2]), "+v"(sb[3]), "+v"(sb[4]), "+v"(sb[5]), "+v"(sb[6]), "+v"(sb[7]) : "n"(N) : "memory")
; #define MU_G_LOAD(ga, kt) do { const PG8_LAS f32x4* gk_ = (const PG8_LAS f32x4*)(lds + GAIN_OFF) + 16 * (kt) + 2 * wid; const f32x4 ga_ = gk_[0], gb_ = gk_[1]; \
;         ga[0] = ga_[0]; ga[1] = ga_[1]; ga[2] = ga_[2]; ga[3] = ga_[3]; ga[4] = gb_[0]; ga[5] = gb_[1]; ga[6] = gb_[2]; ga[7] = gb_[3]; } while (0)
; #define MU_COMPUTE(buf) MU_COMPUTE_N(buf, NMU)
; #define MU_END(last) do { if (last) asm volatile("s_waitcnt vmcnt(0)" ::: "memory"); else asm volatile("s_waitcnt vmcnt(8)" ::: "memory"); \
;         asm volatile("s_waitcnt lgkmcnt(0)" ::: "memory"); __builtin_amdgcn_s_barrier(); asm volatile("" ::: "memory"); } while (0)
; template <int MODE>
; __device__ __forceinline__ void moe_unit(PG8_LAS unsigned char* lds, int e, int cb, int slot0  , int nv  , const bf16_t* A, const int* slot_tok,
;                                          const float* W0, const float* W1, bf16_t* OUT, const float* slot_rs  , const int* slot_dst) {
;     ...
;         if (t + 2 < nt) MU_B_WAIT(s1, 8); else MU_B_WAIT(s1, 0);
;         MU_G_LOAD(g0, t + 1); MU_B_WRITE(s1, 1, g0); __builtin_amdgcn_sched_barrier(0); MU_GLDS_A(1, t + 1); __builtin_amdgcn_sched_barrier(0);
;         if (t + 3 < nt) { MU_B_ISSUE(s1, t + 3); }
;         MU_COMPUTE(0);
;         MU_END(t + 3 >= nt);
;         if (t + 2 < nt) { MU_B_WAIT(s0, 8); MU_G_LOAD(g0, t + 2); MU_B_WRITE(s0, 0, g0); __builtin_amdgcn_sched_barrier(0); MU_GLDS_A(0, t + 2); __builtin_amdgcn_sched_barrier(0); }
;         if (t + 4 < nt) { MU_B_ISSUE(s0, t + 4); }
;         MU_COMPUTE(1);
;         MU_END(t + 4 >= nt);
	s_mov_b32 s47, s42
	s_mov_b32 s42, s43
	s_mov_b32 s43, s44
	s_mov_b32 s44, s47
	v_add_u32_e32 v91, s42, v135
	v_add_u32_e32 v93, s42, v137
	ds_read_b128 v[238:241], v139 offset:19456
	ds_read_b128 v[242:245], v139 offset:21504
	ds_read_b128 v[246:249], v139 offset:23552
	ds_read_b128 v[250:253], v139 offset:25600
	ds_read_b128 v[218:221], v91 offset:0
	ds_read_b128 v[222:225], v91 offset:2048
	ds_read_b128 v[226:229], v91 offset:4096
	ds_read_b128 v[230:233], v91 offset:6144
	ds_read_b128 v[234:237], v91 offset:8192
	s_waitcnt lgkmcnt(0)
	v_mfma_f32_16x16x32_bf16 v[78:81], v[238:241], v[218:221], v[78:81]
	v_mfma_f32_16x16x32_bf16 v[74:77], v[242:245], v[218:221], v[74:77]
	v_mfma_f32_16x16x32_bf16 v[70:73], v[246:249], v[218:221], v[70:73]
	v_mfma_f32_16x16x32_bf16 v[66:69], v[250:253], v[218:221], v[66:69]
	ds_read_b128 v[218:221], v93 offset:0
	ds_read_b128 v[142:145], v141 offset:19456
	v_mfma_f32_16x16x32_bf16 v[62:65], v[238:241], v[222:225], v[62:65]
	v_mfma_f32_16x16x32_bf16 v[58:61], v[242:245], v[222:225], v[58:61]
	v_mfma_f32_16x16x32_bf16 v[54:57], v[246:249], v[222:225], v[54:57]
	v_mfma_f32_16x16x32_bf16 v[50:53], v[250:253], v[222:225], v[50:53]
	ds_read_b128 v[222:225], v93 offset:2048
	ds_read_b128 v[146:149], v141 offset:21504
	v_mfma_f32_16x16x32_bf16 v[46:49], v[238:241], v[226:229], v[46:49]
	v_mfma_f32_16x16x32_bf16 v[42:45], v[242:245], v[226:229], v[42:45]
	v_mfma_f32_16x16x32_bf16 v[38:41], v[246:249], v[226:229], v[38:41]
	v_mfma_f32_16x16x32_bf16 v[34:37], v[250:253], v[226:229], v[34:37]
	ds_read_b128 v[226:229], v93 offset:4096
	ds_read_b128 v[150:153], v141 offset:23552
	v_mfma_f32_16x16x32_bf16 v[18:21], v[238:241], v[230:233], v[18:21]
	v_mfma_f32_16x16x32_bf16 v[22:25], v[242:245], v[230:233], v[22:25]
	v_mfma_f32_16x16x32_bf16 v[26:29], v[246:249], v[230:233], v[26:29]
	v_mfma_f32_16x16x32_bf16 v[30:33], v[250:253], v[230:233], v[30:33]
	ds_read_b128 v[230:233], v93 offset:6144
	ds_read_b128 v[154:157], v141 offset:25600
	v_mfma_f32_16x16x32_bf16 v[2:5], v[238:241], v[234:237], v[2:5]
	v_mfma_f32_16x16x32_bf16 v[6:9], v[242:245], v[234:237], v[6:9]
	v_mfma_f32_16x16x32_bf16 v[10:13], v[246:249], v[234:237], v[10:13]
	v_mfma_f32_16x16x32_bf16 v[14:17], v[250:253], v[234:237], v[14:17]
	ds_read_b128 v[234:237], v93 offset:8192
	s_waitcnt lgkmcnt(0)
	v_mfma_f32_16x16x32_bf16 v[78:81], v[142:145], v[218:221], v[78:81]
	v_mfma_f32_16x16x32_bf16 v[74:77], v[146:149], v[218:221], v[74:77]
	v_mfma_f32_16x16x32_bf16 v[70:73], v[150:153], v[218:221], v[70:73]
	v_mfma_f32_16x16x32_bf16 v[66:69], v[154:157], v[218:221], v[66:69]
	v_mfma_f32_16x16x32_bf16 v[62:65], v[142:145], v[222:225], v[62:65]
	v_mfma_f32_16x16x32_bf16 v[58:61], v[146:149], v[222:225], v[58:61]
	v_mfma_f32_16x16x32_bf16 v[54:57], v[150:153], v[222:225], v[54:57]
	v_mfma_f32_16x16x32_bf16 v[50:53], v[154:157], v[222:225], v[50:53]
	v_mfma_f32_16x16x32_bf16 v[46:49], v[142:145], v[226:229], v[46:49]
	v_mfma_f32_16x16x32_bf16 v[42:45], v[146:149], v[226:229], v[42:45]
	v_mfma_f32_16x16x32_bf16 v[38:41], v[150:153], v[226:229], v[38:41]
	v_mfma_f32_16x16x32_bf16 v[34:37], v[154:157], v[226:229], v[34:37]
	v_mfma_f32_16x16x32_bf16 v[18:21], v[142:145], v[230:233], v[18:21]
	v_mfma_f32_16x16x32_bf16 v[22:25], v[146:149], v[230:233], v[22:25]
	v_mfma_f32_16x16x32_bf16 v[26:29], v[150:153], v[230:233], v[26:29]
	v_mfma_f32_16x16x32_bf16 v[30:33], v[154:157], v[230:233], v[30:33]
	v_mfma_f32_16x16x32_bf16 v[2:5], v[142:145], v[234:237], v[2:5]
	v_mfma_f32_16x16x32_bf16 v[6:9], v[146:149], v[234:237], v[6:9]
	v_mfma_f32_16x16x32_bf16 v[10:13], v[150:153], v[234:237], v[10:13]
	v_mfma_f32_16x16x32_bf16 v[14:17], v[154:157], v[234:237], v[14:17]
	s_waitcnt lgkmcnt(0)
	s_barrier
	s_mov_b32 s47, s42
	s_mov_b32 s42, s43
	s_mov_b32 s43, s44
	s_mov_b32 s44, s47


; __global__ void __launch_bounds__(NTHREADS, 2) hymba_fwd(Args args) {
;     extern __shared__ __attribute__((aligned(16))) unsigned char lds[];
	.amdhsa_kernel _Z9hymba_fwd4Args
		.amdhsa_group_segment_fixed_size 16960
		.amdhsa_private_segment_fixed_size 0
		.amdhsa_kernarg_size 424
		.amdhsa_user_sgpr_count 2
		.amdhsa_user_sgpr_dispatch_ptr 0
		.amdhsa_user_sgpr_queue_ptr 0
		.amdhsa_user_sgpr_kernarg_segment_ptr 1
		.amdhsa_user_sgpr_dispatch_id 0
		.amdhsa_user_sgpr_kernarg_preload_length 0
		.amdhsa_user_sgpr_kernarg_preload_offset 0
		.amdhsa_user_sgpr_private_segment_size 0
		.amdhsa_uses_dynamic_stack 0
		.amdhsa_enable_private_segment 0
		.amdhsa_system_sgpr_workgroup_id_x 1
		.amdhsa_system_sgpr_workgroup_id_y 0
		.amdhsa_system_sgpr_workgroup_id_z 0
		.amdhsa_system_sgpr_workgroup_info 0
		.amdhsa_system_vgpr_workitem_id 0
		.amdhsa_next_free_vgpr 255
		.amdhsa_next_free_sgpr 98
		.amdhsa_accum_offset 256
		.amdhsa_reserve_vcc 1
		.amdhsa_float_round_mode_32 0
		.amdhsa_float_round_mode_16_64 0
		.amdhsa_float_denorm_mode_32 3
		.amdhsa_float_denorm_mode_16_64 3
		.amdhsa_dx10_clamp 1
		.amdhsa_ieee_mode 1
		.amdhsa_fp16_overflow 0
		.amdhsa_tg_split 0
		.amdhsa_exception_fp_ieee_invalid_op 0
		.amdhsa_exception_fp_denorm_src 0
		.amdhsa_exception_fp_ieee_div_zero 0
		.amdhsa_exception_fp_ieee_overflow 0
		.amdhsa_exception_fp_ieee_underflow 0
		.amdhsa_exception_fp_ieee_inexact 0
		.amdhsa_exception_int_div_zero 0
	.end_amdhsa_kernel

; __global__ void __launch_bounds__(NTHREADS, 2) hymba_fwd(Args args) {
;     extern __shared__ __attribute__((aligned(16))) unsigned char lds[];
amdhsa.kernels:
  - .agpr_count:     0
    .args:
      - .offset:         0
        .size:           168
        .value_kind:     by_value
      - .offset:         168
        .size:           4
        .value_kind:     hidden_block_count_x
      - .offset:         172
        .size:           4
        .value_kind:     hidden_block_count_y
      - .offset:         176
        .size:           4
        .value_kind:     hidden_block_count_z
      - .offset:         180
        .size:           2
        .value_kind:     hidden_group_size_x
      - .offset:         182
        .size:           2
        .value_kind:     hidden_group_size_y
      - .offset:         184
        .size:           2
        .value_kind:     hidden_group_size_z
      - .offset:         186
        .size:           2
        .value_kind:     hidden_remainder_x
      - .offset:         188
        .size:           2
        .value_kind:     hidden_remainder_y
      - .offset:         190
        .size:           2
        .value_kind:     hidden_remainder_z
      - .offset:         208
        .size:           8
        .value_kind:     hidden_global_offset_x
      - .offset:         216
        .size:           8
        .value_kind:     hidden_global_offset_y
      - .offset:         224
        .size:           8
        .value_kind:     hidden_global_offset_z
      - .offset:         232
        .size:           2
        .value_kind:     hidden_grid_dims
      - .offset:         288
        .size:           4
        .value_kind:     hidden_dynamic_lds_size
    .group_segment_fixed_size: 16960
    .kernarg_segment_align: 8
    .kernarg_segment_size: 424
    .language:       OpenCL C
    .language_version:
      - 2
      - 0
    .max_flat_workgroup_size: 512
    .name:           _Z9hymba_fwd4Args
    .private_segment_fixed_size: 0
    .sgpr_count:     104
    .sgpr_spill_count: 62
    .symbol:         _Z9hymba_fwd4Args.kd
    .uniform_work_group_size: 1
    .uses_dynamic_stack: false
    .vgpr_count:     255
    .vgpr_spill_count: 0
    .wavefront_size: 64
